# v3 + P12: rmsnorm gain kept in registers; vmcnt waits of the token loop re-derived (counted waits leave the next token's prefetch in flight)
# speedup vs baseline: 1.0153x; 1.0005x over previous
.LBB0_1426:
	s_or_b64 exec, exec, s[2:3]
	v_readlane_b32 s2, v252, 14
	s_cmpk_gt_i32 s2, 0x7ff
	s_waitcnt vmcnt(0) lgkmcnt(0)
	s_barrier
	s_cbranch_scc1 .LBB0_1431
	v_mbcnt_lo_u32_b32 v1, -1, 0
	v_mbcnt_hi_u32_b32 v6, -1, v1
	v_and_b32_e32 v7, 64, v6
	v_add_u32_e32 v8, 64, v7
	v_xor_b32_e32 v1, 1, v6
	v_cmp_lt_i32_e32 vcc, v1, v8
	v_xor_b32_e32 v9, 2, v6
	s_add_u32 s12, s82, 0x74200000
	v_cndmask_b32_e32 v1, v6, v1, vcc
	v_cmp_lt_i32_e32 vcc, v9, v8
	s_addc_u32 s13, s83, 0
	s_add_u32 s14, s82, 0x74400000
	v_cndmask_b32_e32 v9, v6, v9, vcc
	v_lshlrev_b32_e32 v90, 2, v9
	v_xor_b32_e32 v9, 4, v6
	v_cmp_lt_i32_e32 vcc, v9, v8
	s_addc_u32 s15, s83, 0
	v_lshlrev_b32_e32 v14, 4, v198
	v_cndmask_b32_e32 v9, v6, v9, vcc
	v_lshlrev_b32_e32 v91, 2, v9
	v_xor_b32_e32 v9, 8, v6
	v_cmp_lt_i32_e32 vcc, v9, v8
	v_mov_b32_e32 v15, 0
	s_add_u32 s16, s82, 0x74300000
	v_cndmask_b32_e32 v9, v6, v9, vcc
	v_lshlrev_b32_e32 v92, 2, v9
	v_xor_b32_e32 v9, 16, v6
	v_cmp_lt_i32_e32 vcc, v9, v8
	v_lshl_add_u64 v[2:3], s[0:1], 0, v[14:15]
	v_readlane_b32 s0, v252, 14
	v_cndmask_b32_e32 v9, v6, v9, vcc
	v_lshlrev_b32_e32 v14, 2, v198
	v_lshlrev_b32_e32 v93, 2, v9
	v_xor_b32_e32 v9, 32, v6
	s_addc_u32 s17, s83, 0
	s_lshl_b32 s18, s0, 3
	v_lshl_add_u64 v[4:5], s[82:83], 0, v[14:15]
	s_mov_b64 s[0:1], 0xc6800000
	v_cmp_lt_i32_e32 vcc, v9, v8
	v_lshl_add_u64 v[4:5], v[4:5], 0, s[0:1]
	s_mov_b64 s[0:1], 0x1000
	v_cndmask_b32_e32 v6, v6, v9, vcc
	v_lshlrev_b32_e32 v94, 2, v6
	v_lshlrev_b32_e32 v95, 2, v7
	v_lshl_add_u64 v[6:7], v[2:3], 0, s[0:1]
	s_mov_b64 s[0:1], 0x1400
	v_lshl_add_u64 v[8:9], v[2:3], 0, s[0:1]
	s_mov_b64 s[0:1], 0x1800
	v_lshl_add_u64 v[10:11], v[2:3], 0, s[0:1]
	s_mov_b64 s[0:1], 0x1c00
	s_ashr_i32 s19, s18, 31
	v_lshl_add_u64 v[12:13], v[2:3], 0, s[0:1]
	global_load_dwordx4 v[212:215], v[2:3], off
	global_load_dwordx4 v[216:219], v[2:3], off offset:1024
	global_load_dwordx4 v[220:223], v[2:3], off offset:2048
	global_load_dwordx4 v[224:227], v[2:3], off offset:3072
	global_load_dwordx4 v[228:231], v[6:7], off
	global_load_dwordx4 v[232:235], v[8:9], off
	global_load_dwordx4 v[236:239], v[10:11], off
	global_load_dwordx4 v[240:243], v[12:13], off
	s_waitcnt vmcnt(0)
	s_lshl_b64 s[0:1], s[18:19], 11
	v_or_b32_e32 v14, s0, v14
	v_mov_b32_e32 v15, s1
	s_lshl_b64 s[0:1], s[18:19], 12
	v_mov_b32_e32 v17, s1
	v_readlane_b32 s1, v252, 13
	s_lshl_b32 s20, s80, 6
	v_lshl_or_b32 v16, v198, 3, s0
	s_lshl_b32 s0, s90, 8
	s_lshl_b32 s1, s1, 5
	s_ashr_i32 s21, s20, 31
	s_add_i32 s0, s0, s1
	v_cmp_gt_u32_e64 s[6:7], 32, v198
	v_lshlrev_b32_e32 v1, 2, v1
	v_or_b32_e32 v96, 0x70, v95
	v_or_b32_e32 v97, 4, v95
	v_or_b32_e32 v98, 8, v95
	v_or_b32_e32 v99, 12, v95
	v_or_b32_e32 v100, 16, v95
	v_or_b32_e32 v101, 20, v95
	v_or_b32_e32 v102, 24, v95
	v_or_b32_e32 v103, 28, v95
	v_or_b32_e32 v104, 32, v95
	v_or_b32_e32 v105, 36, v95
	v_or_b32_e32 v106, 40, v95
	v_or_b32_e32 v107, 44, v95
	v_or_b32_e32 v108, 48, v95
	v_or_b32_e32 v109, 52, v95
	v_or_b32_e32 v110, 56, v95
	v_or_b32_e32 v111, 60, v95
	v_or_b32_e32 v112, 64, v95
	v_or_b32_e32 v113, 0x44, v95
	v_or_b32_e32 v114, 0x48, v95
	v_or_b32_e32 v115, 0x4c, v95
	v_or_b32_e32 v116, 0x50, v95
	v_or_b32_e32 v117, 0x54, v95
	v_or_b32_e32 v118, 0x58, v95
	v_or_b32_e32 v119, 0x5c, v95
	v_or_b32_e32 v120, 0x60, v95
	v_or_b32_e32 v121, 0x64, v95
	v_or_b32_e32 v122, 0x68, v95
	v_or_b32_e32 v123, 0x6c, v95
	v_or_b32_e32 v124, 0x74, v95
	v_or_b32_e32 v125, 0x78, v95
	v_or_b32_e32 v126, 0x7c, v95
	s_lshl_b64 s[22:23], s[20:21], 11
	s_lshl_b64 s[24:25], s[20:21], 12
	v_add_u32_e32 v18, s0, v198
	s_lshl_b32 s2, s80, 8
	s_mov_b32 s3, 0x68201000
	s_movk_i32 s4, 0x7fff
	s_mov_b32 s5, 0x60200000
	v_mov_b32_e32 v127, 0x358637bd
	s_mov_b32 s19, 0xf800000
	v_mov_b32_e32 v128, 0x260
	s_mov_b32 s21, 0x38a00000
	s_mov_b32 s26, 0x68202000
	s_mov_b32 s27, 0x60201000
	s_mov_b32 s28, 0x68203000
	s_mov_b32 s29, 0x60202000
	s_mov_b32 s30, 0x38a01000
	s_mov_b32 s31, 0x68204000
	s_mov_b32 s33, 0x60203000
	s_mov_b32 s34, 0x68205000
	s_mov_b32 s35, 0x60204000
	s_mov_b32 s36, 0x38a02000
	s_mov_b32 s37, 0x68206000
	s_mov_b32 s38, 0x60205000
	s_mov_b32 s39, 0x68207000
	s_mov_b32 s40, 0x60206000
	s_mov_b32 s41, 0x38a03000
	s_mov_b32 s42, 0x60207000
	v_mov_b32_e32 v129, 1
	s_branch .LBB0_1429
.LBB0_1428:
	s_or_b64 exec, exec, s[0:1]
	ds_bpermute_b32 v26, v95, v130
	ds_bpermute_b32 v30, v97, v130
	v_lshl_add_u64 v[20:21], s[82:83], 0, v[16:17]
	v_add_co_u32_e32 v22, vcc, 0x68200000, v20
	s_waitcnt lgkmcnt(1)
	v_ashrrev_i32_e32 v27, 31, v26
	v_lshlrev_b64 v[26:27], 11, v[26:27]
	v_addc_co_u32_e32 v23, vcc, 0, v21, vcc
	v_lshl_add_u64 v[26:27], v[4:5], 0, v[26:27]
	s_waitcnt lgkmcnt(0)
	v_ashrrev_i32_e32 v31, 31, v30
	global_load_dwordx2 v[24:25], v[22:23], off
	global_load_dwordx2 v[40:41], v[22:23], off offset:512
	global_load_dwordx2 v[54:55], v[22:23], off offset:1024
	global_load_dwordx2 v[64:65], v[22:23], off offset:1536
	global_load_dwordx2 v[68:69], v[22:23], off offset:2048
	global_load_dwordx2 v[48:49], v[22:23], off offset:2560
	global_load_dwordx2 v[28:29], v[22:23], off offset:3072
	s_nop 0
	global_load_dwordx2 v[22:23], v[22:23], off offset:3584
	s_nop 0
	global_load_dword v62, v[26:27], off
	global_load_dword v139, v[26:27], off offset:256
	global_load_dword v141, v[26:27], off offset:512
	global_load_dword v142, v[26:27], off offset:768
	global_load_dword v144, v[26:27], off offset:1024
	global_load_dword v78, v[26:27], off offset:1280
	global_load_dword v80, v[26:27], off offset:1536
	global_load_dword v131, v[26:27], off offset:1792
	v_lshlrev_b64 v[26:27], 11, v[30:31]
	ds_bpermute_b32 v30, v98, v130
	v_lshl_add_u64 v[26:27], v[4:5], 0, v[26:27]
	global_load_dword v63, v[26:27], off
	global_load_dword v149, v[26:27], off offset:256
	global_load_dword v152, v[26:27], off offset:512
	global_load_dword v168, v[26:27], off offset:768
	global_load_dword v170, v[26:27], off offset:1024
	global_load_dword v79, v[26:27], off offset:1280
	global_load_dword v81, v[26:27], off offset:1536
	global_load_dword v133, v[26:27], off offset:1792
	ds_bpermute_b32 v34, v101, v130
	ds_bpermute_b32 v44, v102, v130
	s_waitcnt lgkmcnt(2)
	v_ashrrev_i32_e32 v31, 31, v30
	v_lshlrev_b64 v[26:27], 11, v[30:31]
	ds_bpermute_b32 v30, v99, v130
	v_lshl_add_u64 v[26:27], v[4:5], 0, v[26:27]
	global_load_dword v70, v[26:27], off
	global_load_dword v158, v[26:27], off offset:256
	global_load_dword v176, v[26:27], off offset:512
	global_load_dword v178, v[26:27], off offset:768
	global_load_dword v184, v[26:27], off offset:1024
	global_load_dword v186, v[26:27], off offset:1280
	global_load_dword v84, v[26:27], off offset:1536
	global_load_dword v134, v[26:27], off offset:1792
	s_waitcnt lgkmcnt(2)
	v_ashrrev_i32_e32 v35, 31, v34
	v_lshlrev_b64 v[34:35], 11, v[34:35]
	s_waitcnt lgkmcnt(0)
	v_ashrrev_i32_e32 v31, 31, v30
	v_lshlrev_b64 v[26:27], 11, v[30:31]
	ds_bpermute_b32 v30, v100, v130
	v_lshl_add_u64 v[26:27], v[4:5], 0, v[26:27]
	global_load_dword v74, v[26:27], off
	global_load_dword v159, v[26:27], off offset:256
	global_load_dword v182, v[26:27], off offset:512
	global_load_dword v189, v[26:27], off offset:768
	global_load_dword v196, v[26:27], off offset:1024
	global_load_dword v199, v[26:27], off offset:1280
	global_load_dword v85, v[26:27], off offset:1536
	global_load_dword v136, v[26:27], off offset:1792
	v_add_co_u32_e32 v26, vcc, s3, v20
	s_waitcnt lgkmcnt(0)
	v_ashrrev_i32_e32 v31, 31, v30
	v_lshlrev_b64 v[30:31], 11, v[30:31]
	v_addc_co_u32_e32 v27, vcc, 0, v21, vcc
	v_lshl_add_u64 v[32:33], v[4:5], 0, v[30:31]
	v_ashrrev_i32_e32 v45, 31, v44
	global_load_dwordx2 v[52:53], v[26:27], off offset:512
	global_load_dwordx2 v[46:47], v[26:27], off offset:1024
	global_load_dwordx2 v[42:43], v[26:27], off offset:1536
	global_load_dwordx2 v[38:39], v[26:27], off offset:2048
	global_load_dwordx2 v[36:37], v[26:27], off offset:2560
	global_load_dwordx2 v[30:31], v[26:27], off offset:3072
	s_nop 0
	global_load_dwordx2 v[26:27], v[26:27], off offset:3584
	s_nop 0
	global_load_dword v181, v[32:33], off
	v_lshl_add_u64 v[34:35], v[4:5], 0, v[34:35]
	global_load_dword v173, v[32:33], off offset:256
	global_load_dword v165, v[32:33], off offset:512
	global_load_dword v88, v[32:33], off offset:768
	global_load_dword v155, v[32:33], off offset:1024
	global_load_dword v147, v[32:33], off offset:1280
	global_load_dword v140, v[32:33], off offset:1536
	global_load_dword v132, v[32:33], off offset:1792
	global_load_dword v185, v[34:35], off
	v_lshlrev_b64 v[32:33], 11, v[44:45]
	ds_bpermute_b32 v44, v103, v130
	v_add_co_u32_e32 v56, vcc, s26, v20
	v_lshl_add_u64 v[32:33], v[4:5], 0, v[32:33]
	global_load_dword v177, v[34:35], off offset:256
	global_load_dword v169, v[34:35], off offset:512
	global_load_dword v89, v[34:35], off offset:768
	global_load_dword v156, v[34:35], off offset:1024
	global_load_dword v148, v[34:35], off offset:1280
	global_load_dword v143, v[34:35], off offset:1536
	global_load_dword v135, v[34:35], off offset:1792
	global_load_dword v187, v[32:33], off
	s_waitcnt lgkmcnt(0)
	v_ashrrev_i32_e32 v45, 31, v44
	v_lshlrev_b64 v[34:35], 11, v[44:45]
	v_addc_co_u32_e32 v57, vcc, 0, v21, vcc
	v_lshl_add_u64 v[34:35], v[4:5], 0, v[34:35]
	global_load_dword v179, v[32:33], off offset:256
	global_load_dword v171, v[32:33], off offset:512
	global_load_dword v163, v[32:33], off offset:768
	global_load_dword v157, v[32:33], off offset:1024
	global_load_dword v153, v[32:33], off offset:1280
	global_load_dword v145, v[32:33], off offset:1536
	global_load_dword v137, v[32:33], off offset:1792
	global_load_dword v188, v[34:35], off
	global_load_dwordx2 v[60:61], v[56:57], off offset:-4096
	global_load_dword v180, v[34:35], off offset:256
	global_load_dword v172, v[34:35], off offset:512
	global_load_dword v164, v[34:35], off offset:768
	global_load_dword v162, v[34:35], off offset:1024
	global_load_dword v154, v[34:35], off offset:1280
	global_load_dword v146, v[34:35], off offset:1536
	global_load_dword v138, v[34:35], off offset:1792
	ds_bpermute_b32 v59, v95, v19
	ds_bpermute_b32 v58, v97, v19
	ds_bpermute_b32 v51, v98, v19
	ds_bpermute_b32 v50, v99, v19

	s_waitcnt vmcnt(63)
	v_cvt_pk_f32_fp8_e32 v[32:33], v62
	v_cvt_pk_f32_fp8_sdwa v[34:35], v62 src0_sel:WORD_1
	v_lshlrev_b32_e32 v77, 16, v25
	v_lshlrev_b32_e32 v76, 16, v24
	v_cvt_pk_f32_fp8_e32 v[44:45], v63
	v_cvt_pk_f32_fp8_sdwa v[62:63], v63 src0_sel:WORD_1
	v_mov_b32_e32 v86, v32
	v_and_b32_e32 v83, 0xffff0000, v25
	v_and_b32_e32 v82, 0xffff0000, v24
	v_mov_b32_e32 v87, v62
	v_mov_b32_e32 v62, v33

	s_waitcnt vmcnt(55)
	v_cvt_pk_f32_fp8_e32 v[66:67], v70
	v_cvt_pk_f32_fp8_sdwa v[70:71], v70 src0_sel:WORD_1
	v_mov_b32_e32 v24, v44
	v_mov_b32_e32 v25, v34
	s_waitcnt lgkmcnt(2)
	v_pk_mul_f32 v[86:87], v[86:87], v[58:59] op_sel:[0,1] op_sel_hi:[1,0]
	v_mov_b32_e32 v34, v45
	v_pk_mul_f32 v[32:33], v[62:63], v[58:59] op_sel:[0,1] op_sel_hi:[1,0]

	s_waitcnt vmcnt(47)
	v_cvt_pk_f32_fp8_e32 v[72:73], v74
	v_cvt_pk_f32_fp8_sdwa v[74:75], v74 src0_sel:WORD_1
	v_pk_fma_f32 v[24:25], v[24:25], v[58:59], v[86:87]
	v_mov_b32_e32 v87, v70
	v_mov_b32_e32 v150, v66
	v_mov_b32_e32 v151, v74
	v_mov_b32_e32 v74, v67
	v_pk_fma_f32 v[32:33], v[34:35], v[58:59], v[32:33]
	v_mov_b32_e32 v70, v73
	s_waitcnt lgkmcnt(0)
	v_pk_mul_f32 v[34:35], v[74:75], v[50:51] op_sel:[0,1] op_sel_hi:[1,0]
	v_mov_b32_e32 v86, v72
	v_pk_mul_f32 v[150:151], v[150:151], v[50:51] op_sel:[0,1] op_sel_hi:[1,0]
	v_pk_fma_f32 v[34:35], v[70:71], v[50:51], v[34:35]
	v_pk_fma_f32 v[86:87], v[86:87], v[50:51], v[150:151]
	v_pk_add_f32 v[32:33], v[32:33], v[34:35]
	v_pk_add_f32 v[24:25], v[24:25], v[86:87]
	v_pk_add_f32 v[34:35], v[32:33], v[82:83]
	v_pk_add_f32 v[24:25], v[24:25], v[76:77]
	v_and_b32_sdwa v44, v35, v129 dst_sel:DWORD dst_unused:UNUSED_PAD src0_sel:WORD_1 src1_sel:DWORD
	v_and_b32_sdwa v32, v25, v129 dst_sel:DWORD dst_unused:UNUSED_PAD src0_sel:WORD_1 src1_sel:DWORD
	v_and_b32_sdwa v45, v34, v129 dst_sel:DWORD dst_unused:UNUSED_PAD src0_sel:WORD_1 src1_sel:DWORD
	v_add3_u32 v44, v35, v44, s4
	v_add_co_u32_e32 v66, vcc, s5, v20
	v_and_b32_sdwa v33, v24, v129 dst_sel:DWORD dst_unused:UNUSED_PAD src0_sel:WORD_1 src1_sel:DWORD
	v_add3_u32 v32, v25, v32, s4
	v_add3_u32 v45, v34, v45, s4
	v_and_b32_e32 v44, 0xffff0000, v44
	v_addc_co_u32_e32 v67, vcc, 0, v21, vcc
	v_add3_u32 v33, v24, v33, s4
	v_and_b32_e32 v62, 0xffff0000, v45
	v_or_b32_sdwa v45, v44, v32 dst_sel:DWORD dst_unused:UNUSED_PAD src0_sel:DWORD src1_sel:WORD_1
	v_add_co_u32_e32 v32, vcc, s27, v20
	v_or_b32_sdwa v44, v62, v33 dst_sel:DWORD dst_unused:UNUSED_PAD src0_sel:DWORD src1_sel:WORD_1
	s_nop 0
	v_addc_co_u32_e32 v33, vcc, 0, v21, vcc
	global_store_dwordx2 v[32:33], v[44:45], off offset:-4096
	v_pk_mul_f32 v[44:45], v[34:35], v[34:35]
	s_nop 0
	v_pk_fma_f32 v[70:71], v[24:25], v[24:25], v[44:45]
	v_cvt_pk_f32_fp8_e32 v[44:45], v139
	v_cvt_pk_f32_fp8_sdwa v[74:75], v149 src0_sel:WORD_1
	v_cvt_pk_f32_fp8_sdwa v[62:63], v139 src0_sel:WORD_1
	v_cvt_pk_f32_fp8_e32 v[72:73], v149
	v_cvt_pk_f32_fp8_e32 v[76:77], v158

	s_waitcnt vmcnt(47)
	v_cvt_pk_f32_fp8_sdwa v[150:151], v159 src0_sel:WORD_1
	v_cvt_pk_f32_fp8_sdwa v[82:83], v158 src0_sel:WORD_1
	v_cvt_pk_f32_fp8_e32 v[86:87], v159
	v_mov_b32_e32 v166, v44
	v_mov_b32_e32 v167, v74
	v_lshlrev_b32_e32 v159, 16, v41
	v_lshlrev_b32_e32 v158, 16, v40
	v_and_b32_e32 v161, 0xffff0000, v41
	v_and_b32_e32 v160, 0xffff0000, v40
	v_mov_b32_e32 v40, v72
	v_mov_b32_e32 v41, v62
	v_pk_mul_f32 v[166:167], v[166:167], v[58:59] op_sel:[0,1] op_sel_hi:[1,0]
	v_mov_b32_e32 v174, v76
	v_mov_b32_e32 v175, v150
	v_mov_b32_e32 v74, v45
	v_pk_fma_f32 v[40:41], v[40:41], v[58:59], v[166:167]
	v_mov_b32_e32 v166, v86
	v_mov_b32_e32 v167, v82
	v_pk_mul_f32 v[174:175], v[174:175], v[50:51] op_sel:[0,1] op_sel_hi:[1,0]
	v_mov_b32_e32 v62, v73
	v_pk_mul_f32 v[44:45], v[74:75], v[58:59] op_sel:[0,1] op_sel_hi:[1,0]
	v_mov_b32_e32 v150, v77
	v_pk_fma_f32 v[166:167], v[166:167], v[50:51], v[174:175]
	v_pk_fma_f32 v[44:45], v[62:63], v[58:59], v[44:45]
	v_mov_b32_e32 v82, v87
	v_pk_mul_f32 v[62:63], v[150:151], v[50:51] op_sel:[0,1] op_sel_hi:[1,0]
	v_pk_add_f32 v[40:41], v[40:41], v[166:167]
	v_pk_fma_f32 v[62:63], v[82:83], v[50:51], v[62:63]
	v_pk_add_f32 v[40:41], v[40:41], v[158:159]
	v_pk_add_f32 v[44:45], v[44:45], v[62:63]
	v_and_b32_sdwa v63, v40, v129 dst_sel:DWORD dst_unused:UNUSED_PAD src0_sel:WORD_1 src1_sel:DWORD
	v_pk_add_f32 v[44:45], v[44:45], v[160:161]
	v_add3_u32 v72, v40, v63, s4
	v_and_b32_sdwa v63, v45, v129 dst_sel:DWORD dst_unused:UNUSED_PAD src0_sel:WORD_1 src1_sel:DWORD
	v_and_b32_sdwa v73, v44, v129 dst_sel:DWORD dst_unused:UNUSED_PAD src0_sel:WORD_1 src1_sel:DWORD
	v_and_b32_sdwa v62, v41, v129 dst_sel:DWORD dst_unused:UNUSED_PAD src0_sel:WORD_1 src1_sel:DWORD
	v_add3_u32 v63, v45, v63, s4
	v_add3_u32 v73, v44, v73, s4
	v_add3_u32 v62, v41, v62, s4
	v_and_b32_e32 v63, 0xffff0000, v63
	v_and_b32_e32 v73, 0xffff0000, v73
	v_or_b32_sdwa v63, v63, v62 dst_sel:DWORD dst_unused:UNUSED_PAD src0_sel:DWORD src1_sel:WORD_1
	v_or_b32_sdwa v62, v73, v72 dst_sel:DWORD dst_unused:UNUSED_PAD src0_sel:DWORD src1_sel:WORD_1
	global_store_dwordx2 v[66:67], v[62:63], off offset:512
	v_pk_mul_f32 v[62:63], v[44:45], v[44:45]
	s_nop 0
	v_pk_fma_f32 v[76:77], v[40:41], v[40:41], v[62:63]
	v_cvt_pk_f32_fp8_e32 v[62:63], v141
	v_cvt_pk_f32_fp8_sdwa v[82:83], v152 src0_sel:WORD_1
	v_cvt_pk_f32_fp8_sdwa v[72:73], v141 src0_sel:WORD_1
	v_cvt_pk_f32_fp8_e32 v[74:75], v152
	v_cvt_pk_f32_fp8_e32 v[86:87], v176

	s_waitcnt vmcnt(47)
	v_cvt_pk_f32_fp8_sdwa v[160:161], v182 src0_sel:WORD_1
	v_cvt_pk_f32_fp8_sdwa v[150:151], v176 src0_sel:WORD_1
	v_cvt_pk_f32_fp8_e32 v[158:159], v182
	v_mov_b32_e32 v182, v62
	v_mov_b32_e32 v183, v82
	v_lshlrev_b32_e32 v167, 16, v55
	v_lshlrev_b32_e32 v166, 16, v54
	v_and_b32_e32 v175, 0xffff0000, v55
	v_and_b32_e32 v174, 0xffff0000, v54
	v_mov_b32_e32 v54, v74
	v_mov_b32_e32 v55, v72
	v_pk_mul_f32 v[182:183], v[182:183], v[58:59] op_sel:[0,1] op_sel_hi:[1,0]
	v_mov_b32_e32 v190, v86
	v_mov_b32_e32 v191, v160
	v_mov_b32_e32 v82, v63
	v_pk_fma_f32 v[54:55], v[54:55], v[58:59], v[182:183]
	v_mov_b32_e32 v182, v158
	v_mov_b32_e32 v183, v150
	v_pk_mul_f32 v[190:191], v[190:191], v[50:51] op_sel:[0,1] op_sel_hi:[1,0]
	v_mov_b32_e32 v72, v75
	v_pk_mul_f32 v[62:63], v[82:83], v[58:59] op_sel:[0,1] op_sel_hi:[1,0]
	v_mov_b32_e32 v160, v87
	v_pk_fma_f32 v[182:183], v[182:183], v[50:51], v[190:191]
	v_pk_fma_f32 v[62:63], v[72:73], v[58:59], v[62:63]
	v_mov_b32_e32 v150, v159
	v_pk_mul_f32 v[72:73], v[160:161], v[50:51] op_sel:[0,1] op_sel_hi:[1,0]
	v_pk_add_f32 v[54:55], v[54:55], v[182:183]
	v_pk_fma_f32 v[72:73], v[150:151], v[50:51], v[72:73]
	v_pk_add_f32 v[54:55], v[54:55], v[166:167]
	v_pk_add_f32 v[62:63], v[62:63], v[72:73]
	v_and_b32_sdwa v73, v54, v129 dst_sel:DWORD dst_unused:UNUSED_PAD src0_sel:WORD_1 src1_sel:DWORD
	v_pk_add_f32 v[62:63], v[62:63], v[174:175]
	v_add3_u32 v74, v54, v73, s4
	v_and_b32_sdwa v73, v63, v129 dst_sel:DWORD dst_unused:UNUSED_PAD src0_sel:WORD_1 src1_sel:DWORD
	v_and_b32_sdwa v75, v62, v129 dst_sel:DWORD dst_unused:UNUSED_PAD src0_sel:WORD_1 src1_sel:DWORD
	v_and_b32_sdwa v72, v55, v129 dst_sel:DWORD dst_unused:UNUSED_PAD src0_sel:WORD_1 src1_sel:DWORD
	v_add3_u32 v73, v63, v73, s4
	v_add3_u32 v75, v62, v75, s4
	v_add3_u32 v72, v55, v72, s4
	v_and_b32_e32 v73, 0xffff0000, v73
	v_and_b32_e32 v75, 0xffff0000, v75
	v_or_b32_sdwa v73, v73, v72 dst_sel:DWORD dst_unused:UNUSED_PAD src0_sel:DWORD src1_sel:WORD_1
	v_or_b32_sdwa v72, v75, v74 dst_sel:DWORD dst_unused:UNUSED_PAD src0_sel:DWORD src1_sel:WORD_1
	global_store_dwordx2 v[66:67], v[72:73], off offset:1024
	v_pk_mul_f32 v[72:73], v[62:63], v[62:63]
	s_nop 0
	v_pk_fma_f32 v[82:83], v[54:55], v[54:55], v[72:73]
	v_cvt_pk_f32_fp8_e32 v[72:73], v142
	v_cvt_pk_f32_fp8_sdwa v[150:151], v168 src0_sel:WORD_1
	v_cvt_pk_f32_fp8_sdwa v[74:75], v142 src0_sel:WORD_1
	v_cvt_pk_f32_fp8_e32 v[86:87], v168
	v_cvt_pk_f32_fp8_e32 v[158:159], v178

	s_waitcnt vmcnt(47)
	v_cvt_pk_f32_fp8_sdwa v[174:175], v189 src0_sel:WORD_1
	v_cvt_pk_f32_fp8_sdwa v[160:161], v178 src0_sel:WORD_1
	v_cvt_pk_f32_fp8_e32 v[166:167], v189
	v_mov_b32_e32 v192, v72
	v_mov_b32_e32 v193, v150
	v_lshlrev_b32_e32 v183, 16, v65
	v_lshlrev_b32_e32 v182, 16, v64
	v_and_b32_e32 v191, 0xffff0000, v65
	v_and_b32_e32 v190, 0xffff0000, v64
	v_mov_b32_e32 v64, v86
	v_mov_b32_e32 v65, v74
	v_pk_mul_f32 v[192:193], v[192:193], v[58:59] op_sel:[0,1] op_sel_hi:[1,0]
	v_mov_b32_e32 v194, v158
	v_mov_b32_e32 v195, v174
	v_mov_b32_e32 v150, v73
	v_pk_fma_f32 v[64:65], v[64:65], v[58:59], v[192:193]
	v_mov_b32_e32 v192, v166
	v_mov_b32_e32 v193, v160
	v_pk_mul_f32 v[194:195], v[194:195], v[50:51] op_sel:[0,1] op_sel_hi:[1,0]
	v_mov_b32_e32 v74, v87
	v_pk_mul_f32 v[72:73], v[150:151], v[58:59] op_sel:[0,1] op_sel_hi:[1,0]
	v_mov_b32_e32 v174, v159
	v_pk_fma_f32 v[192:193], v[192:193], v[50:51], v[194:195]
	v_pk_fma_f32 v[72:73], v[74:75], v[58:59], v[72:73]
	v_mov_b32_e32 v160, v167
	v_pk_mul_f32 v[74:75], v[174:175], v[50:51] op_sel:[0,1] op_sel_hi:[1,0]
	v_pk_add_f32 v[64:65], v[64:65], v[192:193]
	v_pk_fma_f32 v[74:75], v[160:161], v[50:51], v[74:75]
	v_pk_add_f32 v[64:65], v[64:65], v[182:183]
	v_pk_add_f32 v[72:73], v[72:73], v[74:75]
	v_and_b32_sdwa v75, v64, v129 dst_sel:DWORD dst_unused:UNUSED_PAD src0_sel:WORD_1 src1_sel:DWORD
	v_pk_add_f32 v[72:73], v[72:73], v[190:191]
	v_add3_u32 v86, v64, v75, s4
	v_and_b32_sdwa v75, v73, v129 dst_sel:DWORD dst_unused:UNUSED_PAD src0_sel:WORD_1 src1_sel:DWORD
	v_and_b32_sdwa v87, v72, v129 dst_sel:DWORD dst_unused:UNUSED_PAD src0_sel:WORD_1 src1_sel:DWORD
	v_and_b32_sdwa v74, v65, v129 dst_sel:DWORD dst_unused:UNUSED_PAD src0_sel:WORD_1 src1_sel:DWORD
	v_add3_u32 v75, v73, v75, s4
	v_add3_u32 v87, v72, v87, s4
	v_add3_u32 v74, v65, v74, s4
	v_and_b32_e32 v75, 0xffff0000, v75
	v_and_b32_e32 v87, 0xffff0000, v87
	v_or_b32_sdwa v75, v75, v74 dst_sel:DWORD dst_unused:UNUSED_PAD src0_sel:DWORD src1_sel:WORD_1
	v_or_b32_sdwa v74, v87, v86 dst_sel:DWORD dst_unused:UNUSED_PAD src0_sel:DWORD src1_sel:WORD_1
	global_store_dwordx2 v[66:67], v[74:75], off offset:1536
	v_pk_mul_f32 v[74:75], v[72:73], v[72:73]
	s_nop 0
	v_pk_fma_f32 v[86:87], v[64:65], v[64:65], v[74:75]
	v_cvt_pk_f32_fp8_e32 v[74:75], v144
	v_cvt_pk_f32_fp8_sdwa v[160:161], v170 src0_sel:WORD_1
	v_cvt_pk_f32_fp8_sdwa v[150:151], v144 src0_sel:WORD_1
	v_cvt_pk_f32_fp8_e32 v[158:159], v170
	v_cvt_pk_f32_fp8_e32 v[166:167], v184

	s_waitcnt vmcnt(47)
	v_cvt_pk_f32_fp8_sdwa v[190:191], v196 src0_sel:WORD_1
	v_cvt_pk_f32_fp8_sdwa v[174:175], v184 src0_sel:WORD_1
	v_cvt_pk_f32_fp8_e32 v[182:183], v196
	v_mov_b32_e32 v196, v74
	v_mov_b32_e32 v197, v160
	v_mov_b32_e32 v160, v75
	v_lshlrev_b32_e32 v193, 16, v69
	v_lshlrev_b32_e32 v192, 16, v68
	v_and_b32_e32 v195, 0xffff0000, v69
	v_and_b32_e32 v194, 0xffff0000, v68
	v_mov_b32_e32 v68, v158
	v_mov_b32_e32 v69, v150
	v_pk_mul_f32 v[196:197], v[196:197], v[58:59] op_sel:[0,1] op_sel_hi:[1,0]
	v_mov_b32_e32 v201, v190
	v_mov_b32_e32 v150, v159
	v_pk_mul_f32 v[74:75], v[160:161], v[58:59] op_sel:[0,1] op_sel_hi:[1,0]
	v_mov_b32_e32 v190, v167
	v_pk_fma_f32 v[68:69], v[68:69], v[58:59], v[196:197]
	v_mov_b32_e32 v197, v174
	v_mov_b32_e32 v200, v166
	v_pk_fma_f32 v[74:75], v[150:151], v[58:59], v[74:75]
	v_mov_b32_e32 v174, v183
	v_pk_mul_f32 v[150:151], v[190:191], v[50:51] op_sel:[0,1] op_sel_hi:[1,0]
	v_mov_b32_e32 v196, v182
	v_pk_mul_f32 v[200:201], v[200:201], v[50:51] op_sel:[0,1] op_sel_hi:[1,0]
	v_pk_fma_f32 v[150:151], v[174:175], v[50:51], v[150:151]
	v_pk_fma_f32 v[196:197], v[196:197], v[50:51], v[200:201]
	v_pk_add_f32 v[74:75], v[74:75], v[150:151]
	v_pk_add_f32 v[68:69], v[68:69], v[196:197]
	v_pk_add_f32 v[74:75], v[74:75], v[194:195]
	v_pk_add_f32 v[68:69], v[68:69], v[192:193]
	v_and_b32_sdwa v142, v75, v129 dst_sel:DWORD dst_unused:UNUSED_PAD src0_sel:WORD_1 src1_sel:DWORD
	v_and_b32_sdwa v144, v74, v129 dst_sel:DWORD dst_unused:UNUSED_PAD src0_sel:WORD_1 src1_sel:DWORD
	v_and_b32_sdwa v139, v69, v129 dst_sel:DWORD dst_unused:UNUSED_PAD src0_sel:WORD_1 src1_sel:DWORD
	v_and_b32_sdwa v141, v68, v129 dst_sel:DWORD dst_unused:UNUSED_PAD src0_sel:WORD_1 src1_sel:DWORD
	v_add3_u32 v142, v75, v142, s4
	v_add3_u32 v144, v74, v144, s4
	v_add3_u32 v141, v68, v141, s4
	v_add3_u32 v139, v69, v139, s4
	v_and_b32_e32 v142, 0xffff0000, v142
	v_and_b32_e32 v144, 0xffff0000, v144
	v_or_b32_sdwa v151, v142, v139 dst_sel:DWORD dst_unused:UNUSED_PAD src0_sel:DWORD src1_sel:WORD_1
	v_or_b32_sdwa v150, v144, v141 dst_sel:DWORD dst_unused:UNUSED_PAD src0_sel:DWORD src1_sel:WORD_1
	global_store_dwordx2 v[66:67], v[150:151], off offset:2048
	v_pk_mul_f32 v[150:151], v[74:75], v[74:75]
	s_nop 0
	v_pk_fma_f32 v[150:151], v[68:69], v[68:69], v[150:151]
	v_cvt_pk_f32_fp8_e32 v[158:159], v78
	v_cvt_pk_f32_fp8_sdwa v[160:161], v78 src0_sel:WORD_1
	v_cvt_pk_f32_fp8_e32 v[166:167], v79
	v_cvt_pk_f32_fp8_sdwa v[78:79], v79 src0_sel:WORD_1
	v_cvt_pk_f32_fp8_e32 v[174:175], v186

	s_waitcnt vmcnt(47)
	v_cvt_pk_f32_fp8_sdwa v[192:193], v199 src0_sel:WORD_1
	v_cvt_pk_f32_fp8_sdwa v[182:183], v186 src0_sel:WORD_1
	v_cvt_pk_f32_fp8_e32 v[190:191], v199
	v_mov_b32_e32 v200, v158
	v_mov_b32_e32 v201, v78
	v_lshlrev_b32_e32 v195, 16, v49
	v_lshlrev_b32_e32 v194, 16, v48
	v_and_b32_e32 v197, 0xffff0000, v49
	v_and_b32_e32 v196, 0xffff0000, v48
	v_mov_b32_e32 v48, v166
	v_mov_b32_e32 v49, v160
	v_pk_mul_f32 v[200:201], v[200:201], v[58:59] op_sel:[0,1] op_sel_hi:[1,0]
	v_mov_b32_e32 v203, v192
	v_mov_b32_e32 v78, v159
	v_mov_b32_e32 v192, v175
	v_pk_fma_f32 v[48:49], v[48:49], v[58:59], v[200:201]
	v_mov_b32_e32 v201, v182
	v_mov_b32_e32 v202, v174
	v_mov_b32_e32 v160, v167
	v_pk_mul_f32 v[78:79], v[78:79], v[58:59] op_sel:[0,1] op_sel_hi:[1,0]
	v_mov_b32_e32 v182, v191
	v_pk_mul_f32 v[158:159], v[192:193], v[50:51] op_sel:[0,1] op_sel_hi:[1,0]
	v_mov_b32_e32 v200, v190
	v_pk_mul_f32 v[202:203], v[202:203], v[50:51] op_sel:[0,1] op_sel_hi:[1,0]
	v_pk_fma_f32 v[78:79], v[160:161], v[58:59], v[78:79]
	v_pk_fma_f32 v[158:159], v[182:183], v[50:51], v[158:159]
	v_pk_fma_f32 v[200:201], v[200:201], v[50:51], v[202:203]
	v_pk_add_f32 v[78:79], v[78:79], v[158:159]
	v_pk_add_f32 v[48:49], v[48:49], v[200:201]
	v_pk_add_f32 v[78:79], v[78:79], v[196:197]
	v_pk_add_f32 v[48:49], v[48:49], v[194:195]
	v_and_b32_sdwa v142, v79, v129 dst_sel:DWORD dst_unused:UNUSED_PAD src0_sel:WORD_1 src1_sel:DWORD
	v_and_b32_sdwa v144, v78, v129 dst_sel:DWORD dst_unused:UNUSED_PAD src0_sel:WORD_1 src1_sel:DWORD
	v_and_b32_sdwa v139, v49, v129 dst_sel:DWORD dst_unused:UNUSED_PAD src0_sel:WORD_1 src1_sel:DWORD
	v_and_b32_sdwa v141, v48, v129 dst_sel:DWORD dst_unused:UNUSED_PAD src0_sel:WORD_1 src1_sel:DWORD
	v_add3_u32 v142, v79, v142, s4
	v_add3_u32 v144, v78, v144, s4
	v_add3_u32 v141, v48, v141, s4
	v_add3_u32 v139, v49, v139, s4
	v_and_b32_e32 v142, 0xffff0000, v142
	v_and_b32_e32 v144, 0xffff0000, v144
	v_or_b32_sdwa v159, v142, v139 dst_sel:DWORD dst_unused:UNUSED_PAD src0_sel:DWORD src1_sel:WORD_1
	v_or_b32_sdwa v158, v144, v141 dst_sel:DWORD dst_unused:UNUSED_PAD src0_sel:DWORD src1_sel:WORD_1
	global_store_dwordx2 v[66:67], v[158:159], off offset:2560
	v_pk_mul_f32 v[158:159], v[78:79], v[78:79]
	s_nop 0
	v_pk_fma_f32 v[158:159], v[48:49], v[48:49], v[158:159]
	v_cvt_pk_f32_fp8_e32 v[160:161], v80
	v_cvt_pk_f32_fp8_sdwa v[182:183], v81 src0_sel:WORD_1
	v_cvt_pk_f32_fp8_sdwa v[166:167], v80 src0_sel:WORD_1
	v_cvt_pk_f32_fp8_e32 v[174:175], v81
	v_cvt_pk_f32_fp8_e32 v[190:191], v84
	v_cvt_pk_f32_fp8_sdwa v[192:193], v84 src0_sel:WORD_1

	s_waitcnt vmcnt(47)
	v_cvt_pk_f32_fp8_e32 v[194:195], v85
	v_cvt_pk_f32_fp8_sdwa v[84:85], v85 src0_sel:WORD_1
	v_mov_b32_e32 v200, v160
	v_mov_b32_e32 v201, v182
	v_mov_b32_e32 v196, v174
	v_mov_b32_e32 v197, v166
	v_pk_mul_f32 v[200:201], v[200:201], v[58:59] op_sel:[0,1] op_sel_hi:[1,0]
	v_mov_b32_e32 v202, v190
	v_mov_b32_e32 v203, v84
	v_pk_fma_f32 v[196:197], v[196:197], v[58:59], v[200:201]
	v_mov_b32_e32 v200, v194
	v_mov_b32_e32 v201, v192
	v_pk_mul_f32 v[202:203], v[202:203], v[50:51] op_sel:[0,1] op_sel_hi:[1,0]
	v_mov_b32_e32 v182, v161
	v_mov_b32_e32 v84, v191
	v_pk_fma_f32 v[200:201], v[200:201], v[50:51], v[202:203]
	v_mov_b32_e32 v166, v175
	v_pk_mul_f32 v[160:161], v[182:183], v[58:59] op_sel:[0,1] op_sel_hi:[1,0]
	v_mov_b32_e32 v192, v195
	v_pk_mul_f32 v[84:85], v[84:85], v[50:51] op_sel:[0,1] op_sel_hi:[1,0]
	v_lshlrev_b32_e32 v81, 16, v29
	v_lshlrev_b32_e32 v80, 16, v28
	v_pk_add_f32 v[196:197], v[196:197], v[200:201]
	v_pk_fma_f32 v[160:161], v[166:167], v[58:59], v[160:161]
	v_pk_fma_f32 v[84:85], v[192:193], v[50:51], v[84:85]
	v_and_b32_e32 v29, 0xffff0000, v29
	v_and_b32_e32 v28, 0xffff0000, v28
	v_pk_add_f32 v[80:81], v[196:197], v[80:81]
	v_pk_add_f32 v[84:85], v[160:161], v[84:85]
	s_nop 0
	v_pk_add_f32 v[84:85], v[84:85], v[28:29]
	v_and_b32_sdwa v29, v80, v129 dst_sel:DWORD dst_unused:UNUSED_PAD src0_sel:WORD_1 src1_sel:DWORD
	v_add3_u32 v139, v80, v29, s4
	v_and_b32_sdwa v29, v85, v129 dst_sel:DWORD dst_unused:UNUSED_PAD src0_sel:WORD_1 src1_sel:DWORD
	v_and_b32_sdwa v141, v84, v129 dst_sel:DWORD dst_unused:UNUSED_PAD src0_sel:WORD_1 src1_sel:DWORD
	v_and_b32_sdwa v28, v81, v129 dst_sel:DWORD dst_unused:UNUSED_PAD src0_sel:WORD_1 src1_sel:DWORD
	v_add3_u32 v29, v85, v29, s4
	v_add3_u32 v141, v84, v141, s4
	v_add3_u32 v28, v81, v28, s4
	v_and_b32_e32 v29, 0xffff0000, v29
	v_and_b32_e32 v141, 0xffff0000, v141
	v_or_b32_sdwa v29, v29, v28 dst_sel:DWORD dst_unused:UNUSED_PAD src0_sel:DWORD src1_sel:WORD_1
	v_or_b32_sdwa v28, v141, v139 dst_sel:DWORD dst_unused:UNUSED_PAD src0_sel:DWORD src1_sel:WORD_1
	global_store_dwordx2 v[66:67], v[28:29], off offset:3072
	v_pk_mul_f32 v[28:29], v[84:85], v[84:85]
	s_nop 0
	v_pk_fma_f32 v[160:161], v[80:81], v[80:81], v[28:29]
	v_cvt_pk_f32_fp8_e32 v[166:167], v131
	v_cvt_pk_f32_fp8_sdwa v[190:191], v133 src0_sel:WORD_1
	v_cvt_pk_f32_fp8_sdwa v[174:175], v131 src0_sel:WORD_1
	v_cvt_pk_f32_fp8_e32 v[182:183], v133
	v_cvt_pk_f32_fp8_e32 v[192:193], v134

	s_waitcnt vmcnt(47)
	v_cvt_pk_f32_fp8_sdwa v[200:201], v136 src0_sel:WORD_1
	v_cvt_pk_f32_fp8_sdwa v[194:195], v134 src0_sel:WORD_1
	v_cvt_pk_f32_fp8_e32 v[196:197], v136
	v_mov_b32_e32 v204, v166
	v_mov_b32_e32 v205, v190
	v_mov_b32_e32 v202, v182
	v_mov_b32_e32 v203, v174
	v_pk_mul_f32 v[204:205], v[204:205], v[58:59] op_sel:[0,1] op_sel_hi:[1,0]
	v_mov_b32_e32 v206, v192
	v_mov_b32_e32 v207, v200
	v_mov_b32_e32 v190, v167
	v_pk_fma_f32 v[202:203], v[202:203], v[58:59], v[204:205]
	v_mov_b32_e32 v204, v196
	v_mov_b32_e32 v205, v194
	v_pk_mul_f32 v[206:207], v[206:207], v[50:51] op_sel:[0,1] op_sel_hi:[1,0]
	v_mov_b32_e32 v174, v183
	v_pk_mul_f32 v[166:167], v[190:191], v[58:59] op_sel:[0,1] op_sel_hi:[1,0]
	v_mov_b32_e32 v200, v193
	v_pk_fma_f32 v[204:205], v[204:205], v[50:51], v[206:207]
	v_pk_fma_f32 v[58:59], v[174:175], v[58:59], v[166:167]
	v_mov_b32_e32 v194, v197
	v_pk_mul_f32 v[166:167], v[200:201], v[50:51] op_sel:[0,1] op_sel_hi:[1,0]
	v_lshlrev_b32_e32 v29, 16, v23
	v_lshlrev_b32_e32 v28, 16, v22
	v_pk_add_f32 v[202:203], v[202:203], v[204:205]
	v_pk_fma_f32 v[50:51], v[194:195], v[50:51], v[166:167]
	v_and_b32_e32 v23, 0xffff0000, v23
	v_and_b32_e32 v22, 0xffff0000, v22
	v_pk_add_f32 v[28:29], v[202:203], v[28:29]
	v_pk_add_f32 v[50:51], v[58:59], v[50:51]
	s_nop 0
	v_pk_add_f32 v[58:59], v[50:51], v[22:23]
	v_and_b32_sdwa v23, v28, v129 dst_sel:DWORD dst_unused:UNUSED_PAD src0_sel:WORD_1 src1_sel:DWORD
	v_add3_u32 v50, v28, v23, s4
	v_and_b32_sdwa v23, v59, v129 dst_sel:DWORD dst_unused:UNUSED_PAD src0_sel:WORD_1 src1_sel:DWORD
	v_and_b32_sdwa v51, v58, v129 dst_sel:DWORD dst_unused:UNUSED_PAD src0_sel:WORD_1 src1_sel:DWORD
	v_and_b32_sdwa v22, v29, v129 dst_sel:DWORD dst_unused:UNUSED_PAD src0_sel:WORD_1 src1_sel:DWORD
	v_add3_u32 v23, v59, v23, s4
	v_add3_u32 v51, v58, v51, s4
	v_add3_u32 v22, v29, v22, s4
	v_and_b32_e32 v23, 0xffff0000, v23
	v_and_b32_e32 v51, 0xffff0000, v51
	v_or_b32_sdwa v23, v23, v22 dst_sel:DWORD dst_unused:UNUSED_PAD src0_sel:DWORD src1_sel:WORD_1
	v_or_b32_sdwa v22, v51, v50 dst_sel:DWORD dst_unused:UNUSED_PAD src0_sel:DWORD src1_sel:WORD_1
	v_add_f32_e32 v50, v76, v77
	v_add_f32_e32 v51, v70, v71
	v_add_f32_e32 v50, v51, v50
	v_add_f32_e32 v51, v82, v83
	v_add_f32_e32 v50, v50, v51
	v_add_f32_e32 v51, v86, v87
	v_add_f32_e32 v50, v50, v51
	v_add_f32_e32 v51, v150, v151
	global_store_dwordx2 v[66:67], v[22:23], off offset:3584
	v_pk_mul_f32 v[22:23], v[58:59], v[58:59]
	v_add_f32_e32 v50, v50, v51
	v_add_f32_e32 v51, v158, v159
	v_pk_fma_f32 v[22:23], v[28:29], v[28:29], v[22:23]
	v_add_f32_e32 v50, v50, v51
	v_add_f32_e32 v51, v160, v161
	v_add_f32_e32 v50, v50, v51
	v_add_f32_e32 v22, v22, v23
	v_add_f32_e32 v22, v50, v22
	v_mov_b64_e32 v[158:159], v[212:213]
	v_mov_b64_e32 v[160:161], v[214:215]
	ds_bpermute_b32 v23, v1, v22


	s_waitcnt vmcnt(16)
	v_cvt_pk_f32_fp8_sdwa v[82:83], v188 src0_sel:WORD_1
	v_mov_b32_e32 v189, v82
	s_waitcnt lgkmcnt(0)
	v_add_f32_e32 v22, v22, v23
	ds_bpermute_b32 v23, v90, v22
	s_waitcnt lgkmcnt(0)
	v_add_f32_e32 v22, v22, v23
	ds_bpermute_b32 v23, v91, v22
	s_waitcnt lgkmcnt(0)
	v_add_f32_e32 v22, v22, v23
	ds_bpermute_b32 v23, v92, v22
	s_waitcnt lgkmcnt(0)
	v_add_f32_e32 v22, v22, v23
	ds_bpermute_b32 v23, v93, v22
	s_waitcnt lgkmcnt(0)
	v_add_f32_e32 v22, v22, v23
	ds_bpermute_b32 v23, v94, v22
	s_waitcnt lgkmcnt(0)
	v_add_f32_e32 v22, v22, v23
	v_fmamk_f32 v22, v22, 0x3a000000, v127
	v_mul_f32_e32 v23, 0x4f800000, v22
	v_cmp_gt_f32_e32 vcc, s19, v22
	s_nop 1
	v_cndmask_b32_e32 v50, v22, v23, vcc
	v_sqrt_f32_e32 v51, v50
	v_lshl_add_u64 v[22:23], s[82:83], 0, v[14:15]
	v_add_u32_e32 v66, -1, v51
	v_add_u32_e32 v67, 1, v51
	v_fma_f32 v70, -v66, v51, v50
	v_fma_f32 v71, -v67, v51, v50
	v_cmp_ge_f32_e64 s[8:9], 0, v70
	s_nop 1
	v_cndmask_b32_e64 v51, v51, v66, s[8:9]
	v_cmp_lt_f32_e64 s[8:9], 0, v71
	s_nop 1
	v_cndmask_b32_e64 v51, v51, v67, s[8:9]
	v_mul_f32_e32 v66, 0x37800000, v51
	v_cndmask_b32_e32 v51, v51, v66, vcc
	v_cmp_class_f32_e32 vcc, v50, v128
	v_mov_b32_e32 v67, 0
	s_nop 0
	v_cndmask_b32_e32 v50, v51, v50, vcc
	v_div_scale_f32 v51, s[0:1], v50, v50, 1.0
	v_rcp_f32_e32 v66, v51
	v_div_scale_f32 v70, vcc, 1.0, v50, 1.0
	v_fma_f32 v71, -v51, v66, 1.0
	v_fmac_f32_e32 v66, v71, v66
	v_mul_f32_e32 v71, v70, v66
	v_fma_f32 v76, -v51, v71, v70
	v_fmac_f32_e32 v71, v76, v66
	v_fma_f32 v51, -v51, v71, v70
	v_div_fmas_f32 v51, v51, v66, v71
	v_div_fixup_f32 v66, v51, v50, 1.0
	v_mul_f32_e32 v24, v66, v24
	v_mul_f32_e32 v34, v66, v34

	v_mul_f32_e32 v24, v158, v24
	v_mul_f32_e32 v34, v159, v34
	v_cvt_pk_fp8_f32 v67, v24, v34
	v_mul_f32_e32 v25, v66, v25
	v_mul_f32_e32 v24, v66, v35
	v_mul_f32_e32 v25, v160, v25
	v_mul_f32_e32 v24, v161, v24
	v_cvt_pk_fp8_f32 v67, v25, v24 op_sel:[0,0,1]
	v_add_co_u32_e32 v24, vcc, s30, v22
	v_mul_f32_e32 v35, v66, v40
	s_nop 0
	v_addc_co_u32_e32 v25, vcc, 0, v23, vcc
	global_store_dword v[24:25], v67, off offset:-4096
	v_mov_b64_e32 v[158:159], v[216:217]
	v_mov_b64_e32 v[160:161], v[218:219]
	v_mul_f32_e32 v40, v66, v44
	v_mov_b32_e32 v34, 0
	v_mul_f32_e32 v41, v66, v41
	v_add_co_u32_e32 v50, vcc, s21, v22
	v_mul_f32_e32 v28, v66, v28
	s_nop 0
	v_addc_co_u32_e32 v51, vcc, 0, v23, vcc
	ds_bpermute_b32 v44, v105, v130
	v_mul_f32_e32 v29, v66, v29
	ds_bpermute_b32 v67, v102, v19
	v_cvt_pk_f32_fp8_sdwa v[70:71], v181 src0_sel:WORD_1
	v_cvt_pk_f32_fp8_e32 v[76:77], v187
	v_mov_b32_e32 v82, v77

	v_mul_f32_e32 v35, v158, v35
	v_mul_f32_e32 v40, v159, v40
	v_cvt_pk_fp8_f32 v34, v35, v40
	v_mul_f32_e32 v35, v66, v45
	v_mul_f32_e32 v40, v160, v41
	v_mul_f32_e32 v35, v161, v35
	v_cvt_pk_fp8_f32 v34, v40, v35 op_sel:[0,0,1]
	v_mul_f32_e32 v35, v66, v54
	v_mul_f32_e32 v40, v66, v62
	v_mul_f32_e32 v41, v66, v55
	global_store_dword v[50:51], v34, off offset:256
	v_mov_b64_e32 v[158:159], v[220:221]
	v_mov_b64_e32 v[160:161], v[222:223]
	v_mov_b32_e32 v34, 0
	v_mul_f32_e32 v55, v66, v58
	v_mov_b32_e32 v54, 0
	s_waitcnt lgkmcnt(1)
	v_ashrrev_i32_e32 v45, 31, v44
	v_lshlrev_b64 v[44:45], 11, v[44:45]

	v_mul_f32_e32 v35, v158, v35
	v_mul_f32_e32 v40, v159, v40
	v_cvt_pk_fp8_f32 v34, v35, v40
	v_mul_f32_e32 v35, v66, v63
	v_mul_f32_e32 v40, v160, v41
	v_mul_f32_e32 v35, v161, v35
	v_cvt_pk_fp8_f32 v34, v40, v35 op_sel:[0,0,1]
	v_mul_f32_e32 v35, v66, v64
	v_mul_f32_e32 v40, v66, v72
	v_mul_f32_e32 v41, v66, v65
	global_store_dword v[50:51], v34, off offset:512
	v_mov_b64_e32 v[158:159], v[224:225]
	v_mov_b64_e32 v[160:161], v[226:227]
	v_mov_b32_e32 v34, 0

	v_mul_f32_e32 v35, v158, v35
	v_mul_f32_e32 v40, v159, v40
	v_cvt_pk_fp8_f32 v34, v35, v40
	v_mul_f32_e32 v35, v66, v73
	v_mul_f32_e32 v40, v160, v41
	v_mul_f32_e32 v35, v161, v35
	v_cvt_pk_fp8_f32 v34, v40, v35 op_sel:[0,0,1]
	v_mul_f32_e32 v35, v66, v68
	v_mul_f32_e32 v40, v66, v74
	v_mul_f32_e32 v41, v66, v69
	global_store_dword v[50:51], v34, off offset:768
	v_mov_b64_e32 v[62:63], v[228:229]
	v_mov_b64_e32 v[64:65], v[230:231]
	v_mov_b32_e32 v34, 0
	ds_bpermute_b32 v69, v100, v19
	ds_bpermute_b32 v68, v101, v19
	v_cvt_pk_f32_fp8_e32 v[72:73], v185

	v_mul_f32_e32 v35, v62, v35
	v_mul_f32_e32 v40, v63, v40
	v_cvt_pk_fp8_f32 v34, v35, v40
	v_mul_f32_e32 v35, v66, v75
	v_mul_f32_e32 v40, v64, v41
	v_mul_f32_e32 v35, v65, v35
	v_cvt_pk_fp8_f32 v34, v40, v35 op_sel:[0,0,1]
	v_mul_f32_e32 v35, v66, v48
	v_mul_f32_e32 v40, v66, v78
	v_mul_f32_e32 v41, v66, v49
	global_store_dword v[50:51], v34, off offset:1024
	v_mov_b64_e32 v[62:63], v[232:233]
	v_mov_b64_e32 v[64:65], v[234:235]
	v_mov_b32_e32 v34, 0
	ds_bpermute_b32 v48, v104, v130
	v_cvt_pk_f32_fp8_sdwa v[74:75], v185 src0_sel:WORD_1
	s_waitcnt lgkmcnt(0)
	v_ashrrev_i32_e32 v49, 31, v48
	v_lshlrev_b64 v[48:49], 11, v[48:49]
	v_mov_b32_e32 v87, v74

	v_mul_f32_e32 v35, v62, v35
	v_mul_f32_e32 v40, v63, v40
	v_cvt_pk_fp8_f32 v34, v35, v40
	v_mul_f32_e32 v35, v66, v79
	v_mul_f32_e32 v40, v64, v41
	v_mul_f32_e32 v35, v65, v35
	v_cvt_pk_fp8_f32 v34, v40, v35 op_sel:[0,0,1]
	v_mul_f32_e32 v35, v66, v80
	v_mul_f32_e32 v40, v66, v84
	v_mul_f32_e32 v41, v66, v81
	global_store_dword v[50:51], v34, off offset:1280
	v_mov_b64_e32 v[62:63], v[236:237]
	v_mov_b64_e32 v[64:65], v[238:239]
	v_mov_b32_e32 v34, 0
	v_cvt_pk_f32_fp8_sdwa v[78:79], v187 src0_sel:WORD_1
	v_cvt_pk_f32_fp8_e32 v[80:81], v188
	v_mov_b32_e32 v84, v72
	v_mov_b32_e32 v188, v76

	v_mul_f32_e32 v35, v62, v35
	v_mul_f32_e32 v40, v63, v40
	v_cvt_pk_fp8_f32 v34, v35, v40
	v_mul_f32_e32 v35, v66, v85
	v_mul_f32_e32 v40, v64, v41
	v_mul_f32_e32 v35, v65, v35
	v_cvt_pk_fp8_f32 v34, v40, v35 op_sel:[0,0,1]
	ds_bpermute_b32 v40, v106, v130
	v_mov_b32_e32 v85, v70
	v_mov_b32_e32 v70, v73
	global_store_dword v[50:51], v34, off offset:1536
	v_mov_b64_e32 v[62:63], v[240:241]
	v_mov_b64_e32 v[64:65], v[242:243]
	ds_bpermute_b32 v34, v107, v130
	s_waitcnt lgkmcnt(1)
	v_ashrrev_i32_e32 v41, 31, v40
	v_lshlrev_b64 v[40:41], 11, v[40:41]
	s_waitcnt lgkmcnt(0)
	v_ashrrev_i32_e32 v35, 31, v34
	v_lshlrev_b64 v[34:35], 11, v[34:35]
	v_lshl_add_u64 v[34:35], v[4:5], 0, v[34:35]

	v_mul_f32_e32 v28, v62, v28
	v_mul_f32_e32 v55, v63, v55
	v_cvt_pk_fp8_f32 v54, v28, v55
	v_mul_f32_e32 v28, v66, v59
	v_mul_f32_e32 v29, v64, v29
	v_mul_f32_e32 v28, v65, v28
	v_cvt_pk_fp8_f32 v54, v29, v28 op_sel:[0,0,1]
	v_lshl_add_u64 v[28:29], v[4:5], 0, v[40:41]
	v_lshl_add_u64 v[40:41], v[4:5], 0, v[44:45]
	v_lshl_add_u64 v[44:45], v[4:5], 0, v[48:49]
	global_store_dword v[50:51], v54, off offset:1792
	global_load_dword v131, v[34:35], off offset:1792
	global_load_dword v139, v[34:35], off offset:1536
	global_load_dword v149, v[34:35], off offset:1280
	global_load_dword v158, v[34:35], off offset:1024
	global_load_dword v166, v[34:35], off offset:768
	global_load_dword v174, v[34:35], off offset:512
	global_load_dword v182, v[34:35], off offset:256
	global_load_dword v190, v[34:35], off
	global_load_dword v133, v[28:29], off offset:1792
	global_load_dword v141, v[28:29], off offset:1536
	global_load_dword v150, v[28:29], off offset:1280
	global_load_dword v159, v[28:29], off offset:1024
	global_load_dword v167, v[28:29], off offset:768
	global_load_dword v175, v[28:29], off offset:512
	global_load_dword v183, v[28:29], off offset:256
	global_load_dword v191, v[28:29], off
	global_load_dword v134, v[40:41], off offset:1792
	global_load_dword v142, v[40:41], off offset:1536
	global_load_dword v151, v[40:41], off offset:1280
	global_load_dword v160, v[40:41], off offset:1024
	global_load_dword v168, v[40:41], off offset:768
	global_load_dword v176, v[40:41], off offset:512
	global_load_dword v184, v[40:41], off offset:256
	global_load_dword v193, v[40:41], off
	global_load_dword v136, v[44:45], off offset:1792
	global_load_dword v144, v[44:45], off offset:1536
	global_load_dword v152, v[44:45], off offset:1280
	global_load_dword v161, v[44:45], off offset:1024
	global_load_dword v170, v[44:45], off offset:768
	global_load_dword v178, v[44:45], off offset:512
	global_load_dword v186, v[44:45], off offset:256
	global_load_dword v196, v[44:45], off
	global_load_dwordx2 v[28:29], v[56:57], off offset:3584
	global_load_dwordx2 v[34:35], v[56:57], off offset:3072
	global_load_dwordx2 v[40:41], v[56:57], off offset:2560
	s_nop 0
	global_load_dwordx2 v[44:45], v[56:57], off offset:2048
	global_load_dwordx2 v[48:49], v[56:57], off offset:1536
	global_load_dwordx2 v[54:55], v[56:57], off offset:1024
	global_load_dwordx2 v[58:59], v[56:57], off offset:512
	global_load_dwordx2 v[62:63], v[56:57], off
	v_cvt_pk_f32_fp8_e32 v[64:65], v181
	ds_bpermute_b32 v66, v103, v19
	s_waitcnt vmcnt(63)
	v_lshlrev_b32_e32 v57, 16, v61
	v_lshlrev_b32_e32 v56, 16, v60
	v_mov_b32_e32 v86, v64
	v_pk_mul_f32 v[86:87], v[86:87], v[68:69] op_sel:[0,1] op_sel_hi:[1,0]
	v_mov_b32_e32 v74, v65
	v_pk_fma_f32 v[84:85], v[84:85], v[68:69], v[86:87]
	v_mov_b32_e32 v86, v80
	v_mov_b32_e32 v87, v78
	s_waitcnt lgkmcnt(0)
	v_pk_mul_f32 v[188:189], v[188:189], v[66:67] op_sel:[0,1] op_sel_hi:[1,0]
	v_pk_mul_f32 v[64:65], v[74:75], v[68:69] op_sel:[0,1] op_sel_hi:[1,0]
	v_pk_fma_f32 v[86:87], v[86:87], v[66:67], v[188:189]
	v_pk_fma_f32 v[64:65], v[70:71], v[68:69], v[64:65]
	v_mov_b32_e32 v78, v81
	v_pk_mul_f32 v[70:71], v[82:83], v[66:67] op_sel:[0,1] op_sel_hi:[1,0]
	v_pk_add_f32 v[84:85], v[84:85], v[86:87]
	v_pk_fma_f32 v[70:71], v[78:79], v[66:67], v[70:71]
	v_and_b32_e32 v61, 0xffff0000, v61
	v_and_b32_e32 v60, 0xffff0000, v60
	v_pk_add_f32 v[56:57], v[84:85], v[56:57]
	v_pk_add_f32 v[64:65], v[64:65], v[70:71]
	s_nop 0
	v_pk_add_f32 v[60:61], v[64:65], v[60:61]
	v_and_b32_sdwa v65, v56, v129 dst_sel:DWORD dst_unused:UNUSED_PAD src0_sel:WORD_1 src1_sel:DWORD
	v_add3_u32 v70, v56, v65, s4
	v_and_b32_sdwa v65, v61, v129 dst_sel:DWORD dst_unused:UNUSED_PAD src0_sel:WORD_1 src1_sel:DWORD
	v_and_b32_sdwa v71, v60, v129 dst_sel:DWORD dst_unused:UNUSED_PAD src0_sel:WORD_1 src1_sel:DWORD
	v_and_b32_sdwa v64, v57, v129 dst_sel:DWORD dst_unused:UNUSED_PAD src0_sel:WORD_1 src1_sel:DWORD
	v_add3_u32 v65, v61, v65, s4
	v_add3_u32 v71, v60, v71, s4
	v_add3_u32 v64, v57, v64, s4
	v_and_b32_e32 v65, 0xffff0000, v65
	v_and_b32_e32 v71, 0xffff0000, v71
	v_or_b32_sdwa v65, v65, v64 dst_sel:DWORD dst_unused:UNUSED_PAD src0_sel:DWORD src1_sel:WORD_1
	v_or_b32_sdwa v64, v71, v70 dst_sel:DWORD dst_unused:UNUSED_PAD src0_sel:DWORD src1_sel:WORD_1
	global_store_dwordx2 v[32:33], v[64:65], off
	v_pk_mul_f32 v[64:65], v[60:61], v[60:61]
	s_nop 0
	v_pk_fma_f32 v[72:73], v[56:57], v[56:57], v[64:65]
	v_cvt_pk_f32_fp8_e32 v[64:65], v173
	v_cvt_pk_f32_fp8_sdwa v[76:77], v177 src0_sel:WORD_1
	v_cvt_pk_f32_fp8_sdwa v[70:71], v173 src0_sel:WORD_1
	v_cvt_pk_f32_fp8_e32 v[74:75], v177
	v_cvt_pk_f32_fp8_e32 v[78:79], v179
	s_waitcnt vmcnt(63)
	v_cvt_pk_f32_fp8_sdwa v[84:85], v180 src0_sel:WORD_1
	v_cvt_pk_f32_fp8_sdwa v[80:81], v179 src0_sel:WORD_1
	v_cvt_pk_f32_fp8_e32 v[82:83], v180
	v_mov_b32_e32 v188, v64
	v_mov_b32_e32 v189, v76
	v_lshlrev_b32_e32 v87, 16, v53
	v_lshlrev_b32_e32 v86, 16, v52
	v_and_b32_e32 v181, 0xffff0000, v53
	v_and_b32_e32 v180, 0xffff0000, v52
	v_mov_b32_e32 v52, v74
	v_mov_b32_e32 v53, v70
	v_pk_mul_f32 v[188:189], v[188:189], v[68:69] op_sel:[0,1] op_sel_hi:[1,0]
	v_mov_b32_e32 v194, v78
	v_mov_b32_e32 v195, v84
	v_mov_b32_e32 v76, v65
	v_pk_fma_f32 v[52:53], v[52:53], v[68:69], v[188:189]
	v_mov_b32_e32 v188, v82
	v_mov_b32_e32 v189, v80
	v_pk_mul_f32 v[194:195], v[194:195], v[66:67] op_sel:[0,1] op_sel_hi:[1,0]
	v_mov_b32_e32 v70, v75
	v_pk_mul_f32 v[64:65], v[76:77], v[68:69] op_sel:[0,1] op_sel_hi:[1,0]
	v_mov_b32_e32 v84, v79
	v_pk_fma_f32 v[188:189], v[188:189], v[66:67], v[194:195]
	v_pk_fma_f32 v[64:65], v[70:71], v[68:69], v[64:65]
	v_mov_b32_e32 v80, v83
	v_pk_mul_f32 v[70:71], v[84:85], v[66:67] op_sel:[0,1] op_sel_hi:[1,0]
	v_pk_add_f32 v[52:53], v[52:53], v[188:189]
	v_pk_fma_f32 v[70:71], v[80:81], v[66:67], v[70:71]
	v_pk_add_f32 v[52:53], v[52:53], v[86:87]
	v_pk_add_f32 v[64:65], v[64:65], v[70:71]
	v_and_b32_sdwa v71, v52, v129 dst_sel:DWORD dst_unused:UNUSED_PAD src0_sel:WORD_1 src1_sel:DWORD
	v_pk_add_f32 v[64:65], v[64:65], v[180:181]
	v_add3_u32 v74, v52, v71, s4
	v_and_b32_sdwa v71, v65, v129 dst_sel:DWORD dst_unused:UNUSED_PAD src0_sel:WORD_1 src1_sel:DWORD
	v_and_b32_sdwa v75, v64, v129 dst_sel:DWORD dst_unused:UNUSED_PAD src0_sel:WORD_1 src1_sel:DWORD
	v_and_b32_sdwa v70, v53, v129 dst_sel:DWORD dst_unused:UNUSED_PAD src0_sel:WORD_1 src1_sel:DWORD
	v_add3_u32 v71, v65, v71, s4
	v_add3_u32 v75, v64, v75, s4
	v_add3_u32 v70, v53, v70, s4
	v_and_b32_e32 v71, 0xffff0000, v71
	v_and_b32_e32 v75, 0xffff0000, v75
	v_or_b32_sdwa v71, v71, v70 dst_sel:DWORD dst_unused:UNUSED_PAD src0_sel:DWORD src1_sel:WORD_1
	v_or_b32_sdwa v70, v75, v74 dst_sel:DWORD dst_unused:UNUSED_PAD src0_sel:DWORD src1_sel:WORD_1
	global_store_dwordx2 v[32:33], v[70:71], off offset:512
	v_pk_mul_f32 v[70:71], v[64:65], v[64:65]
	s_nop 0
	v_pk_fma_f32 v[78:79], v[52:53], v[52:53], v[70:71]
	v_cvt_pk_f32_fp8_e32 v[70:71], v165
	v_cvt_pk_f32_fp8_sdwa v[80:81], v169 src0_sel:WORD_1
	v_cvt_pk_f32_fp8_sdwa v[74:75], v165 src0_sel:WORD_1
	v_cvt_pk_f32_fp8_e32 v[76:77], v169
	v_cvt_pk_f32_fp8_e32 v[82:83], v171
	s_waitcnt vmcnt(63)
	v_cvt_pk_f32_fp8_e32 v[86:87], v172
	v_cvt_pk_f32_fp8_sdwa v[172:173], v172 src0_sel:WORD_1
	v_cvt_pk_f32_fp8_sdwa v[84:85], v171 src0_sel:WORD_1
	v_mov_b32_e32 v194, v70
	v_mov_b32_e32 v195, v80
	v_lshlrev_b32_e32 v181, 16, v47
	v_lshlrev_b32_e32 v180, 16, v46
	v_and_b32_e32 v189, 0xffff0000, v47
	v_and_b32_e32 v188, 0xffff0000, v46
	v_mov_b32_e32 v46, v76
	v_mov_b32_e32 v47, v74
	v_pk_mul_f32 v[194:195], v[194:195], v[68:69] op_sel:[0,1] op_sel_hi:[1,0]
	v_mov_b32_e32 v200, v82
	v_mov_b32_e32 v201, v172
	v_mov_b32_e32 v80, v71
	v_pk_fma_f32 v[46:47], v[46:47], v[68:69], v[194:195]
	v_mov_b32_e32 v194, v86
	v_mov_b32_e32 v195, v84
	v_pk_mul_f32 v[200:201], v[200:201], v[66:67] op_sel:[0,1] op_sel_hi:[1,0]
	v_mov_b32_e32 v74, v77
	v_pk_mul_f32 v[70:71], v[80:81], v[68:69] op_sel:[0,1] op_sel_hi:[1,0]
	v_mov_b32_e32 v172, v83
	v_pk_fma_f32 v[194:195], v[194:195], v[66:67], v[200:201]
	v_pk_fma_f32 v[70:71], v[74:75], v[68:69], v[70:71]
	v_mov_b32_e32 v84, v87
	v_pk_mul_f32 v[74:75], v[172:173], v[66:67] op_sel:[0,1] op_sel_hi:[1,0]
	v_pk_add_f32 v[46:47], v[46:47], v[194:195]
	v_pk_fma_f32 v[74:75], v[84:85], v[66:67], v[74:75]
	v_pk_add_f32 v[46:47], v[46:47], v[180:181]
	v_pk_add_f32 v[70:71], v[70:71], v[74:75]
	v_and_b32_sdwa v75, v46, v129 dst_sel:DWORD dst_unused:UNUSED_PAD src0_sel:WORD_1 src1_sel:DWORD
	v_pk_add_f32 v[70:71], v[70:71], v[188:189]
	v_add3_u32 v76, v46, v75, s4
	v_and_b32_sdwa v75, v71, v129 dst_sel:DWORD dst_unused:UNUSED_PAD src0_sel:WORD_1 src1_sel:DWORD
	v_and_b32_sdwa v77, v70, v129 dst_sel:DWORD dst_unused:UNUSED_PAD src0_sel:WORD_1 src1_sel:DWORD
	v_and_b32_sdwa v74, v47, v129 dst_sel:DWORD dst_unused:UNUSED_PAD src0_sel:WORD_1 src1_sel:DWORD
	v_add3_u32 v75, v71, v75, s4
	v_add3_u32 v77, v70, v77, s4
	v_add3_u32 v74, v47, v74, s4
	v_and_b32_e32 v75, 0xffff0000, v75
	v_and_b32_e32 v77, 0xffff0000, v77
	v_or_b32_sdwa v75, v75, v74 dst_sel:DWORD dst_unused:UNUSED_PAD src0_sel:DWORD src1_sel:WORD_1
	v_or_b32_sdwa v74, v77, v76 dst_sel:DWORD dst_unused:UNUSED_PAD src0_sel:DWORD src1_sel:WORD_1
	global_store_dwordx2 v[32:33], v[74:75], off offset:1024
	v_pk_mul_f32 v[74:75], v[70:71], v[70:71]
	s_nop 0
	v_pk_fma_f32 v[82:83], v[46:47], v[46:47], v[74:75]
	v_cvt_pk_f32_fp8_e32 v[74:75], v88
	v_cvt_pk_f32_fp8_sdwa v[84:85], v89 src0_sel:WORD_1
	v_cvt_pk_f32_fp8_sdwa v[76:77], v88 src0_sel:WORD_1
	v_cvt_pk_f32_fp8_e32 v[80:81], v89
	v_cvt_pk_f32_fp8_e32 v[86:87], v163
	s_waitcnt vmcnt(63)
	v_cvt_pk_f32_fp8_e32 v[172:173], v164
	v_cvt_pk_f32_fp8_sdwa v[164:165], v164 src0_sel:WORD_1
	v_cvt_pk_f32_fp8_sdwa v[88:89], v163 src0_sel:WORD_1
	v_mov_b32_e32 v194, v74
	v_mov_b32_e32 v195, v84
	v_lshlrev_b32_e32 v181, 16, v43
	v_lshlrev_b32_e32 v180, 16, v42
	v_and_b32_e32 v189, 0xffff0000, v43
	v_and_b32_e32 v188, 0xffff0000, v42
	v_mov_b32_e32 v42, v80
	v_mov_b32_e32 v43, v76
	v_pk_mul_f32 v[194:195], v[194:195], v[68:69] op_sel:[0,1] op_sel_hi:[1,0]
	v_mov_b32_e32 v200, v86
	v_mov_b32_e32 v201, v164
	v_mov_b32_e32 v84, v75
	v_pk_fma_f32 v[42:43], v[42:43], v[68:69], v[194:195]
	v_mov_b32_e32 v194, v172
	v_mov_b32_e32 v195, v88
	v_pk_mul_f32 v[200:201], v[200:201], v[66:67] op_sel:[0,1] op_sel_hi:[1,0]
	v_mov_b32_e32 v76, v81
	v_pk_mul_f32 v[74:75], v[84:85], v[68:69] op_sel:[0,1] op_sel_hi:[1,0]
	v_mov_b32_e32 v164, v87
	v_pk_fma_f32 v[194:195], v[194:195], v[66:67], v[200:201]
	v_pk_fma_f32 v[74:75], v[76:77], v[68:69], v[74:75]
	v_mov_b32_e32 v88, v173
	v_pk_mul_f32 v[76:77], v[164:165], v[66:67] op_sel:[0,1] op_sel_hi:[1,0]
	v_pk_add_f32 v[42:43], v[42:43], v[194:195]
	v_pk_fma_f32 v[76:77], v[88:89], v[66:67], v[76:77]
	v_pk_add_f32 v[42:43], v[42:43], v[180:181]
	v_pk_add_f32 v[74:75], v[74:75], v[76:77]
	v_and_b32_sdwa v77, v42, v129 dst_sel:DWORD dst_unused:UNUSED_PAD src0_sel:WORD_1 src1_sel:DWORD
	v_pk_add_f32 v[74:75], v[74:75], v[188:189]
	v_add3_u32 v80, v42, v77, s4
	v_and_b32_sdwa v77, v75, v129 dst_sel:DWORD dst_unused:UNUSED_PAD src0_sel:WORD_1 src1_sel:DWORD
	v_and_b32_sdwa v81, v74, v129 dst_sel:DWORD dst_unused:UNUSED_PAD src0_sel:WORD_1 src1_sel:DWORD
	v_and_b32_sdwa v76, v43, v129 dst_sel:DWORD dst_unused:UNUSED_PAD src0_sel:WORD_1 src1_sel:DWORD
	v_add3_u32 v77, v75, v77, s4
	v_add3_u32 v81, v74, v81, s4
	v_add3_u32 v76, v43, v76, s4
	v_and_b32_e32 v77, 0xffff0000, v77
	v_and_b32_e32 v81, 0xffff0000, v81
	v_or_b32_sdwa v77, v77, v76 dst_sel:DWORD dst_unused:UNUSED_PAD src0_sel:DWORD src1_sel:WORD_1
	v_or_b32_sdwa v76, v81, v80 dst_sel:DWORD dst_unused:UNUSED_PAD src0_sel:DWORD src1_sel:WORD_1
	global_store_dwordx2 v[32:33], v[76:77], off offset:1536
	v_pk_mul_f32 v[76:77], v[74:75], v[74:75]
	s_nop 0
	v_pk_fma_f32 v[88:89], v[42:43], v[42:43], v[76:77]
	v_cvt_pk_f32_fp8_e32 v[76:77], v155
	v_cvt_pk_f32_fp8_sdwa v[86:87], v156 src0_sel:WORD_1
	v_cvt_pk_f32_fp8_sdwa v[80:81], v155 src0_sel:WORD_1
	v_cvt_pk_f32_fp8_e32 v[84:85], v156
	v_cvt_pk_f32_fp8_e32 v[164:165], v157
	s_waitcnt vmcnt(63)
	v_cvt_pk_f32_fp8_e32 v[172:173], v162
	v_cvt_pk_f32_fp8_sdwa v[162:163], v162 src0_sel:WORD_1
	v_cvt_pk_f32_fp8_sdwa v[156:157], v157 src0_sel:WORD_1
	v_mov_b32_e32 v194, v76
	v_mov_b32_e32 v195, v86
	v_lshlrev_b32_e32 v181, 16, v39
	v_lshlrev_b32_e32 v180, 16, v38
	v_and_b32_e32 v189, 0xffff0000, v39
	v_and_b32_e32 v188, 0xffff0000, v38
	v_mov_b32_e32 v38, v84
	v_mov_b32_e32 v39, v80
	v_pk_mul_f32 v[194:195], v[194:195], v[68:69] op_sel:[0,1] op_sel_hi:[1,0]
	v_mov_b32_e32 v200, v164
	v_mov_b32_e32 v201, v162
	v_mov_b32_e32 v86, v77
	v_pk_fma_f32 v[38:39], v[38:39], v[68:69], v[194:195]
	v_mov_b32_e32 v194, v172
	v_mov_b32_e32 v195, v156
	v_pk_mul_f32 v[200:201], v[200:201], v[66:67] op_sel:[0,1] op_sel_hi:[1,0]
	v_mov_b32_e32 v80, v85
	v_pk_mul_f32 v[76:77], v[86:87], v[68:69] op_sel:[0,1] op_sel_hi:[1,0]
	v_mov_b32_e32 v162, v165
	v_pk_fma_f32 v[194:195], v[194:195], v[66:67], v[200:201]
	v_pk_fma_f32 v[76:77], v[80:81], v[68:69], v[76:77]
	v_mov_b32_e32 v156, v173
	v_pk_mul_f32 v[80:81], v[162:163], v[66:67] op_sel:[0,1] op_sel_hi:[1,0]
	v_pk_add_f32 v[38:39], v[38:39], v[194:195]
	v_pk_fma_f32 v[80:81], v[156:157], v[66:67], v[80:81]
	v_pk_add_f32 v[38:39], v[38:39], v[180:181]
	v_pk_add_f32 v[76:77], v[76:77], v[80:81]
	v_and_b32_sdwa v81, v38, v129 dst_sel:DWORD dst_unused:UNUSED_PAD src0_sel:WORD_1 src1_sel:DWORD
	v_pk_add_f32 v[76:77], v[76:77], v[188:189]
	v_add3_u32 v84, v38, v81, s4
	v_and_b32_sdwa v81, v77, v129 dst_sel:DWORD dst_unused:UNUSED_PAD src0_sel:WORD_1 src1_sel:DWORD
	v_and_b32_sdwa v85, v76, v129 dst_sel:DWORD dst_unused:UNUSED_PAD src0_sel:WORD_1 src1_sel:DWORD
	v_and_b32_sdwa v80, v39, v129 dst_sel:DWORD dst_unused:UNUSED_PAD src0_sel:WORD_1 src1_sel:DWORD
	v_add3_u32 v81, v77, v81, s4
	v_add3_u32 v85, v76, v85, s4
	v_add3_u32 v80, v39, v80, s4
	v_and_b32_e32 v81, 0xffff0000, v81
	v_and_b32_e32 v85, 0xffff0000, v85
	v_or_b32_sdwa v81, v81, v80 dst_sel:DWORD dst_unused:UNUSED_PAD src0_sel:DWORD src1_sel:WORD_1
	v_or_b32_sdwa v80, v85, v84 dst_sel:DWORD dst_unused:UNUSED_PAD src0_sel:DWORD src1_sel:WORD_1
	global_store_dwordx2 v[32:33], v[80:81], off offset:2048
	v_pk_mul_f32 v[80:81], v[76:77], v[76:77]
	s_nop 0
	v_pk_fma_f32 v[156:157], v[38:39], v[38:39], v[80:81]
	v_cvt_pk_f32_fp8_e32 v[80:81], v147
	v_cvt_pk_f32_fp8_sdwa v[162:163], v148 src0_sel:WORD_1
	v_cvt_pk_f32_fp8_sdwa v[84:85], v147 src0_sel:WORD_1
	v_cvt_pk_f32_fp8_e32 v[86:87], v148
	v_cvt_pk_f32_fp8_e32 v[164:165], v153
	s_waitcnt vmcnt(63)
	v_cvt_pk_f32_fp8_e32 v[180:181], v154
	v_cvt_pk_f32_fp8_sdwa v[154:155], v154 src0_sel:WORD_1
	v_cvt_pk_f32_fp8_sdwa v[172:173], v153 src0_sel:WORD_1
	v_mov_b32_e32 v200, v80
	v_mov_b32_e32 v201, v162
	v_lshlrev_b32_e32 v189, 16, v37
	v_lshlrev_b32_e32 v188, 16, v36
	v_and_b32_e32 v195, 0xffff0000, v37
	v_and_b32_e32 v194, 0xffff0000, v36
	v_mov_b32_e32 v36, v86
	v_mov_b32_e32 v37, v84
	v_pk_mul_f32 v[200:201], v[200:201], v[68:69] op_sel:[0,1] op_sel_hi:[1,0]
	v_mov_b32_e32 v202, v164
	v_mov_b32_e32 v203, v154
	v_mov_b32_e32 v162, v81
	v_pk_fma_f32 v[36:37], v[36:37], v[68:69], v[200:201]
	v_mov_b32_e32 v200, v180
	v_mov_b32_e32 v201, v172
	v_pk_mul_f32 v[202:203], v[202:203], v[66:67] op_sel:[0,1] op_sel_hi:[1,0]
	v_mov_b32_e32 v84, v87
	v_pk_mul_f32 v[80:81], v[162:163], v[68:69] op_sel:[0,1] op_sel_hi:[1,0]
	v_mov_b32_e32 v154, v165
	v_pk_fma_f32 v[200:201], v[200:201], v[66:67], v[202:203]
	v_pk_fma_f32 v[80:81], v[84:85], v[68:69], v[80:81]
	v_mov_b32_e32 v172, v181
	v_pk_mul_f32 v[84:85], v[154:155], v[66:67] op_sel:[0,1] op_sel_hi:[1,0]
	v_pk_add_f32 v[36:37], v[36:37], v[200:201]
	v_pk_fma_f32 v[84:85], v[172:173], v[66:67], v[84:85]
	v_pk_add_f32 v[36:37], v[36:37], v[188:189]
	v_pk_add_f32 v[80:81], v[80:81], v[84:85]
	v_and_b32_sdwa v85, v36, v129 dst_sel:DWORD dst_unused:UNUSED_PAD src0_sel:WORD_1 src1_sel:DWORD
	v_pk_add_f32 v[80:81], v[80:81], v[194:195]
	v_add3_u32 v86, v36, v85, s4
	v_and_b32_sdwa v85, v81, v129 dst_sel:DWORD dst_unused:UNUSED_PAD src0_sel:WORD_1 src1_sel:DWORD
	v_and_b32_sdwa v87, v80, v129 dst_sel:DWORD dst_unused:UNUSED_PAD src0_sel:WORD_1 src1_sel:DWORD
	v_and_b32_sdwa v84, v37, v129 dst_sel:DWORD dst_unused:UNUSED_PAD src0_sel:WORD_1 src1_sel:DWORD
	v_add3_u32 v85, v81, v85, s4
	v_add3_u32 v87, v80, v87, s4
	v_add3_u32 v84, v37, v84, s4
	v_and_b32_e32 v85, 0xffff0000, v85
	v_and_b32_e32 v87, 0xffff0000, v87
	v_or_b32_sdwa v85, v85, v84 dst_sel:DWORD dst_unused:UNUSED_PAD src0_sel:DWORD src1_sel:WORD_1
	v_or_b32_sdwa v84, v87, v86 dst_sel:DWORD dst_unused:UNUSED_PAD src0_sel:DWORD src1_sel:WORD_1
	global_store_dwordx2 v[32:33], v[84:85], off offset:2560
	v_pk_mul_f32 v[84:85], v[80:81], v[80:81]
	s_nop 0
	v_pk_fma_f32 v[154:155], v[36:37], v[36:37], v[84:85]
	v_cvt_pk_f32_fp8_e32 v[86:87], v140
	v_cvt_pk_f32_fp8_sdwa v[172:173], v143 src0_sel:WORD_1
	v_cvt_pk_f32_fp8_sdwa v[162:163], v140 src0_sel:WORD_1
	v_cvt_pk_f32_fp8_e32 v[164:165], v143
	v_cvt_pk_f32_fp8_e32 v[180:181], v145
	s_waitcnt vmcnt(63)
	v_cvt_pk_f32_fp8_e32 v[194:195], v146
	v_cvt_pk_f32_fp8_sdwa v[146:147], v146 src0_sel:WORD_1
	v_cvt_pk_f32_fp8_sdwa v[188:189], v145 src0_sel:WORD_1
	v_mov_b32_e32 v202, v86
	v_mov_b32_e32 v203, v172
	v_mov_b32_e32 v200, v164
	v_mov_b32_e32 v201, v162
	v_pk_mul_f32 v[202:203], v[202:203], v[68:69] op_sel:[0,1] op_sel_hi:[1,0]
	v_mov_b32_e32 v204, v180
	v_mov_b32_e32 v205, v146
	v_pk_fma_f32 v[200:201], v[200:201], v[68:69], v[202:203]
	v_mov_b32_e32 v202, v194
	v_mov_b32_e32 v203, v188
	v_pk_mul_f32 v[204:205], v[204:205], v[66:67] op_sel:[0,1] op_sel_hi:[1,0]
	v_mov_b32_e32 v172, v87
	v_mov_b32_e32 v146, v181
	v_pk_fma_f32 v[202:203], v[202:203], v[66:67], v[204:205]
	v_mov_b32_e32 v162, v165
	v_pk_mul_f32 v[86:87], v[172:173], v[68:69] op_sel:[0,1] op_sel_hi:[1,0]
	v_mov_b32_e32 v188, v195
	v_pk_mul_f32 v[146:147], v[146:147], v[66:67] op_sel:[0,1] op_sel_hi:[1,0]
	v_lshlrev_b32_e32 v85, 16, v31
	v_lshlrev_b32_e32 v84, 16, v30
	v_pk_add_f32 v[200:201], v[200:201], v[202:203]
	v_pk_fma_f32 v[86:87], v[162:163], v[68:69], v[86:87]
	v_pk_fma_f32 v[146:147], v[188:189], v[66:67], v[146:147]
	v_and_b32_e32 v31, 0xffff0000, v31
	v_and_b32_e32 v30, 0xffff0000, v30
	v_pk_add_f32 v[84:85], v[200:201], v[84:85]
	v_pk_add_f32 v[86:87], v[86:87], v[146:147]
	s_nop 0
	v_pk_add_f32 v[86:87], v[86:87], v[30:31]
	v_and_b32_sdwa v31, v84, v129 dst_sel:DWORD dst_unused:UNUSED_PAD src0_sel:WORD_1 src1_sel:DWORD
	v_add3_u32 v140, v84, v31, s4
	v_and_b32_sdwa v31, v87, v129 dst_sel:DWORD dst_unused:UNUSED_PAD src0_sel:WORD_1 src1_sel:DWORD
	v_and_b32_sdwa v143, v86, v129 dst_sel:DWORD dst_unused:UNUSED_PAD src0_sel:WORD_1 src1_sel:DWORD
	v_and_b32_sdwa v30, v85, v129 dst_sel:DWORD dst_unused:UNUSED_PAD src0_sel:WORD_1 src1_sel:DWORD
	v_add3_u32 v31, v87, v31, s4
	v_add3_u32 v143, v86, v143, s4
	v_add3_u32 v30, v85, v30, s4
	v_and_b32_e32 v31, 0xffff0000, v31
	v_and_b32_e32 v143, 0xffff0000, v143
	v_or_b32_sdwa v31, v31, v30 dst_sel:DWORD dst_unused:UNUSED_PAD src0_sel:DWORD src1_sel:WORD_1
	v_or_b32_sdwa v30, v143, v140 dst_sel:DWORD dst_unused:UNUSED_PAD src0_sel:DWORD src1_sel:WORD_1
	global_store_dwordx2 v[32:33], v[30:31], off offset:3072
	v_pk_mul_f32 v[30:31], v[86:87], v[86:87]
	s_nop 0
	v_pk_fma_f32 v[146:147], v[84:85], v[84:85], v[30:31]
	v_cvt_pk_f32_fp8_e32 v[30:31], v132
	v_cvt_pk_f32_fp8_sdwa v[172:173], v135 src0_sel:WORD_1
	v_cvt_pk_f32_fp8_sdwa v[162:163], v132 src0_sel:WORD_1
	v_cvt_pk_f32_fp8_e32 v[164:165], v135
	v_cvt_pk_f32_fp8_e32 v[180:181], v137
	s_waitcnt vmcnt(63)
	v_cvt_pk_f32_fp8_sdwa v[200:201], v138 src0_sel:WORD_1
	v_cvt_pk_f32_fp8_sdwa v[188:189], v137 src0_sel:WORD_1
	v_cvt_pk_f32_fp8_e32 v[194:195], v138
	v_mov_b32_e32 v206, v30
	v_mov_b32_e32 v207, v172
	v_lshlrev_b32_e32 v203, 16, v27
	v_lshlrev_b32_e32 v202, 16, v26
	v_and_b32_e32 v205, 0xffff0000, v27
	v_and_b32_e32 v204, 0xffff0000, v26
	v_mov_b32_e32 v26, v164
	v_mov_b32_e32 v27, v162
	v_pk_mul_f32 v[206:207], v[206:207], v[68:69] op_sel:[0,1] op_sel_hi:[1,0]
	v_mov_b32_e32 v208, v180
	v_mov_b32_e32 v209, v200
	v_mov_b32_e32 v172, v31
	v_pk_fma_f32 v[26:27], v[26:27], v[68:69], v[206:207]
	v_mov_b32_e32 v206, v194
	v_mov_b32_e32 v207, v188
	v_pk_mul_f32 v[208:209], v[208:209], v[66:67] op_sel:[0,1] op_sel_hi:[1,0]
	v_mov_b32_e32 v162, v165
	v_pk_mul_f32 v[30:31], v[172:173], v[68:69] op_sel:[0,1] op_sel_hi:[1,0]
	v_mov_b32_e32 v200, v181
	v_pk_fma_f32 v[206:207], v[206:207], v[66:67], v[208:209]
	v_pk_fma_f32 v[30:31], v[162:163], v[68:69], v[30:31]
	v_mov_b32_e32 v188, v195
	v_pk_mul_f32 v[68:69], v[200:201], v[66:67] op_sel:[0,1] op_sel_hi:[1,0]
	v_pk_add_f32 v[26:27], v[26:27], v[206:207]
	v_pk_fma_f32 v[66:67], v[188:189], v[66:67], v[68:69]
	v_pk_add_f32 v[26:27], v[26:27], v[202:203]
	v_pk_add_f32 v[30:31], v[30:31], v[66:67]
	v_and_b32_sdwa v67, v26, v129 dst_sel:DWORD dst_unused:UNUSED_PAD src0_sel:WORD_1 src1_sel:DWORD
	v_pk_add_f32 v[30:31], v[30:31], v[204:205]
	v_add3_u32 v68, v26, v67, s4
	v_and_b32_sdwa v67, v31, v129 dst_sel:DWORD dst_unused:UNUSED_PAD src0_sel:WORD_1 src1_sel:DWORD
	v_and_b32_sdwa v69, v30, v129 dst_sel:DWORD dst_unused:UNUSED_PAD src0_sel:WORD_1 src1_sel:DWORD
	v_and_b32_sdwa v66, v27, v129 dst_sel:DWORD dst_unused:UNUSED_PAD src0_sel:WORD_1 src1_sel:DWORD
	v_add3_u32 v67, v31, v67, s4
	v_add3_u32 v69, v30, v69, s4
	v_add3_u32 v66, v27, v66, s4
	v_and_b32_e32 v67, 0xffff0000, v67
	v_and_b32_e32 v69, 0xffff0000, v69
	v_or_b32_sdwa v67, v67, v66 dst_sel:DWORD dst_unused:UNUSED_PAD src0_sel:DWORD src1_sel:WORD_1
	v_or_b32_sdwa v66, v69, v68 dst_sel:DWORD dst_unused:UNUSED_PAD src0_sel:DWORD src1_sel:WORD_1
	global_store_dwordx2 v[32:33], v[66:67], off offset:3584
	v_add_f32_e32 v66, v78, v79
	v_add_f32_e32 v67, v72, v73
	v_add_f32_e32 v66, v67, v66
	v_add_f32_e32 v67, v82, v83
	v_add_f32_e32 v66, v66, v67
	v_add_f32_e32 v67, v88, v89
	v_add_f32_e32 v66, v66, v67
	v_add_f32_e32 v67, v156, v157
	v_pk_mul_f32 v[32:33], v[30:31], v[30:31]
	v_add_f32_e32 v66, v66, v67
	v_add_f32_e32 v67, v154, v155
	v_pk_fma_f32 v[32:33], v[26:27], v[26:27], v[32:33]
	v_add_f32_e32 v66, v66, v67
	v_add_f32_e32 v67, v146, v147
	v_add_f32_e32 v66, v66, v67
	v_add_f32_e32 v32, v32, v33
	v_add_f32_e32 v32, v66, v32
	v_mov_b64_e32 v[66:67], v[212:213]
	v_mov_b64_e32 v[68:69], v[214:215]
	ds_bpermute_b32 v33, v1, v32
	s_waitcnt lgkmcnt(0)
	v_add_f32_e32 v32, v32, v33
	ds_bpermute_b32 v33, v90, v32
	s_waitcnt lgkmcnt(0)
	v_add_f32_e32 v32, v32, v33
	ds_bpermute_b32 v33, v91, v32
	s_waitcnt lgkmcnt(0)
	v_add_f32_e32 v32, v32, v33
	ds_bpermute_b32 v33, v92, v32
	s_waitcnt lgkmcnt(0)
	v_add_f32_e32 v32, v32, v33
	ds_bpermute_b32 v33, v93, v32
	s_waitcnt lgkmcnt(0)
	v_add_f32_e32 v32, v32, v33
	ds_bpermute_b32 v33, v94, v32
	s_waitcnt lgkmcnt(0)
	v_add_f32_e32 v32, v32, v33
	v_fmamk_f32 v32, v32, 0x3a000000, v127
	v_mul_f32_e32 v33, 0x4f800000, v32
	v_cmp_gt_f32_e32 vcc, s19, v32
	s_nop 1
	v_cndmask_b32_e32 v32, v32, v33, vcc
	v_sqrt_f32_e32 v33, v32
	s_nop 0
	v_add_u32_e32 v72, -1, v33
	v_add_u32_e32 v73, 1, v33
	v_fma_f32 v78, -v72, v33, v32
	v_fma_f32 v79, -v73, v33, v32
	v_cmp_ge_f32_e64 s[8:9], 0, v78
	s_nop 1
	v_cndmask_b32_e64 v33, v33, v72, s[8:9]
	v_cmp_lt_f32_e64 s[8:9], 0, v79
	s_nop 1
	v_cndmask_b32_e64 v33, v33, v73, s[8:9]
	v_mul_f32_e32 v72, 0x37800000, v33
	v_cndmask_b32_e32 v33, v33, v72, vcc
	v_cmp_class_f32_e32 vcc, v32, v128
	v_mov_b32_e32 v73, 0
	s_nop 0
	v_cndmask_b32_e32 v32, v33, v32, vcc
	v_div_scale_f32 v33, s[0:1], v32, v32, 1.0
	v_rcp_f32_e32 v72, v33
	v_div_scale_f32 v78, vcc, 1.0, v32, 1.0
	v_fma_f32 v79, -v33, v72, 1.0
	v_fmac_f32_e32 v72, v79, v72
	v_mul_f32_e32 v79, v78, v72
	v_fma_f32 v82, -v33, v79, v78
	v_fmac_f32_e32 v79, v82, v72
	v_fma_f32 v33, -v33, v79, v78
	v_div_fmas_f32 v33, v33, v72, v79
	v_div_fixup_f32 v72, v33, v32, 1.0
	v_mul_f32_e32 v32, v72, v56
	v_mul_f32_e32 v33, v72, v60

	v_mul_f32_e32 v32, v66, v32
	v_mul_f32_e32 v33, v67, v33
	v_cvt_pk_fp8_f32 v73, v32, v33
	v_mul_f32_e32 v56, v72, v57
	v_mul_f32_e32 v32, v72, v61
	v_mul_f32_e32 v33, v68, v56
	v_mul_f32_e32 v32, v69, v32
	v_cvt_pk_fp8_f32 v73, v33, v32 op_sel:[0,0,1]
	v_mul_f32_e32 v33, v72, v52
	v_mul_f32_e32 v52, v72, v64
	v_mov_b32_e32 v32, 0
	global_store_dword v[50:51], v73, off offset:2048
	v_mov_b64_e32 v[66:67], v[216:217]
	v_mov_b64_e32 v[68:69], v[218:219]
	v_mul_f32_e32 v53, v72, v53
	v_mul_f32_e32 v47, v72, v47
	v_mul_f32_e32 v43, v72, v43
	v_mul_f32_e32 v39, v72, v39
	v_mul_f32_e32 v37, v72, v37
	v_mul_f32_e32 v26, v72, v26
	v_mul_f32_e32 v30, v72, v30
	ds_bpermute_b32 v56, v111, v130
	v_mul_f32_e32 v27, v72, v27
	s_waitcnt vmcnt(41)
	v_cvt_pk_f32_fp8_e32 v[78:79], v190
	s_waitcnt lgkmcnt(0)
	v_ashrrev_i32_e32 v57, 31, v56
	v_lshlrev_b64 v[56:57], 11, v[56:57]

	v_mul_f32_e32 v33, v66, v33
	v_mul_f32_e32 v52, v67, v52
	v_cvt_pk_fp8_f32 v32, v33, v52
	v_mul_f32_e32 v33, v72, v65
	v_mul_f32_e32 v52, v68, v53
	v_mul_f32_e32 v33, v69, v33
	v_cvt_pk_fp8_f32 v32, v52, v33 op_sel:[0,0,1]
	v_mul_f32_e32 v33, v72, v46
	v_mul_f32_e32 v46, v72, v70
	v_mov_b32_e32 v68, 0
	global_store_dword v[50:51], v32, off offset:2304
	v_mov_b64_e32 v[64:65], v[220:221]
	v_mov_b64_e32 v[66:67], v[222:223]
	v_mov_b32_e32 v32, 0
	v_add_co_u32_e32 v52, vcc, s28, v20
	ds_bpermute_b32 v69, v104, v19
	s_nop 0
	v_addc_co_u32_e32 v53, vcc, 0, v21, vcc
	v_add_co_u32_e32 v60, vcc, s31, v20

	v_mul_f32_e32 v33, v64, v33
	v_mul_f32_e32 v46, v65, v46
	v_cvt_pk_fp8_f32 v32, v33, v46
	v_mul_f32_e32 v33, v72, v71
	v_mul_f32_e32 v46, v66, v47
	v_mul_f32_e32 v33, v67, v33
	v_cvt_pk_fp8_f32 v32, v46, v33 op_sel:[0,0,1]
	v_mul_f32_e32 v33, v72, v42
	v_mul_f32_e32 v42, v72, v74
	ds_bpermute_b32 v46, v110, v130
	global_store_dword v[50:51], v32, off offset:2560
	v_mov_b64_e32 v[64:65], v[224:225]
	v_mov_b64_e32 v[66:67], v[226:227]
	v_mov_b32_e32 v32, 0
	v_addc_co_u32_e32 v61, vcc, 0, v21, vcc
	s_waitcnt lgkmcnt(0)
	v_ashrrev_i32_e32 v47, 31, v46
	v_lshlrev_b64 v[46:47], 11, v[46:47]
	s_waitcnt vmcnt(27)
	v_cvt_pk_f32_fp8_e32 v[70:71], v193
	v_mov_b32_e32 v82, v70

	v_mul_f32_e32 v33, v64, v33
	v_mul_f32_e32 v42, v65, v42
	v_cvt_pk_fp8_f32 v32, v33, v42
	v_mul_f32_e32 v33, v72, v75
	v_mul_f32_e32 v42, v66, v43
	v_mul_f32_e32 v33, v67, v33
	v_cvt_pk_fp8_f32 v32, v42, v33 op_sel:[0,0,1]
	v_mul_f32_e32 v33, v72, v38
	v_mul_f32_e32 v38, v72, v76
	v_mul_f32_e32 v42, v72, v86
	global_store_dword v[50:51], v32, off offset:2816
	v_mov_b64_e32 v[64:65], v[228:229]
	v_mov_b64_e32 v[66:67], v[230:231]
	v_mov_b32_e32 v32, 0
	v_mul_f32_e32 v43, v72, v85
	v_cvt_pk_f32_fp8_e32 v[74:75], v191
	v_mov_b32_e32 v86, v74

	v_mul_f32_e32 v33, v64, v33
	v_mul_f32_e32 v38, v65, v38
	v_cvt_pk_fp8_f32 v32, v33, v38
	v_mul_f32_e32 v33, v72, v77
	v_mul_f32_e32 v38, v66, v39
	v_mul_f32_e32 v33, v67, v33
	v_cvt_pk_fp8_f32 v32, v38, v33 op_sel:[0,0,1]
	v_mul_f32_e32 v33, v72, v36
	v_mul_f32_e32 v36, v72, v80
	v_cvt_pk_f32_fp8_sdwa v[76:77], v191 src0_sel:WORD_1
	global_store_dword v[50:51], v32, off offset:3072
	v_mov_b64_e32 v[64:65], v[232:233]
	v_mov_b64_e32 v[66:67], v[234:235]
	v_mov_b32_e32 v32, 0

	v_mul_f32_e32 v33, v64, v33
	v_mul_f32_e32 v36, v65, v36
	v_cvt_pk_fp8_f32 v32, v33, v36
	v_mul_f32_e32 v33, v72, v81
	v_mul_f32_e32 v36, v66, v37
	v_mul_f32_e32 v33, v67, v33
	v_cvt_pk_fp8_f32 v32, v36, v33 op_sel:[0,0,1]
	v_mul_f32_e32 v33, v72, v84
	v_lshl_add_u64 v[66:67], v[4:5], 0, v[56:57]
	v_cvt_pk_f32_fp8_sdwa v[80:81], v190 src0_sel:WORD_1
	global_store_dword v[50:51], v32, off offset:3328
	v_mov_b64_e32 v[36:37], v[236:237]
	v_mov_b64_e32 v[38:39], v[238:239]
	v_mov_b32_e32 v32, 0

	v_mul_f32_e32 v33, v36, v33
	v_mul_f32_e32 v36, v37, v42
	v_cvt_pk_fp8_f32 v32, v33, v36
	v_mul_f32_e32 v33, v72, v87
	v_mul_f32_e32 v36, v38, v43
	v_mul_f32_e32 v33, v39, v33
	v_cvt_pk_fp8_f32 v32, v36, v33 op_sel:[0,0,1]
	ds_bpermute_b32 v42, v109, v130
	v_mov_b32_e32 v87, v80
	v_mov_b32_e32 v80, v75
	global_store_dword v[50:51], v32, off offset:3584
	v_mov_b64_e32 v[36:37], v[240:241]
	v_mov_b64_e32 v[38:39], v[242:243]
	ds_bpermute_b32 v32, v108, v130
	s_waitcnt lgkmcnt(1)
	v_ashrrev_i32_e32 v43, 31, v42
	v_lshlrev_b64 v[42:43], 11, v[42:43]
	s_waitcnt lgkmcnt(0)
	v_ashrrev_i32_e32 v33, 31, v32
	v_lshlrev_b64 v[32:33], 11, v[32:33]
	v_lshl_add_u64 v[64:65], v[4:5], 0, v[32:33]

	v_mul_f32_e32 v26, v36, v26
	v_mul_f32_e32 v30, v37, v30
	v_cvt_pk_fp8_f32 v68, v26, v30
	v_mul_f32_e32 v26, v72, v31
	v_mul_f32_e32 v27, v38, v27
	v_mul_f32_e32 v26, v39, v26
	v_cvt_pk_fp8_f32 v68, v27, v26 op_sel:[0,0,1]
	v_lshl_add_u64 v[30:31], v[4:5], 0, v[42:43]
	v_lshl_add_u64 v[38:39], v[4:5], 0, v[46:47]
	v_cvt_pk_f32_fp8_sdwa v[72:73], v193 src0_sel:WORD_1
	global_store_dword v[50:51], v68, off offset:3840
	global_load_dwordx2 v[56:57], v[52:53], off offset:512
	s_nop 0
	global_load_dwordx2 v[50:51], v[52:53], off offset:1024
	global_load_dwordx2 v[46:47], v[52:53], off offset:1536
	global_load_dwordx2 v[42:43], v[52:53], off offset:2048
	global_load_dwordx2 v[36:37], v[52:53], off offset:2560
	global_load_dwordx2 v[32:33], v[52:53], off offset:3072
	global_load_dwordx2 v[26:27], v[52:53], off offset:3584
	global_load_dword v192, v[64:65], off
	global_load_dword v185, v[64:65], off offset:256
	global_load_dword v177, v[64:65], off offset:512
	global_load_dword v169, v[64:65], off offset:768
	global_load_dword v162, v[64:65], off offset:1024
	global_load_dword v154, v[64:65], off offset:1280
	global_load_dword v145, v[64:65], off offset:1536
	global_load_dword v132, v[64:65], off offset:1792
	global_load_dword v194, v[30:31], off
	global_load_dword v187, v[30:31], off offset:256
	global_load_dword v179, v[30:31], off offset:512
	global_load_dword v171, v[30:31], off offset:768
	global_load_dword v163, v[30:31], off offset:1024
	global_load_dword v155, v[30:31], off offset:1280
	global_load_dword v146, v[30:31], off offset:1536
	global_load_dword v135, v[30:31], off offset:1792
	global_load_dword v195, v[38:39], off
	global_load_dword v188, v[38:39], off offset:256
	global_load_dword v180, v[38:39], off offset:512
	global_load_dword v172, v[38:39], off offset:768
	global_load_dword v164, v[38:39], off offset:1024
	global_load_dword v156, v[38:39], off offset:1280
	global_load_dword v147, v[38:39], off offset:1536
	global_load_dword v137, v[38:39], off offset:1792
	global_load_dword v197, v[66:67], off
	global_load_dwordx2 v[64:65], v[60:61], off offset:-4096
	global_load_dword v189, v[66:67], off offset:256
	global_load_dword v181, v[66:67], off offset:512
	global_load_dword v173, v[66:67], off offset:768
	global_load_dword v165, v[66:67], off offset:1024
	global_load_dword v157, v[66:67], off offset:1280
	global_load_dword v148, v[66:67], off offset:1536
	global_load_dword v138, v[66:67], off offset:1792
	ds_bpermute_b32 v68, v105, v19
	s_waitcnt vmcnt(63)
	v_cvt_pk_f32_fp8_e32 v[30:31], v196
	ds_bpermute_b32 v67, v106, v19
	ds_bpermute_b32 v66, v107, v19
	v_cvt_pk_f32_fp8_sdwa v[52:53], v196 src0_sel:WORD_1
	v_mov_b32_e32 v84, v30
	v_mov_b32_e32 v85, v72
	v_mov_b32_e32 v72, v31
	v_mov_b32_e32 v83, v52
	s_waitcnt lgkmcnt(2)
	v_pk_mul_f32 v[84:85], v[84:85], v[68:69] op_sel:[0,1] op_sel_hi:[1,0]
	v_mov_b32_e32 v52, v71
	v_pk_mul_f32 v[30:31], v[72:73], v[68:69] op_sel:[0,1] op_sel_hi:[1,0]
	v_pk_fma_f32 v[82:83], v[82:83], v[68:69], v[84:85]
	v_mov_b32_e32 v85, v76
	v_pk_fma_f32 v[30:31], v[52:53], v[68:69], v[30:31]
	v_mov_b32_e32 v76, v79
	s_waitcnt lgkmcnt(0)
	v_pk_mul_f32 v[52:53], v[80:81], v[66:67] op_sel:[0,1] op_sel_hi:[1,0]
	v_mov_b32_e32 v84, v78
	v_pk_mul_f32 v[86:87], v[86:87], v[66:67] op_sel:[0,1] op_sel_hi:[1,0]
	v_pk_fma_f32 v[52:53], v[76:77], v[66:67], v[52:53]
	s_waitcnt vmcnt(56)
	v_lshlrev_b32_e32 v39, 16, v63
	v_lshlrev_b32_e32 v38, 16, v62
	v_and_b32_e32 v63, 0xffff0000, v63
	v_and_b32_e32 v62, 0xffff0000, v62
	v_pk_fma_f32 v[84:85], v[84:85], v[66:67], v[86:87]
	v_pk_add_f32 v[30:31], v[30:31], v[52:53]
	v_pk_add_f32 v[82:83], v[82:83], v[84:85]
	v_pk_add_f32 v[52:53], v[30:31], v[62:63]
	v_pk_add_f32 v[38:39], v[82:83], v[38:39]
	v_and_b32_sdwa v62, v53, v129 dst_sel:DWORD dst_unused:UNUSED_PAD src0_sel:WORD_1 src1_sel:DWORD
	v_and_b32_sdwa v30, v39, v129 dst_sel:DWORD dst_unused:UNUSED_PAD src0_sel:WORD_1 src1_sel:DWORD
	v_and_b32_sdwa v63, v52, v129 dst_sel:DWORD dst_unused:UNUSED_PAD src0_sel:WORD_1 src1_sel:DWORD
	v_add3_u32 v62, v53, v62, s4
	v_add_co_u32_e32 v72, vcc, s29, v20
	v_and_b32_sdwa v31, v38, v129 dst_sel:DWORD dst_unused:UNUSED_PAD src0_sel:WORD_1 src1_sel:DWORD
	v_add3_u32 v30, v39, v30, s4
	v_add3_u32 v63, v52, v63, s4
	v_and_b32_e32 v62, 0xffff0000, v62
	v_addc_co_u32_e32 v73, vcc, 0, v21, vcc
	v_add3_u32 v31, v38, v31, s4
	v_and_b32_e32 v70, 0xffff0000, v63
	v_or_b32_sdwa v63, v62, v30 dst_sel:DWORD dst_unused:UNUSED_PAD src0_sel:DWORD src1_sel:WORD_1
	v_add_co_u32_e32 v30, vcc, s33, v20
	v_or_b32_sdwa v62, v70, v31 dst_sel:DWORD dst_unused:UNUSED_PAD src0_sel:DWORD src1_sel:WORD_1
	s_nop 0
	v_addc_co_u32_e32 v31, vcc, 0, v21, vcc
	global_store_dwordx2 v[30:31], v[62:63], off offset:-4096
	v_pk_mul_f32 v[62:63], v[52:53], v[52:53]
	s_nop 0
	v_pk_fma_f32 v[74:75], v[38:39], v[38:39], v[62:63]
	v_cvt_pk_f32_fp8_e32 v[62:63], v186
	v_cvt_pk_f32_fp8_sdwa v[78:79], v184 src0_sel:WORD_1
	v_cvt_pk_f32_fp8_sdwa v[70:71], v186 src0_sel:WORD_1
	v_cvt_pk_f32_fp8_e32 v[76:77], v184
	v_cvt_pk_f32_fp8_e32 v[80:81], v183
	v_cvt_pk_f32_fp8_sdwa v[86:87], v182 src0_sel:WORD_1
	v_cvt_pk_f32_fp8_sdwa v[82:83], v183 src0_sel:WORD_1
	v_cvt_pk_f32_fp8_e32 v[84:85], v182
	v_mov_b32_e32 v190, v62
	v_mov_b32_e32 v191, v78
	v_lshlrev_b32_e32 v89, 16, v59
	v_lshlrev_b32_e32 v88, 16, v58
	v_and_b32_e32 v183, 0xffff0000, v59
	v_and_b32_e32 v182, 0xffff0000, v58
	v_mov_b32_e32 v58, v76
	v_mov_b32_e32 v59, v70
	v_pk_mul_f32 v[190:191], v[190:191], v[68:69] op_sel:[0,1] op_sel_hi:[1,0]
	v_mov_b32_e32 v200, v80
	v_mov_b32_e32 v201, v86
	v_mov_b32_e32 v78, v63
	v_pk_fma_f32 v[58:59], v[58:59], v[68:69], v[190:191]
	v_mov_b32_e32 v190, v84
	v_mov_b32_e32 v191, v82
	v_pk_mul_f32 v[200:201], v[200:201], v[66:67] op_sel:[0,1] op_sel_hi:[1,0]
	v_mov_b32_e32 v70, v77
	v_pk_mul_f32 v[62:63], v[78:79], v[68:69] op_sel:[0,1] op_sel_hi:[1,0]
	v_mov_b32_e32 v86, v81
	v_pk_fma_f32 v[190:191], v[190:191], v[66:67], v[200:201]
	v_pk_fma_f32 v[62:63], v[70:71], v[68:69], v[62:63]
	v_mov_b32_e32 v82, v85
	v_pk_mul_f32 v[70:71], v[86:87], v[66:67] op_sel:[0,1] op_sel_hi:[1,0]
	v_pk_add_f32 v[58:59], v[58:59], v[190:191]
	v_pk_fma_f32 v[70:71], v[82:83], v[66:67], v[70:71]
	v_pk_add_f32 v[58:59], v[58:59], v[88:89]
	v_pk_add_f32 v[62:63], v[62:63], v[70:71]
	v_and_b32_sdwa v71, v58, v129 dst_sel:DWORD dst_unused:UNUSED_PAD src0_sel:WORD_1 src1_sel:DWORD
	v_pk_add_f32 v[62:63], v[62:63], v[182:183]
	v_add3_u32 v76, v58, v71, s4
	v_and_b32_sdwa v71, v63, v129 dst_sel:DWORD dst_unused:UNUSED_PAD src0_sel:WORD_1 src1_sel:DWORD
	v_and_b32_sdwa v77, v62, v129 dst_sel:DWORD dst_unused:UNUSED_PAD src0_sel:WORD_1 src1_sel:DWORD
	v_and_b32_sdwa v70, v59, v129 dst_sel:DWORD dst_unused:UNUSED_PAD src0_sel:WORD_1 src1_sel:DWORD
	v_add3_u32 v71, v63, v71, s4
	v_add3_u32 v77, v62, v77, s4
	v_add3_u32 v70, v59, v70, s4
	v_and_b32_e32 v71, 0xffff0000, v71
	v_and_b32_e32 v77, 0xffff0000, v77
	v_or_b32_sdwa v71, v71, v70 dst_sel:DWORD dst_unused:UNUSED_PAD src0_sel:DWORD src1_sel:WORD_1
	v_or_b32_sdwa v70, v77, v76 dst_sel:DWORD dst_unused:UNUSED_PAD src0_sel:DWORD src1_sel:WORD_1
	global_store_dwordx2 v[72:73], v[70:71], off offset:512
	v_pk_mul_f32 v[70:71], v[62:63], v[62:63]
	s_nop 0
	v_pk_fma_f32 v[80:81], v[58:59], v[58:59], v[70:71]
	v_cvt_pk_f32_fp8_e32 v[70:71], v178
	v_cvt_pk_f32_fp8_sdwa v[82:83], v176 src0_sel:WORD_1
	v_cvt_pk_f32_fp8_sdwa v[76:77], v178 src0_sel:WORD_1
	v_cvt_pk_f32_fp8_e32 v[78:79], v176
	v_cvt_pk_f32_fp8_e32 v[84:85], v175
	v_cvt_pk_f32_fp8_sdwa v[86:87], v175 src0_sel:WORD_1
	v_cvt_pk_f32_fp8_e32 v[88:89], v174
	v_cvt_pk_f32_fp8_sdwa v[174:175], v174 src0_sel:WORD_1
	v_mov_b32_e32 v200, v70
	v_mov_b32_e32 v201, v82
	v_lshlrev_b32_e32 v183, 16, v55
	v_lshlrev_b32_e32 v182, 16, v54
	v_and_b32_e32 v191, 0xffff0000, v55
	v_and_b32_e32 v190, 0xffff0000, v54
	v_mov_b32_e32 v54, v78
	v_mov_b32_e32 v55, v76
	v_pk_mul_f32 v[200:201], v[200:201], v[68:69] op_sel:[0,1] op_sel_hi:[1,0]
	v_mov_b32_e32 v202, v84
	v_mov_b32_e32 v203, v174
	v_mov_b32_e32 v82, v71
	v_pk_fma_f32 v[54:55], v[54:55], v[68:69], v[200:201]
	v_mov_b32_e32 v200, v88
	v_mov_b32_e32 v201, v86
	v_pk_mul_f32 v[202:203], v[202:203], v[66:67] op_sel:[0,1] op_sel_hi:[1,0]
	v_mov_b32_e32 v76, v79
	v_pk_mul_f32 v[70:71], v[82:83], v[68:69] op_sel:[0,1] op_sel_hi:[1,0]
	v_mov_b32_e32 v174, v85
	v_pk_fma_f32 v[200:201], v[200:201], v[66:67], v[202:203]
	v_pk_fma_f32 v[70:71], v[76:77], v[68:69], v[70:71]
	v_mov_b32_e32 v86, v89
	v_pk_mul_f32 v[76:77], v[174:175], v[66:67] op_sel:[0,1] op_sel_hi:[1,0]
	v_pk_add_f32 v[54:55], v[54:55], v[200:201]
	v_pk_fma_f32 v[76:77], v[86:87], v[66:67], v[76:77]
	v_pk_add_f32 v[54:55], v[54:55], v[182:183]
	v_pk_add_f32 v[70:71], v[70:71], v[76:77]
	v_and_b32_sdwa v77, v54, v129 dst_sel:DWORD dst_unused:UNUSED_PAD src0_sel:WORD_1 src1_sel:DWORD
	v_pk_add_f32 v[70:71], v[70:71], v[190:191]
	v_add3_u32 v78, v54, v77, s4
	v_and_b32_sdwa v77, v71, v129 dst_sel:DWORD dst_unused:UNUSED_PAD src0_sel:WORD_1 src1_sel:DWORD
	v_and_b32_sdwa v79, v70, v129 dst_sel:DWORD dst_unused:UNUSED_PAD src0_sel:WORD_1 src1_sel:DWORD
	v_and_b32_sdwa v76, v55, v129 dst_sel:DWORD dst_unused:UNUSED_PAD src0_sel:WORD_1 src1_sel:DWORD
	v_add3_u32 v77, v71, v77, s4
	v_add3_u32 v79, v70, v79, s4
	v_add3_u32 v76, v55, v76, s4
	v_and_b32_e32 v77, 0xffff0000, v77
	v_and_b32_e32 v79, 0xffff0000, v79
	v_or_b32_sdwa v77, v77, v76 dst_sel:DWORD dst_unused:UNUSED_PAD src0_sel:DWORD src1_sel:WORD_1
	v_or_b32_sdwa v76, v79, v78 dst_sel:DWORD dst_unused:UNUSED_PAD src0_sel:DWORD src1_sel:WORD_1
	global_store_dwordx2 v[72:73], v[76:77], off offset:1024
	v_pk_mul_f32 v[76:77], v[70:71], v[70:71]
	s_nop 0
	v_pk_fma_f32 v[84:85], v[54:55], v[54:55], v[76:77]
	v_cvt_pk_f32_fp8_e32 v[76:77], v170
	v_cvt_pk_f32_fp8_sdwa v[86:87], v168 src0_sel:WORD_1
	v_cvt_pk_f32_fp8_sdwa v[78:79], v170 src0_sel:WORD_1
	v_cvt_pk_f32_fp8_e32 v[82:83], v168
	v_cvt_pk_f32_fp8_e32 v[88:89], v167
	v_cvt_pk_f32_fp8_sdwa v[174:175], v167 src0_sel:WORD_1
	v_cvt_pk_f32_fp8_e32 v[182:183], v166
	v_cvt_pk_f32_fp8_sdwa v[166:167], v166 src0_sel:WORD_1
	v_mov_b32_e32 v202, v76
	v_mov_b32_e32 v203, v86
	v_lshlrev_b32_e32 v191, 16, v49
	v_lshlrev_b32_e32 v190, 16, v48
	v_and_b32_e32 v201, 0xffff0000, v49
	v_and_b32_e32 v200, 0xffff0000, v48
	v_mov_b32_e32 v48, v82
	v_mov_b32_e32 v49, v78
	v_pk_mul_f32 v[202:203], v[202:203], v[68:69] op_sel:[0,1] op_sel_hi:[1,0]
	v_mov_b32_e32 v204, v88
	v_mov_b32_e32 v205, v166
	v_mov_b32_e32 v86, v77
	v_pk_fma_f32 v[48:49], v[48:49], v[68:69], v[202:203]
	v_mov_b32_e32 v202, v182
	v_mov_b32_e32 v203, v174
	v_pk_mul_f32 v[204:205], v[204:205], v[66:67] op_sel:[0,1] op_sel_hi:[1,0]
	v_mov_b32_e32 v78, v83
	v_pk_mul_f32 v[76:77], v[86:87], v[68:69] op_sel:[0,1] op_sel_hi:[1,0]
	v_mov_b32_e32 v166, v89
	v_pk_fma_f32 v[202:203], v[202:203], v[66:67], v[204:205]
	v_pk_fma_f32 v[76:77], v[78:79], v[68:69], v[76:77]
	v_mov_b32_e32 v174, v183
	v_pk_mul_f32 v[78:79], v[166:167], v[66:67] op_sel:[0,1] op_sel_hi:[1,0]
	v_pk_add_f32 v[48:49], v[48:49], v[202:203]
	v_pk_fma_f32 v[78:79], v[174:175], v[66:67], v[78:79]
	v_pk_add_f32 v[48:49], v[48:49], v[190:191]
	v_pk_add_f32 v[76:77], v[76:77], v[78:79]
	v_and_b32_sdwa v79, v48, v129 dst_sel:DWORD dst_unused:UNUSED_PAD src0_sel:WORD_1 src1_sel:DWORD
	v_pk_add_f32 v[76:77], v[76:77], v[200:201]
	v_add3_u32 v82, v48, v79, s4
	v_and_b32_sdwa v79, v77, v129 dst_sel:DWORD dst_unused:UNUSED_PAD src0_sel:WORD_1 src1_sel:DWORD
	v_and_b32_sdwa v83, v76, v129 dst_sel:DWORD dst_unused:UNUSED_PAD src0_sel:WORD_1 src1_sel:DWORD
	v_and_b32_sdwa v78, v49, v129 dst_sel:DWORD dst_unused:UNUSED_PAD src0_sel:WORD_1 src1_sel:DWORD
	v_add3_u32 v79, v77, v79, s4
	v_add3_u32 v83, v76, v83, s4
	v_add3_u32 v78, v49, v78, s4
	v_and_b32_e32 v79, 0xffff0000, v79
	v_and_b32_e32 v83, 0xffff0000, v83
	v_or_b32_sdwa v79, v79, v78 dst_sel:DWORD dst_unused:UNUSED_PAD src0_sel:DWORD src1_sel:WORD_1
	v_or_b32_sdwa v78, v83, v82 dst_sel:DWORD dst_unused:UNUSED_PAD src0_sel:DWORD src1_sel:WORD_1
	global_store_dwordx2 v[72:73], v[78:79], off offset:1536
	v_pk_mul_f32 v[78:79], v[76:77], v[76:77]
	s_nop 0
	v_pk_fma_f32 v[88:89], v[48:49], v[48:49], v[78:79]
	v_cvt_pk_f32_fp8_e32 v[78:79], v161
	v_cvt_pk_f32_fp8_sdwa v[82:83], v161 src0_sel:WORD_1
	v_cvt_pk_f32_fp8_e32 v[86:87], v160
	v_cvt_pk_f32_fp8_sdwa v[160:161], v160 src0_sel:WORD_1
	v_cvt_pk_f32_fp8_e32 v[166:167], v159
	v_cvt_pk_f32_fp8_sdwa v[174:175], v159 src0_sel:WORD_1
	v_cvt_pk_f32_fp8_e32 v[182:183], v158
	v_cvt_pk_f32_fp8_sdwa v[158:159], v158 src0_sel:WORD_1
	v_mov_b32_e32 v202, v78
	v_mov_b32_e32 v203, v160
	v_lshlrev_b32_e32 v191, 16, v45
	v_lshlrev_b32_e32 v190, 16, v44
	v_and_b32_e32 v201, 0xffff0000, v45
	v_and_b32_e32 v200, 0xffff0000, v44
	v_mov_b32_e32 v44, v86
	v_mov_b32_e32 v45, v82
	v_pk_mul_f32 v[202:203], v[202:203], v[68:69] op_sel:[0,1] op_sel_hi:[1,0]
	v_mov_b32_e32 v204, v166
	v_mov_b32_e32 v205, v158
	v_mov_b32_e32 v160, v79
	v_pk_fma_f32 v[44:45], v[44:45], v[68:69], v[202:203]
	v_mov_b32_e32 v202, v182
	v_mov_b32_e32 v203, v174
	v_pk_mul_f32 v[204:205], v[204:205], v[66:67] op_sel:[0,1] op_sel_hi:[1,0]
	v_mov_b32_e32 v82, v87
	v_pk_mul_f32 v[78:79], v[160:161], v[68:69] op_sel:[0,1] op_sel_hi:[1,0]
	v_mov_b32_e32 v158, v167
	v_pk_fma_f32 v[202:203], v[202:203], v[66:67], v[204:205]
	v_pk_fma_f32 v[78:79], v[82:83], v[68:69], v[78:79]
	v_mov_b32_e32 v174, v183
	v_pk_mul_f32 v[82:83], v[158:159], v[66:67] op_sel:[0,1] op_sel_hi:[1,0]
	v_pk_add_f32 v[44:45], v[44:45], v[202:203]
	v_pk_fma_f32 v[82:83], v[174:175], v[66:67], v[82:83]
	v_pk_add_f32 v[44:45], v[44:45], v[190:191]
	v_pk_add_f32 v[78:79], v[78:79], v[82:83]
	v_and_b32_sdwa v83, v44, v129 dst_sel:DWORD dst_unused:UNUSED_PAD src0_sel:WORD_1 src1_sel:DWORD
	v_pk_add_f32 v[78:79], v[78:79], v[200:201]
	v_add3_u32 v86, v44, v83, s4
	v_and_b32_sdwa v83, v79, v129 dst_sel:DWORD dst_unused:UNUSED_PAD src0_sel:WORD_1 src1_sel:DWORD
	v_and_b32_sdwa v87, v78, v129 dst_sel:DWORD dst_unused:UNUSED_PAD src0_sel:WORD_1 src1_sel:DWORD
	v_and_b32_sdwa v82, v45, v129 dst_sel:DWORD dst_unused:UNUSED_PAD src0_sel:WORD_1 src1_sel:DWORD
	v_add3_u32 v83, v79, v83, s4
	v_add3_u32 v87, v78, v87, s4
	v_add3_u32 v82, v45, v82, s4
	v_and_b32_e32 v83, 0xffff0000, v83
	v_and_b32_e32 v87, 0xffff0000, v87
	v_or_b32_sdwa v83, v83, v82 dst_sel:DWORD dst_unused:UNUSED_PAD src0_sel:DWORD src1_sel:WORD_1
	v_or_b32_sdwa v82, v87, v86 dst_sel:DWORD dst_unused:UNUSED_PAD src0_sel:DWORD src1_sel:WORD_1
	global_store_dwordx2 v[72:73], v[82:83], off offset:2048
	v_pk_mul_f32 v[82:83], v[78:79], v[78:79]
	s_nop 0
	v_pk_fma_f32 v[158:159], v[44:45], v[44:45], v[82:83]
	v_cvt_pk_f32_fp8_e32 v[82:83], v152
	v_cvt_pk_f32_fp8_sdwa v[160:161], v151 src0_sel:WORD_1
	v_cvt_pk_f32_fp8_sdwa v[86:87], v152 src0_sel:WORD_1
	v_cvt_pk_f32_fp8_e32 v[152:153], v151
	v_cvt_pk_f32_fp8_e32 v[166:167], v150
	v_cvt_pk_f32_fp8_sdwa v[182:183], v149 src0_sel:WORD_1
	v_cvt_pk_f32_fp8_sdwa v[150:151], v150 src0_sel:WORD_1
	v_cvt_pk_f32_fp8_e32 v[174:175], v149
	v_mov_b32_e32 v202, v82
	v_mov_b32_e32 v203, v160
	v_lshlrev_b32_e32 v191, 16, v41
	v_lshlrev_b32_e32 v190, 16, v40
	v_and_b32_e32 v201, 0xffff0000, v41
	v_and_b32_e32 v200, 0xffff0000, v40
	v_mov_b32_e32 v40, v152
	v_mov_b32_e32 v41, v86
	v_pk_mul_f32 v[202:203], v[202:203], v[68:69] op_sel:[0,1] op_sel_hi:[1,0]
	v_mov_b32_e32 v204, v166
	v_mov_b32_e32 v205, v182
	v_mov_b32_e32 v160, v83
	v_pk_fma_f32 v[40:41], v[40:41], v[68:69], v[202:203]
	v_mov_b32_e32 v202, v174
	v_mov_b32_e32 v203, v150
	v_pk_mul_f32 v[204:205], v[204:205], v[66:67] op_sel:[0,1] op_sel_hi:[1,0]
	v_mov_b32_e32 v86, v153
	v_pk_mul_f32 v[82:83], v[160:161], v[68:69] op_sel:[0,1] op_sel_hi:[1,0]
	v_mov_b32_e32 v182, v167
	v_pk_fma_f32 v[202:203], v[202:203], v[66:67], v[204:205]
	v_pk_fma_f32 v[82:83], v[86:87], v[68:69], v[82:83]
	v_mov_b32_e32 v150, v175
	v_pk_mul_f32 v[86:87], v[182:183], v[66:67] op_sel:[0,1] op_sel_hi:[1,0]
	v_pk_add_f32 v[40:41], v[40:41], v[202:203]
	v_pk_fma_f32 v[86:87], v[150:151], v[66:67], v[86:87]
	v_pk_add_f32 v[40:41], v[40:41], v[190:191]
	v_pk_add_f32 v[82:83], v[82:83], v[86:87]
	v_and_b32_sdwa v87, v40, v129 dst_sel:DWORD dst_unused:UNUSED_PAD src0_sel:WORD_1 src1_sel:DWORD
	v_pk_add_f32 v[82:83], v[82:83], v[200:201]
	v_add3_u32 v140, v40, v87, s4
	v_and_b32_sdwa v87, v83, v129 dst_sel:DWORD dst_unused:UNUSED_PAD src0_sel:WORD_1 src1_sel:DWORD
	v_and_b32_sdwa v143, v82, v129 dst_sel:DWORD dst_unused:UNUSED_PAD src0_sel:WORD_1 src1_sel:DWORD
	v_and_b32_sdwa v86, v41, v129 dst_sel:DWORD dst_unused:UNUSED_PAD src0_sel:WORD_1 src1_sel:DWORD
	v_add3_u32 v87, v83, v87, s4
	v_add3_u32 v143, v82, v143, s4
	v_add3_u32 v86, v41, v86, s4
	v_and_b32_e32 v87, 0xffff0000, v87
	v_and_b32_e32 v143, 0xffff0000, v143
	v_or_b32_sdwa v87, v87, v86 dst_sel:DWORD dst_unused:UNUSED_PAD src0_sel:DWORD src1_sel:WORD_1
	v_or_b32_sdwa v86, v143, v140 dst_sel:DWORD dst_unused:UNUSED_PAD src0_sel:DWORD src1_sel:WORD_1
	global_store_dwordx2 v[72:73], v[86:87], off offset:2560
	v_pk_mul_f32 v[86:87], v[82:83], v[82:83]
	s_nop 0
	v_pk_fma_f32 v[150:151], v[40:41], v[40:41], v[86:87]
	v_cvt_pk_f32_fp8_e32 v[86:87], v144
	v_cvt_pk_f32_fp8_e32 v[160:161], v142
	v_cvt_pk_f32_fp8_sdwa v[142:143], v142 src0_sel:WORD_1
	v_cvt_pk_f32_fp8_sdwa v[152:153], v144 src0_sel:WORD_1
	v_cvt_pk_f32_fp8_e32 v[166:167], v141
	v_cvt_pk_f32_fp8_sdwa v[182:183], v139 src0_sel:WORD_1
	v_cvt_pk_f32_fp8_sdwa v[140:141], v141 src0_sel:WORD_1
	v_cvt_pk_f32_fp8_e32 v[174:175], v139
	v_mov_b32_e32 v202, v86
	v_mov_b32_e32 v203, v142
	v_lshlrev_b32_e32 v191, 16, v35
	v_lshlrev_b32_e32 v190, 16, v34
	v_and_b32_e32 v201, 0xffff0000, v35
	v_and_b32_e32 v200, 0xffff0000, v34
	v_mov_b32_e32 v34, v160
	v_mov_b32_e32 v35, v152
	v_pk_mul_f32 v[202:203], v[202:203], v[68:69] op_sel:[0,1] op_sel_hi:[1,0]
	v_mov_b32_e32 v205, v182
	v_mov_b32_e32 v142, v87
	v_mov_b32_e32 v182, v167
	v_pk_fma_f32 v[34:35], v[34:35], v[68:69], v[202:203]
	v_mov_b32_e32 v203, v140
	v_mov_b32_e32 v204, v166
	v_mov_b32_e32 v152, v161
	v_pk_mul_f32 v[86:87], v[142:143], v[68:69] op_sel:[0,1] op_sel_hi:[1,0]
	v_mov_b32_e32 v140, v175
	v_pk_mul_f32 v[142:143], v[182:183], v[66:67] op_sel:[0,1] op_sel_hi:[1,0]
	v_mov_b32_e32 v202, v174
	v_pk_mul_f32 v[204:205], v[204:205], v[66:67] op_sel:[0,1] op_sel_hi:[1,0]
	v_pk_fma_f32 v[86:87], v[152:153], v[68:69], v[86:87]
	v_pk_fma_f32 v[140:141], v[140:141], v[66:67], v[142:143]
	v_pk_fma_f32 v[202:203], v[202:203], v[66:67], v[204:205]
	v_pk_add_f32 v[86:87], v[86:87], v[140:141]
	v_pk_add_f32 v[34:35], v[34:35], v[202:203]
	v_pk_add_f32 v[86:87], v[86:87], v[200:201]
	v_pk_add_f32 v[34:35], v[34:35], v[190:191]
	v_and_b32_sdwa v141, v87, v129 dst_sel:DWORD dst_unused:UNUSED_PAD src0_sel:WORD_1 src1_sel:DWORD
	v_and_b32_sdwa v142, v86, v129 dst_sel:DWORD dst_unused:UNUSED_PAD src0_sel:WORD_1 src1_sel:DWORD
	v_and_b32_sdwa v139, v35, v129 dst_sel:DWORD dst_unused:UNUSED_PAD src0_sel:WORD_1 src1_sel:DWORD
	v_and_b32_sdwa v140, v34, v129 dst_sel:DWORD dst_unused:UNUSED_PAD src0_sel:WORD_1 src1_sel:DWORD
	v_add3_u32 v141, v87, v141, s4
	v_add3_u32 v142, v86, v142, s4
	v_add3_u32 v140, v34, v140, s4
	v_add3_u32 v139, v35, v139, s4
	v_and_b32_e32 v141, 0xffff0000, v141
	v_and_b32_e32 v142, 0xffff0000, v142
	v_or_b32_sdwa v141, v141, v139 dst_sel:DWORD dst_unused:UNUSED_PAD src0_sel:DWORD src1_sel:WORD_1
	v_or_b32_sdwa v140, v142, v140 dst_sel:DWORD dst_unused:UNUSED_PAD src0_sel:DWORD src1_sel:WORD_1
	global_store_dwordx2 v[72:73], v[140:141], off offset:3072
	v_pk_mul_f32 v[140:141], v[86:87], v[86:87]
	s_nop 0
	v_pk_fma_f32 v[140:141], v[34:35], v[34:35], v[140:141]
	v_cvt_pk_f32_fp8_e32 v[142:143], v136
	v_cvt_pk_f32_fp8_sdwa v[166:167], v134 src0_sel:WORD_1
	v_cvt_pk_f32_fp8_sdwa v[152:153], v136 src0_sel:WORD_1
	v_cvt_pk_f32_fp8_e32 v[160:161], v134
	v_cvt_pk_f32_fp8_e32 v[174:175], v133
	v_cvt_pk_f32_fp8_sdwa v[200:201], v131 src0_sel:WORD_1
	v_cvt_pk_f32_fp8_sdwa v[182:183], v133 src0_sel:WORD_1
	v_cvt_pk_f32_fp8_e32 v[190:191], v131
	v_mov_b32_e32 v206, v142
	v_mov_b32_e32 v207, v166
	v_lshlrev_b32_e32 v203, 16, v29
	v_lshlrev_b32_e32 v202, 16, v28
	v_and_b32_e32 v205, 0xffff0000, v29
	v_and_b32_e32 v204, 0xffff0000, v28
	v_mov_b32_e32 v28, v160
	v_mov_b32_e32 v29, v152
	v_pk_mul_f32 v[206:207], v[206:207], v[68:69] op_sel:[0,1] op_sel_hi:[1,0]
	v_mov_b32_e32 v208, v174
	v_mov_b32_e32 v209, v200
	v_mov_b32_e32 v166, v143
	v_pk_fma_f32 v[28:29], v[28:29], v[68:69], v[206:207]
	v_mov_b32_e32 v206, v190
	v_mov_b32_e32 v207, v182
	v_pk_mul_f32 v[208:209], v[208:209], v[66:67] op_sel:[0,1] op_sel_hi:[1,0]
	v_mov_b32_e32 v152, v161
	v_pk_mul_f32 v[142:143], v[166:167], v[68:69] op_sel:[0,1] op_sel_hi:[1,0]
	v_mov_b32_e32 v200, v175
	v_pk_fma_f32 v[206:207], v[206:207], v[66:67], v[208:209]
	v_pk_fma_f32 v[68:69], v[152:153], v[68:69], v[142:143]
	v_mov_b32_e32 v182, v191
	v_pk_mul_f32 v[142:143], v[200:201], v[66:67] op_sel:[0,1] op_sel_hi:[1,0]
	v_pk_add_f32 v[28:29], v[28:29], v[206:207]
	v_pk_fma_f32 v[66:67], v[182:183], v[66:67], v[142:143]
	v_pk_add_f32 v[28:29], v[28:29], v[202:203]
	v_pk_add_f32 v[66:67], v[68:69], v[66:67]
	v_and_b32_sdwa v69, v28, v129 dst_sel:DWORD dst_unused:UNUSED_PAD src0_sel:WORD_1 src1_sel:DWORD
	v_pk_add_f32 v[66:67], v[66:67], v[204:205]
	v_add3_u32 v131, v28, v69, s4
	v_and_b32_sdwa v69, v67, v129 dst_sel:DWORD dst_unused:UNUSED_PAD src0_sel:WORD_1 src1_sel:DWORD
	v_and_b32_sdwa v133, v66, v129 dst_sel:DWORD dst_unused:UNUSED_PAD src0_sel:WORD_1 src1_sel:DWORD
	v_and_b32_sdwa v68, v29, v129 dst_sel:DWORD dst_unused:UNUSED_PAD src0_sel:WORD_1 src1_sel:DWORD
	v_add3_u32 v69, v67, v69, s4
	v_add3_u32 v133, v66, v133, s4
	v_add3_u32 v68, v29, v68, s4
	v_and_b32_e32 v69, 0xffff0000, v69
	v_and_b32_e32 v133, 0xffff0000, v133
	v_or_b32_sdwa v69, v69, v68 dst_sel:DWORD dst_unused:UNUSED_PAD src0_sel:DWORD src1_sel:WORD_1
	v_or_b32_sdwa v68, v133, v131 dst_sel:DWORD dst_unused:UNUSED_PAD src0_sel:DWORD src1_sel:WORD_1
	global_store_dwordx2 v[72:73], v[68:69], off offset:3584
	v_add_f32_e32 v72, v80, v81
	v_add_f32_e32 v73, v74, v75
	v_add_f32_e32 v72, v73, v72
	v_add_f32_e32 v73, v84, v85
	v_add_f32_e32 v72, v72, v73
	v_add_f32_e32 v73, v88, v89
	v_add_f32_e32 v72, v72, v73
	v_add_f32_e32 v73, v158, v159
	v_pk_mul_f32 v[68:69], v[66:67], v[66:67]
	v_add_f32_e32 v72, v72, v73
	v_add_f32_e32 v73, v150, v151
	v_pk_fma_f32 v[68:69], v[28:29], v[28:29], v[68:69]
	v_add_f32_e32 v72, v72, v73
	v_add_f32_e32 v73, v140, v141
	v_add_f32_e32 v72, v72, v73
	v_add_f32_e32 v68, v68, v69
	v_add_f32_e32 v68, v72, v68
	v_mov_b64_e32 v[72:73], v[212:213]
	v_mov_b64_e32 v[74:75], v[214:215]
	ds_bpermute_b32 v69, v1, v68
	s_waitcnt lgkmcnt(0)
	v_add_f32_e32 v68, v68, v69
	ds_bpermute_b32 v69, v90, v68
	s_waitcnt lgkmcnt(0)
	v_add_f32_e32 v68, v68, v69
	ds_bpermute_b32 v69, v91, v68
	s_waitcnt lgkmcnt(0)
	v_add_f32_e32 v68, v68, v69
	ds_bpermute_b32 v69, v92, v68
	s_waitcnt lgkmcnt(0)
	v_add_f32_e32 v68, v68, v69
	ds_bpermute_b32 v69, v93, v68
	s_waitcnt lgkmcnt(0)
	v_add_f32_e32 v68, v68, v69
	ds_bpermute_b32 v69, v94, v68
	s_waitcnt lgkmcnt(0)
	v_add_f32_e32 v68, v68, v69
	v_fmamk_f32 v68, v68, 0x3a000000, v127
	v_mul_f32_e32 v69, 0x4f800000, v68
	v_cmp_gt_f32_e32 vcc, s19, v68
	s_nop 1
	v_cndmask_b32_e32 v68, v68, v69, vcc
	v_sqrt_f32_e32 v69, v68
	s_nop 0
	v_add_u32_e32 v80, -1, v69
	v_add_u32_e32 v81, 1, v69
	v_fma_f32 v84, -v80, v69, v68
	v_fma_f32 v85, -v81, v69, v68
	v_cmp_ge_f32_e64 s[8:9], 0, v84
	s_nop 1
	v_cndmask_b32_e64 v69, v69, v80, s[8:9]
	v_cmp_lt_f32_e64 s[8:9], 0, v85
	s_nop 1
	v_cndmask_b32_e64 v69, v69, v81, s[8:9]
	v_mul_f32_e32 v80, 0x37800000, v69
	v_cndmask_b32_e32 v69, v69, v80, vcc
	v_cmp_class_f32_e32 vcc, v68, v128
	v_mov_b32_e32 v81, 0
	s_nop 0
	v_cndmask_b32_e32 v68, v69, v68, vcc
	v_div_scale_f32 v69, s[0:1], v68, v68, 1.0
	v_rcp_f32_e32 v80, v69
	v_div_scale_f32 v84, vcc, 1.0, v68, 1.0
	v_fma_f32 v85, -v69, v80, 1.0
	v_fmac_f32_e32 v80, v85, v80
	v_mul_f32_e32 v85, v84, v80
	v_fma_f32 v88, -v69, v85, v84
	v_fmac_f32_e32 v85, v88, v80
	v_fma_f32 v69, -v69, v85, v84
	v_div_fmas_f32 v69, v69, v80, v85
	v_div_fixup_f32 v68, v69, v68, 1.0
	v_mul_f32_e32 v38, v68, v38
	v_mul_f32_e32 v52, v68, v52

	v_mul_f32_e32 v38, v72, v38
	v_mul_f32_e32 v52, v73, v52
	v_cvt_pk_fp8_f32 v81, v38, v52
	v_mul_f32_e32 v39, v68, v39
	v_mul_f32_e32 v38, v68, v53
	v_mul_f32_e32 v39, v74, v39
	v_mul_f32_e32 v38, v75, v38
	v_cvt_pk_fp8_f32 v81, v39, v38 op_sel:[0,0,1]
	v_mul_f32_e32 v39, v68, v58
	v_mul_f32_e32 v52, v68, v62
	v_mov_b32_e32 v38, 0
	global_store_dword v[24:25], v81, off
	v_mov_b64_e32 v[72:73], v[216:217]
	v_mov_b64_e32 v[74:75], v[218:219]
	v_mul_f32_e32 v53, v68, v59
	v_mul_f32_e32 v49, v68, v49
	v_mul_f32_e32 v45, v68, v45
	v_mul_f32_e32 v41, v68, v41
	v_mul_f32_e32 v34, v68, v34
	v_mul_f32_e32 v35, v68, v35
	v_mul_f32_e32 v28, v68, v28
	v_mul_f32_e32 v29, v68, v29
	ds_bpermute_b32 v69, v108, v19
	s_waitcnt vmcnt(17)
	v_cvt_pk_f32_fp8_sdwa v[80:81], v197 src0_sel:WORD_1

	v_mul_f32_e32 v39, v72, v39
	v_mul_f32_e32 v52, v73, v52
	v_cvt_pk_fp8_f32 v38, v39, v52
	v_mul_f32_e32 v39, v68, v63
	v_mul_f32_e32 v52, v74, v53
	v_mul_f32_e32 v39, v75, v39
	v_cvt_pk_fp8_f32 v38, v52, v39 op_sel:[0,0,1]
	v_mul_f32_e32 v39, v68, v54
	v_mul_f32_e32 v52, v68, v70
	v_mul_f32_e32 v53, v68, v55
	global_store_dword v[24:25], v38, off offset:256
	v_mov_b64_e32 v[72:73], v[220:221]
	v_mov_b64_e32 v[74:75], v[222:223]
	v_mov_b32_e32 v38, 0

	v_mul_f32_e32 v39, v72, v39
	v_mul_f32_e32 v52, v73, v52
	v_cvt_pk_fp8_f32 v38, v39, v52
	v_mul_f32_e32 v39, v68, v71
	v_mul_f32_e32 v52, v74, v53
	v_mul_f32_e32 v39, v75, v39
	v_cvt_pk_fp8_f32 v38, v52, v39 op_sel:[0,0,1]
	v_mul_f32_e32 v39, v68, v48
	v_mul_f32_e32 v48, v68, v76
	v_cvt_pk_f32_fp8_sdwa v[72:73], v194 src0_sel:WORD_1
	global_store_dword v[24:25], v38, off offset:512
	v_mov_b64_e32 v[52:53], v[224:225]
	v_mov_b64_e32 v[54:55], v[226:227]
	v_mov_b32_e32 v38, 0
	v_cvt_pk_f32_fp8_e32 v[70:71], v194
	v_cvt_pk_f32_fp8_e32 v[74:75], v195
	v_mov_b32_e32 v85, v72

	v_mul_f32_e32 v39, v52, v39
	v_mul_f32_e32 v48, v53, v48
	v_cvt_pk_fp8_f32 v38, v39, v48
	v_mul_f32_e32 v39, v68, v77
	v_mul_f32_e32 v48, v54, v49
	v_mul_f32_e32 v39, v55, v39
	v_cvt_pk_fp8_f32 v38, v48, v39 op_sel:[0,0,1]
	v_mul_f32_e32 v39, v68, v44
	v_mul_f32_e32 v44, v68, v78
	ds_bpermute_b32 v48, v113, v130
	global_store_dword v[24:25], v38, off offset:768
	v_mov_b64_e32 v[52:53], v[228:229]
	v_mov_b64_e32 v[54:55], v[230:231]
	v_mov_b32_e32 v38, 0
	v_cvt_pk_f32_fp8_sdwa v[76:77], v195 src0_sel:WORD_1
	s_waitcnt lgkmcnt(0)
	v_ashrrev_i32_e32 v49, 31, v48
	v_lshlrev_b64 v[48:49], 11, v[48:49]

	v_mul_f32_e32 v39, v52, v39
	v_mul_f32_e32 v44, v53, v44
	v_cvt_pk_fp8_f32 v38, v39, v44
	v_mul_f32_e32 v39, v68, v79
	v_mul_f32_e32 v44, v54, v45
	v_mul_f32_e32 v39, v55, v39
	v_cvt_pk_fp8_f32 v38, v44, v39 op_sel:[0,0,1]
	v_mul_f32_e32 v39, v68, v40
	v_mul_f32_e32 v40, v68, v82
	v_mul_f32_e32 v45, v68, v86
	global_store_dword v[24:25], v38, off offset:1024
	v_mov_b64_e32 v[52:53], v[232:233]
	v_mov_b64_e32 v[54:55], v[234:235]
	v_mov_b32_e32 v38, 0
	v_mov_b32_e32 v44, 0
	v_cvt_pk_f32_fp8_e32 v[78:79], v197
	v_mov_b32_e32 v82, v70
	v_mov_b32_e32 v86, v74

	v_mul_f32_e32 v39, v52, v39
	v_mul_f32_e32 v40, v53, v40
	v_cvt_pk_fp8_f32 v38, v39, v40
	v_mul_f32_e32 v39, v68, v83
	v_mul_f32_e32 v40, v54, v41
	v_mul_f32_e32 v39, v55, v39
	v_cvt_pk_fp8_f32 v38, v40, v39 op_sel:[0,0,1]
	v_mul_f32_e32 v55, v68, v66
	v_mov_b32_e32 v54, 0
	ds_bpermute_b32 v52, v112, v130
	global_store_dword v[24:25], v38, off offset:1280
	v_mov_b64_e32 v[38:39], v[236:237]
	v_mov_b64_e32 v[40:41], v[238:239]
	ds_bpermute_b32 v66, v111, v19
	s_waitcnt lgkmcnt(1)
	v_ashrrev_i32_e32 v53, 31, v52
	v_lshlrev_b64 v[52:53], 11, v[52:53]

	v_mul_f32_e32 v34, v38, v34
	v_mul_f32_e32 v38, v39, v45
	v_cvt_pk_fp8_f32 v44, v34, v38
	v_mul_f32_e32 v34, v68, v87
	v_mul_f32_e32 v35, v40, v35
	v_mul_f32_e32 v34, v41, v34
	v_cvt_pk_fp8_f32 v44, v35, v34 op_sel:[0,0,1]
	ds_bpermute_b32 v34, v115, v130
	v_mov_b32_e32 v87, v80
	v_mov_b32_e32 v80, v75
	global_store_dword v[24:25], v44, off offset:1536
	v_mov_b64_e32 v[38:39], v[240:241]
	v_mov_b64_e32 v[40:41], v[242:243]
	ds_bpermute_b32 v44, v114, v130
	s_waitcnt lgkmcnt(1)
	v_ashrrev_i32_e32 v35, 31, v34
	v_lshlrev_b64 v[34:35], 11, v[34:35]
	v_lshl_add_u64 v[34:35], v[4:5], 0, v[34:35]
	s_waitcnt lgkmcnt(0)
	v_ashrrev_i32_e32 v45, 31, v44
	v_lshlrev_b64 v[44:45], 11, v[44:45]

	v_mul_f32_e32 v28, v38, v28
	v_mul_f32_e32 v38, v39, v55
	v_cvt_pk_fp8_f32 v54, v28, v38
	v_mul_f32_e32 v28, v68, v67
	v_mul_f32_e32 v29, v40, v29
	v_mul_f32_e32 v28, v41, v28
	v_cvt_pk_fp8_f32 v54, v29, v28 op_sel:[0,0,1]
	v_lshl_add_u64 v[28:29], v[4:5], 0, v[44:45]
	v_lshl_add_u64 v[38:39], v[4:5], 0, v[48:49]
	v_lshl_add_u64 v[40:41], v[4:5], 0, v[52:53]
	global_store_dword v[24:25], v54, off offset:1792
	global_load_dword v88, v[34:35], off offset:1792
	global_load_dword v139, v[34:35], off offset:1536
	global_load_dword v149, v[34:35], off offset:1280
	global_load_dword v158, v[34:35], off offset:1024
	global_load_dword v166, v[34:35], off offset:768
	global_load_dword v174, v[34:35], off offset:512
	global_load_dword v182, v[34:35], off offset:256
	global_load_dword v190, v[34:35], off
	global_load_dword v89, v[28:29], off offset:1792
	global_load_dword v140, v[28:29], off offset:1536
	global_load_dword v150, v[28:29], off offset:1280
	global_load_dword v159, v[28:29], off offset:1024
	global_load_dword v167, v[28:29], off offset:768
	global_load_dword v175, v[28:29], off offset:512
	global_load_dword v183, v[28:29], off offset:256
	global_load_dword v191, v[28:29], off
	global_load_dword v131, v[38:39], off offset:1792
	global_load_dword v141, v[38:39], off offset:1536
	global_load_dword v151, v[38:39], off offset:1280
	global_load_dword v160, v[38:39], off offset:1024
	global_load_dword v168, v[38:39], off offset:768
	global_load_dword v176, v[38:39], off offset:512
	global_load_dword v184, v[38:39], off offset:256
	global_load_dword v193, v[38:39], off
	global_load_dword v133, v[40:41], off offset:1792
	global_load_dword v143, v[40:41], off offset:1536
	global_load_dword v153, v[40:41], off offset:1280
	global_load_dword v161, v[40:41], off offset:1024
	global_load_dword v170, v[40:41], off offset:768
	global_load_dword v178, v[40:41], off offset:512
	global_load_dword v186, v[40:41], off offset:256
	global_load_dword v196, v[40:41], off
	global_load_dwordx2 v[28:29], v[60:61], off offset:3584
	global_load_dwordx2 v[34:35], v[60:61], off offset:3072
	global_load_dwordx2 v[38:39], v[60:61], off offset:2560
	global_load_dwordx2 v[44:45], v[60:61], off offset:2048
	global_load_dwordx2 v[48:49], v[60:61], off offset:1536
	global_load_dwordx2 v[52:53], v[60:61], off offset:1024
	global_load_dwordx2 v[58:59], v[60:61], off offset:512
	global_load_dwordx2 v[62:63], v[60:61], off
	ds_bpermute_b32 v68, v109, v19
	v_cvt_pk_f32_fp8_e32 v[54:55], v192
	ds_bpermute_b32 v67, v110, v19
	v_cvt_pk_f32_fp8_sdwa v[60:61], v192 src0_sel:WORD_1
	s_waitcnt vmcnt(63)
	v_lshlrev_b32_e32 v41, 16, v65
	v_mov_b32_e32 v84, v54
	s_waitcnt lgkmcnt(1)
	v_pk_mul_f32 v[84:85], v[84:85], v[68:69] op_sel:[0,1] op_sel_hi:[1,0]
	v_mov_b32_e32 v83, v60
	v_mov_b32_e32 v72, v55
	v_pk_fma_f32 v[82:83], v[82:83], v[68:69], v[84:85]
	v_mov_b32_e32 v84, v78
	v_mov_b32_e32 v85, v76
	s_waitcnt lgkmcnt(0)
	v_pk_mul_f32 v[86:87], v[86:87], v[66:67] op_sel:[0,1] op_sel_hi:[1,0]
	v_mov_b32_e32 v60, v71
	v_pk_mul_f32 v[54:55], v[72:73], v[68:69] op_sel:[0,1] op_sel_hi:[1,0]
	v_pk_fma_f32 v[84:85], v[84:85], v[66:67], v[86:87]
	v_pk_fma_f32 v[54:55], v[60:61], v[68:69], v[54:55]
	v_mov_b32_e32 v76, v79
	v_pk_mul_f32 v[60:61], v[80:81], v[66:67] op_sel:[0,1] op_sel_hi:[1,0]
	v_lshlrev_b32_e32 v40, 16, v64
	v_pk_add_f32 v[82:83], v[82:83], v[84:85]
	v_pk_fma_f32 v[60:61], v[76:77], v[66:67], v[60:61]
	v_and_b32_e32 v65, 0xffff0000, v65
	v_and_b32_e32 v64, 0xffff0000, v64
	v_pk_add_f32 v[40:41], v[82:83], v[40:41]
	v_pk_add_f32 v[54:55], v[54:55], v[60:61]
	v_and_b32_sdwa v61, v40, v129 dst_sel:DWORD dst_unused:UNUSED_PAD src0_sel:WORD_1 src1_sel:DWORD
	v_pk_add_f32 v[54:55], v[54:55], v[64:65]
	v_add3_u32 v64, v40, v61, s4
	v_and_b32_sdwa v61, v55, v129 dst_sel:DWORD dst_unused:UNUSED_PAD src0_sel:WORD_1 src1_sel:DWORD
	v_and_b32_sdwa v65, v54, v129 dst_sel:DWORD dst_unused:UNUSED_PAD src0_sel:WORD_1 src1_sel:DWORD
	v_and_b32_sdwa v60, v41, v129 dst_sel:DWORD dst_unused:UNUSED_PAD src0_sel:WORD_1 src1_sel:DWORD
	v_add3_u32 v61, v55, v61, s4
	v_add3_u32 v65, v54, v65, s4
	v_add3_u32 v60, v41, v60, s4
	v_and_b32_e32 v61, 0xffff0000, v61
	v_and_b32_e32 v65, 0xffff0000, v65
	v_or_b32_sdwa v61, v61, v60 dst_sel:DWORD dst_unused:UNUSED_PAD src0_sel:DWORD src1_sel:WORD_1
	v_or_b32_sdwa v60, v65, v64 dst_sel:DWORD dst_unused:UNUSED_PAD src0_sel:DWORD src1_sel:WORD_1
	global_store_dwordx2 v[30:31], v[60:61], off
	v_pk_mul_f32 v[60:61], v[54:55], v[54:55]
	s_nop 0
	v_pk_fma_f32 v[70:71], v[40:41], v[40:41], v[60:61]
	v_cvt_pk_f32_fp8_e32 v[60:61], v185
	v_cvt_pk_f32_fp8_sdwa v[74:75], v187 src0_sel:WORD_1
	v_cvt_pk_f32_fp8_sdwa v[64:65], v185 src0_sel:WORD_1
	v_cvt_pk_f32_fp8_e32 v[72:73], v187
	v_cvt_pk_f32_fp8_e32 v[76:77], v188
	s_waitcnt vmcnt(63)
	v_cvt_pk_f32_fp8_sdwa v[82:83], v189 src0_sel:WORD_1
	v_cvt_pk_f32_fp8_sdwa v[78:79], v188 src0_sel:WORD_1
	v_cvt_pk_f32_fp8_e32 v[80:81], v189
	v_mov_b32_e32 v188, v60
	v_mov_b32_e32 v189, v74
	v_lshlrev_b32_e32 v85, 16, v57
	v_lshlrev_b32_e32 v84, 16, v56
	v_and_b32_e32 v87, 0xffff0000, v57
	v_and_b32_e32 v86, 0xffff0000, v56
	v_mov_b32_e32 v56, v72
	v_mov_b32_e32 v57, v64
	v_pk_mul_f32 v[188:189], v[188:189], v[68:69] op_sel:[0,1] op_sel_hi:[1,0]
	v_mov_b32_e32 v194, v76
	v_mov_b32_e32 v195, v82
	v_mov_b32_e32 v74, v61
	v_pk_fma_f32 v[56:57], v[56:57], v[68:69], v[188:189]
	v_mov_b32_e32 v188, v80
	v_mov_b32_e32 v189, v78
	v_pk_mul_f32 v[194:195], v[194:195], v[66:67] op_sel:[0,1] op_sel_hi:[1,0]
	v_mov_b32_e32 v64, v73
	v_pk_mul_f32 v[60:61], v[74:75], v[68:69] op_sel:[0,1] op_sel_hi:[1,0]
	v_mov_b32_e32 v82, v77
	v_pk_fma_f32 v[188:189], v[188:189], v[66:67], v[194:195]
	v_pk_fma_f32 v[60:61], v[64:65], v[68:69], v[60:61]
	v_mov_b32_e32 v78, v81
	v_pk_mul_f32 v[64:65], v[82:83], v[66:67] op_sel:[0,1] op_sel_hi:[1,0]
	v_pk_add_f32 v[56:57], v[56:57], v[188:189]
	v_pk_fma_f32 v[64:65], v[78:79], v[66:67], v[64:65]
	v_pk_add_f32 v[56:57], v[56:57], v[84:85]
	v_pk_add_f32 v[60:61], v[60:61], v[64:65]
	v_and_b32_sdwa v65, v56, v129 dst_sel:DWORD dst_unused:UNUSED_PAD src0_sel:WORD_1 src1_sel:DWORD
	v_pk_add_f32 v[60:61], v[60:61], v[86:87]
	v_add3_u32 v72, v56, v65, s4
	v_and_b32_sdwa v65, v61, v129 dst_sel:DWORD dst_unused:UNUSED_PAD src0_sel:WORD_1 src1_sel:DWORD
	v_and_b32_sdwa v73, v60, v129 dst_sel:DWORD dst_unused:UNUSED_PAD src0_sel:WORD_1 src1_sel:DWORD
	v_and_b32_sdwa v64, v57, v129 dst_sel:DWORD dst_unused:UNUSED_PAD src0_sel:WORD_1 src1_sel:DWORD
	v_add3_u32 v65, v61, v65, s4
	v_add3_u32 v73, v60, v73, s4
	v_add3_u32 v64, v57, v64, s4
	v_and_b32_e32 v65, 0xffff0000, v65
	v_and_b32_e32 v73, 0xffff0000, v73
	v_or_b32_sdwa v65, v65, v64 dst_sel:DWORD dst_unused:UNUSED_PAD src0_sel:DWORD src1_sel:WORD_1
	v_or_b32_sdwa v64, v73, v72 dst_sel:DWORD dst_unused:UNUSED_PAD src0_sel:DWORD src1_sel:WORD_1
	global_store_dwordx2 v[30:31], v[64:65], off offset:512
	v_pk_mul_f32 v[64:65], v[60:61], v[60:61]
	s_nop 0
	v_pk_fma_f32 v[76:77], v[56:57], v[56:57], v[64:65]
	v_cvt_pk_f32_fp8_e32 v[64:65], v177
	v_cvt_pk_f32_fp8_sdwa v[78:79], v179 src0_sel:WORD_1
	v_cvt_pk_f32_fp8_sdwa v[72:73], v177 src0_sel:WORD_1
	v_cvt_pk_f32_fp8_e32 v[74:75], v179
	v_cvt_pk_f32_fp8_e32 v[80:81], v180
	s_waitcnt vmcnt(63)
	v_cvt_pk_f32_fp8_sdwa v[86:87], v181 src0_sel:WORD_1
	v_cvt_pk_f32_fp8_sdwa v[82:83], v180 src0_sel:WORD_1
	v_cvt_pk_f32_fp8_e32 v[84:85], v181
	v_mov_b32_e32 v194, v64
	v_mov_b32_e32 v195, v78
	v_lshlrev_b32_e32 v181, 16, v51
	v_lshlrev_b32_e32 v180, 16, v50
	v_and_b32_e32 v189, 0xffff0000, v51
	v_and_b32_e32 v188, 0xffff0000, v50
	v_mov_b32_e32 v50, v74
	v_mov_b32_e32 v51, v72
	v_pk_mul_f32 v[194:195], v[194:195], v[68:69] op_sel:[0,1] op_sel_hi:[1,0]
	v_mov_b32_e32 v200, v80
	v_mov_b32_e32 v201, v86
	v_mov_b32_e32 v78, v65
	v_pk_fma_f32 v[50:51], v[50:51], v[68:69], v[194:195]
	v_mov_b32_e32 v194, v84
	v_mov_b32_e32 v195, v82
	v_pk_mul_f32 v[200:201], v[200:201], v[66:67] op_sel:[0,1] op_sel_hi:[1,0]
	v_mov_b32_e32 v72, v75
	v_pk_mul_f32 v[64:65], v[78:79], v[68:69] op_sel:[0,1] op_sel_hi:[1,0]
	v_mov_b32_e32 v86, v81
	v_pk_fma_f32 v[194:195], v[194:195], v[66:67], v[200:201]
	v_pk_fma_f32 v[64:65], v[72:73], v[68:69], v[64:65]
	v_mov_b32_e32 v82, v85
	v_pk_mul_f32 v[72:73], v[86:87], v[66:67] op_sel:[0,1] op_sel_hi:[1,0]
	v_pk_add_f32 v[50:51], v[50:51], v[194:195]
	v_pk_fma_f32 v[72:73], v[82:83], v[66:67], v[72:73]
	v_pk_add_f32 v[50:51], v[50:51], v[180:181]
	v_pk_add_f32 v[64:65], v[64:65], v[72:73]
	v_and_b32_sdwa v73, v50, v129 dst_sel:DWORD dst_unused:UNUSED_PAD src0_sel:WORD_1 src1_sel:DWORD
	v_pk_add_f32 v[64:65], v[64:65], v[188:189]
	v_add3_u32 v74, v50, v73, s4
	v_and_b32_sdwa v73, v65, v129 dst_sel:DWORD dst_unused:UNUSED_PAD src0_sel:WORD_1 src1_sel:DWORD
	v_and_b32_sdwa v75, v64, v129 dst_sel:DWORD dst_unused:UNUSED_PAD src0_sel:WORD_1 src1_sel:DWORD
	v_and_b32_sdwa v72, v51, v129 dst_sel:DWORD dst_unused:UNUSED_PAD src0_sel:WORD_1 src1_sel:DWORD
	v_add3_u32 v73, v65, v73, s4
	v_add3_u32 v75, v64, v75, s4
	v_add3_u32 v72, v51, v72, s4
	v_and_b32_e32 v73, 0xffff0000, v73
	v_and_b32_e32 v75, 0xffff0000, v75
	v_or_b32_sdwa v73, v73, v72 dst_sel:DWORD dst_unused:UNUSED_PAD src0_sel:DWORD src1_sel:WORD_1
	v_or_b32_sdwa v72, v75, v74 dst_sel:DWORD dst_unused:UNUSED_PAD src0_sel:DWORD src1_sel:WORD_1
	global_store_dwordx2 v[30:31], v[72:73], off offset:1024
	v_pk_mul_f32 v[72:73], v[64:65], v[64:65]
	s_nop 0
	v_pk_fma_f32 v[80:81], v[50:51], v[50:51], v[72:73]
	v_cvt_pk_f32_fp8_e32 v[72:73], v169
	v_cvt_pk_f32_fp8_sdwa v[82:83], v171 src0_sel:WORD_1
	v_cvt_pk_f32_fp8_sdwa v[74:75], v169 src0_sel:WORD_1
	v_cvt_pk_f32_fp8_e32 v[78:79], v171
	v_cvt_pk_f32_fp8_e32 v[84:85], v172
	v_cvt_pk_f32_fp8_sdwa v[86:87], v172 src0_sel:WORD_1
	s_waitcnt vmcnt(63)
	v_cvt_pk_f32_fp8_e32 v[180:181], v173
	v_cvt_pk_f32_fp8_sdwa v[172:173], v173 src0_sel:WORD_1
	v_mov_b32_e32 v200, v72
	v_mov_b32_e32 v201, v82
	v_lshlrev_b32_e32 v189, 16, v47
	v_lshlrev_b32_e32 v188, 16, v46
	v_and_b32_e32 v195, 0xffff0000, v47
	v_and_b32_e32 v194, 0xffff0000, v46
	v_mov_b32_e32 v46, v78
	v_mov_b32_e32 v47, v74
	v_pk_mul_f32 v[200:201], v[200:201], v[68:69] op_sel:[0,1] op_sel_hi:[1,0]
	v_mov_b32_e32 v202, v84
	v_mov_b32_e32 v203, v172
	v_mov_b32_e32 v82, v73
	v_pk_fma_f32 v[46:47], v[46:47], v[68:69], v[200:201]
	v_mov_b32_e32 v200, v180
	v_mov_b32_e32 v201, v86
	v_pk_mul_f32 v[202:203], v[202:203], v[66:67] op_sel:[0,1] op_sel_hi:[1,0]
	v_mov_b32_e32 v74, v79
	v_pk_mul_f32 v[72:73], v[82:83], v[68:69] op_sel:[0,1] op_sel_hi:[1,0]
	v_mov_b32_e32 v172, v85
	v_pk_fma_f32 v[200:201], v[200:201], v[66:67], v[202:203]
	v_pk_fma_f32 v[72:73], v[74:75], v[68:69], v[72:73]
	v_mov_b32_e32 v86, v181
	v_pk_mul_f32 v[74:75], v[172:173], v[66:67] op_sel:[0,1] op_sel_hi:[1,0]
	v_pk_add_f32 v[46:47], v[46:47], v[200:201]
	v_pk_fma_f32 v[74:75], v[86:87], v[66:67], v[74:75]
	v_pk_add_f32 v[46:47], v[46:47], v[188:189]
	v_pk_add_f32 v[72:73], v[72:73], v[74:75]
	v_and_b32_sdwa v75, v46, v129 dst_sel:DWORD dst_unused:UNUSED_PAD src0_sel:WORD_1 src1_sel:DWORD
	v_pk_add_f32 v[72:73], v[72:73], v[194:195]
	v_add3_u32 v78, v46, v75, s4
	v_and_b32_sdwa v75, v73, v129 dst_sel:DWORD dst_unused:UNUSED_PAD src0_sel:WORD_1 src1_sel:DWORD
	v_and_b32_sdwa v79, v72, v129 dst_sel:DWORD dst_unused:UNUSED_PAD src0_sel:WORD_1 src1_sel:DWORD
	v_and_b32_sdwa v74, v47, v129 dst_sel:DWORD dst_unused:UNUSED_PAD src0_sel:WORD_1 src1_sel:DWORD
	v_add3_u32 v75, v73, v75, s4
	v_add3_u32 v79, v72, v79, s4
	v_add3_u32 v74, v47, v74, s4
	v_and_b32_e32 v75, 0xffff0000, v75
	v_and_b32_e32 v79, 0xffff0000, v79
	v_or_b32_sdwa v75, v75, v74 dst_sel:DWORD dst_unused:UNUSED_PAD src0_sel:DWORD src1_sel:WORD_1
	v_or_b32_sdwa v74, v79, v78 dst_sel:DWORD dst_unused:UNUSED_PAD src0_sel:DWORD src1_sel:WORD_1
	global_store_dwordx2 v[30:31], v[74:75], off offset:1536
	v_pk_mul_f32 v[74:75], v[72:73], v[72:73]
	s_nop 0
	v_pk_fma_f32 v[86:87], v[46:47], v[46:47], v[74:75]
	v_cvt_pk_f32_fp8_e32 v[74:75], v162
	v_cvt_pk_f32_fp8_sdwa v[84:85], v163 src0_sel:WORD_1
	v_cvt_pk_f32_fp8_sdwa v[78:79], v162 src0_sel:WORD_1
	v_cvt_pk_f32_fp8_e32 v[82:83], v163
	v_cvt_pk_f32_fp8_e32 v[162:163], v164
	v_cvt_pk_f32_fp8_sdwa v[172:173], v164 src0_sel:WORD_1
	s_waitcnt vmcnt(63)
	v_cvt_pk_f32_fp8_e32 v[180:181], v165
	v_cvt_pk_f32_fp8_sdwa v[164:165], v165 src0_sel:WORD_1
	v_mov_b32_e32 v200, v74
	v_mov_b32_e32 v201, v84
	v_lshlrev_b32_e32 v189, 16, v43
	v_lshlrev_b32_e32 v188, 16, v42
	v_and_b32_e32 v195, 0xffff0000, v43
	v_and_b32_e32 v194, 0xffff0000, v42
	v_mov_b32_e32 v42, v82
	v_mov_b32_e32 v43, v78
	v_pk_mul_f32 v[200:201], v[200:201], v[68:69] op_sel:[0,1] op_sel_hi:[1,0]
	v_mov_b32_e32 v202, v162
	v_mov_b32_e32 v203, v164
	v_mov_b32_e32 v84, v75
	v_pk_fma_f32 v[42:43], v[42:43], v[68:69], v[200:201]
	v_mov_b32_e32 v200, v180
	v_mov_b32_e32 v201, v172
	v_pk_mul_f32 v[202:203], v[202:203], v[66:67] op_sel:[0,1] op_sel_hi:[1,0]
	v_mov_b32_e32 v78, v83
	v_pk_mul_f32 v[74:75], v[84:85], v[68:69] op_sel:[0,1] op_sel_hi:[1,0]
	v_mov_b32_e32 v164, v163
	v_pk_fma_f32 v[200:201], v[200:201], v[66:67], v[202:203]
	v_pk_fma_f32 v[74:75], v[78:79], v[68:69], v[74:75]
	v_mov_b32_e32 v172, v181
	v_pk_mul_f32 v[78:79], v[164:165], v[66:67] op_sel:[0,1] op_sel_hi:[1,0]
	v_pk_add_f32 v[42:43], v[42:43], v[200:201]
	v_pk_fma_f32 v[78:79], v[172:173], v[66:67], v[78:79]
	v_pk_add_f32 v[42:43], v[42:43], v[188:189]
	v_pk_add_f32 v[74:75], v[74:75], v[78:79]
	v_and_b32_sdwa v79, v42, v129 dst_sel:DWORD dst_unused:UNUSED_PAD src0_sel:WORD_1 src1_sel:DWORD
	v_pk_add_f32 v[74:75], v[74:75], v[194:195]
	v_add3_u32 v82, v42, v79, s4
	v_and_b32_sdwa v79, v75, v129 dst_sel:DWORD dst_unused:UNUSED_PAD src0_sel:WORD_1 src1_sel:DWORD
	v_and_b32_sdwa v83, v74, v129 dst_sel:DWORD dst_unused:UNUSED_PAD src0_sel:WORD_1 src1_sel:DWORD
	v_and_b32_sdwa v78, v43, v129 dst_sel:DWORD dst_unused:UNUSED_PAD src0_sel:WORD_1 src1_sel:DWORD
	v_add3_u32 v79, v75, v79, s4
	v_add3_u32 v83, v74, v83, s4
	v_add3_u32 v78, v43, v78, s4
	v_and_b32_e32 v79, 0xffff0000, v79
	v_and_b32_e32 v83, 0xffff0000, v83
	v_or_b32_sdwa v79, v79, v78 dst_sel:DWORD dst_unused:UNUSED_PAD src0_sel:DWORD src1_sel:WORD_1
	v_or_b32_sdwa v78, v83, v82 dst_sel:DWORD dst_unused:UNUSED_PAD src0_sel:DWORD src1_sel:WORD_1
	global_store_dwordx2 v[30:31], v[78:79], off offset:2048
	v_pk_mul_f32 v[78:79], v[74:75], v[74:75]
	s_nop 0
	v_pk_fma_f32 v[162:163], v[42:43], v[42:43], v[78:79]
	v_cvt_pk_f32_fp8_e32 v[78:79], v154
	v_cvt_pk_f32_fp8_sdwa v[82:83], v154 src0_sel:WORD_1
	v_cvt_pk_f32_fp8_e32 v[84:85], v155
	v_cvt_pk_f32_fp8_sdwa v[154:155], v155 src0_sel:WORD_1
	v_cvt_pk_f32_fp8_e32 v[164:165], v156
	v_cvt_pk_f32_fp8_sdwa v[172:173], v156 src0_sel:WORD_1
	s_waitcnt vmcnt(63)
	v_cvt_pk_f32_fp8_e32 v[180:181], v157
	v_cvt_pk_f32_fp8_sdwa v[156:157], v157 src0_sel:WORD_1
	v_mov_b32_e32 v200, v78
	v_mov_b32_e32 v201, v154
	v_lshlrev_b32_e32 v189, 16, v37
	v_lshlrev_b32_e32 v188, 16, v36
	v_and_b32_e32 v195, 0xffff0000, v37
	v_and_b32_e32 v194, 0xffff0000, v36
	v_mov_b32_e32 v36, v84
	v_mov_b32_e32 v37, v82
	v_pk_mul_f32 v[200:201], v[200:201], v[68:69] op_sel:[0,1] op_sel_hi:[1,0]
	v_mov_b32_e32 v202, v164
	v_mov_b32_e32 v203, v156
	v_mov_b32_e32 v154, v79
	v_pk_fma_f32 v[36:37], v[36:37], v[68:69], v[200:201]
	v_mov_b32_e32 v200, v180
	v_mov_b32_e32 v201, v172
	v_pk_mul_f32 v[202:203], v[202:203], v[66:67] op_sel:[0,1] op_sel_hi:[1,0]
	v_mov_b32_e32 v82, v85
	v_pk_mul_f32 v[78:79], v[154:155], v[68:69] op_sel:[0,1] op_sel_hi:[1,0]
	v_mov_b32_e32 v156, v165
	v_pk_fma_f32 v[200:201], v[200:201], v[66:67], v[202:203]
	v_pk_fma_f32 v[78:79], v[82:83], v[68:69], v[78:79]
	v_mov_b32_e32 v172, v181
	v_pk_mul_f32 v[82:83], v[156:157], v[66:67] op_sel:[0,1] op_sel_hi:[1,0]
	v_pk_add_f32 v[36:37], v[36:37], v[200:201]
	v_pk_fma_f32 v[82:83], v[172:173], v[66:67], v[82:83]
	v_pk_add_f32 v[36:37], v[36:37], v[188:189]
	v_pk_add_f32 v[78:79], v[78:79], v[82:83]
	v_and_b32_sdwa v83, v36, v129 dst_sel:DWORD dst_unused:UNUSED_PAD src0_sel:WORD_1 src1_sel:DWORD
	v_pk_add_f32 v[78:79], v[78:79], v[194:195]
	v_add3_u32 v84, v36, v83, s4
	v_and_b32_sdwa v83, v79, v129 dst_sel:DWORD dst_unused:UNUSED_PAD src0_sel:WORD_1 src1_sel:DWORD
	v_and_b32_sdwa v85, v78, v129 dst_sel:DWORD dst_unused:UNUSED_PAD src0_sel:WORD_1 src1_sel:DWORD
	v_and_b32_sdwa v82, v37, v129 dst_sel:DWORD dst_unused:UNUSED_PAD src0_sel:WORD_1 src1_sel:DWORD
	v_add3_u32 v83, v79, v83, s4
	v_add3_u32 v85, v78, v85, s4
	v_add3_u32 v82, v37, v82, s4
	v_and_b32_e32 v83, 0xffff0000, v83
	v_and_b32_e32 v85, 0xffff0000, v85
	v_or_b32_sdwa v83, v83, v82 dst_sel:DWORD dst_unused:UNUSED_PAD src0_sel:DWORD src1_sel:WORD_1
	v_or_b32_sdwa v82, v85, v84 dst_sel:DWORD dst_unused:UNUSED_PAD src0_sel:DWORD src1_sel:WORD_1
	global_store_dwordx2 v[30:31], v[82:83], off offset:2560
	v_pk_mul_f32 v[82:83], v[78:79], v[78:79]
	s_nop 0
	v_pk_fma_f32 v[154:155], v[36:37], v[36:37], v[82:83]
	v_cvt_pk_f32_fp8_e32 v[84:85], v145
	v_cvt_pk_f32_fp8_sdwa v[164:165], v146 src0_sel:WORD_1
	v_cvt_pk_f32_fp8_sdwa v[144:145], v145 src0_sel:WORD_1
	v_cvt_pk_f32_fp8_e32 v[156:157], v146
	v_cvt_pk_f32_fp8_e32 v[172:173], v147
	s_waitcnt vmcnt(63)
	v_cvt_pk_f32_fp8_sdwa v[188:189], v148 src0_sel:WORD_1
	v_cvt_pk_f32_fp8_sdwa v[146:147], v147 src0_sel:WORD_1
	v_cvt_pk_f32_fp8_e32 v[180:181], v148
	v_mov_b32_e32 v200, v84
	v_mov_b32_e32 v201, v164
	v_mov_b32_e32 v194, v156
	v_mov_b32_e32 v195, v144
	v_pk_mul_f32 v[200:201], v[200:201], v[68:69] op_sel:[0,1] op_sel_hi:[1,0]
	v_mov_b32_e32 v202, v172
	v_mov_b32_e32 v203, v188
	v_mov_b32_e32 v164, v85
	v_pk_fma_f32 v[194:195], v[194:195], v[68:69], v[200:201]
	v_mov_b32_e32 v200, v180
	v_mov_b32_e32 v201, v146
	v_pk_mul_f32 v[202:203], v[202:203], v[66:67] op_sel:[0,1] op_sel_hi:[1,0]
	v_mov_b32_e32 v144, v157
	v_pk_mul_f32 v[84:85], v[164:165], v[68:69] op_sel:[0,1] op_sel_hi:[1,0]
	v_mov_b32_e32 v188, v173
	v_pk_fma_f32 v[200:201], v[200:201], v[66:67], v[202:203]
	v_pk_fma_f32 v[84:85], v[144:145], v[68:69], v[84:85]
	v_mov_b32_e32 v146, v181
	v_pk_mul_f32 v[144:145], v[188:189], v[66:67] op_sel:[0,1] op_sel_hi:[1,0]
	v_lshlrev_b32_e32 v83, 16, v33
	v_lshlrev_b32_e32 v82, 16, v32
	v_pk_add_f32 v[194:195], v[194:195], v[200:201]
	v_pk_fma_f32 v[144:145], v[146:147], v[66:67], v[144:145]
	v_and_b32_e32 v33, 0xffff0000, v33
	v_and_b32_e32 v32, 0xffff0000, v32
	v_pk_add_f32 v[82:83], v[194:195], v[82:83]
	v_pk_add_f32 v[84:85], v[84:85], v[144:145]
	s_nop 0
	v_pk_add_f32 v[84:85], v[84:85], v[32:33]
	v_and_b32_sdwa v33, v82, v129 dst_sel:DWORD dst_unused:UNUSED_PAD src0_sel:WORD_1 src1_sel:DWORD
	v_add3_u32 v134, v82, v33, s4
	v_and_b32_sdwa v33, v85, v129 dst_sel:DWORD dst_unused:UNUSED_PAD src0_sel:WORD_1 src1_sel:DWORD
	v_and_b32_sdwa v136, v84, v129 dst_sel:DWORD dst_unused:UNUSED_PAD src0_sel:WORD_1 src1_sel:DWORD
	v_and_b32_sdwa v32, v83, v129 dst_sel:DWORD dst_unused:UNUSED_PAD src0_sel:WORD_1 src1_sel:DWORD
	v_add3_u32 v33, v85, v33, s4
	v_add3_u32 v136, v84, v136, s4
	v_add3_u32 v32, v83, v32, s4
	v_and_b32_e32 v33, 0xffff0000, v33
	v_and_b32_e32 v136, 0xffff0000, v136
	v_or_b32_sdwa v33, v33, v32 dst_sel:DWORD dst_unused:UNUSED_PAD src0_sel:DWORD src1_sel:WORD_1
	v_or_b32_sdwa v32, v136, v134 dst_sel:DWORD dst_unused:UNUSED_PAD src0_sel:DWORD src1_sel:WORD_1
	global_store_dwordx2 v[30:31], v[32:33], off offset:3072
	v_pk_mul_f32 v[32:33], v[84:85], v[84:85]
	s_nop 0
	v_pk_fma_f32 v[144:145], v[82:83], v[82:83], v[32:33]
	v_cvt_pk_f32_fp8_e32 v[32:33], v132
	v_cvt_pk_f32_fp8_e32 v[156:157], v135
	v_cvt_pk_f32_fp8_sdwa v[134:135], v135 src0_sel:WORD_1
	v_cvt_pk_f32_fp8_sdwa v[146:147], v132 src0_sel:WORD_1
	v_cvt_pk_f32_fp8_e32 v[164:165], v137
	s_waitcnt vmcnt(63)
	v_cvt_pk_f32_fp8_sdwa v[180:181], v138 src0_sel:WORD_1
	v_cvt_pk_f32_fp8_sdwa v[136:137], v137 src0_sel:WORD_1
	v_cvt_pk_f32_fp8_e32 v[172:173], v138
	v_mov_b32_e32 v200, v32
	v_mov_b32_e32 v201, v134
	v_lshlrev_b32_e32 v189, 16, v27
	v_lshlrev_b32_e32 v188, 16, v26
	v_and_b32_e32 v195, 0xffff0000, v27
	v_and_b32_e32 v194, 0xffff0000, v26
	v_mov_b32_e32 v26, v156
	v_mov_b32_e32 v27, v146
	v_pk_mul_f32 v[200:201], v[200:201], v[68:69] op_sel:[0,1] op_sel_hi:[1,0]
	v_mov_b32_e32 v202, v164
	v_mov_b32_e32 v203, v180
	v_mov_b32_e32 v134, v33
	v_pk_fma_f32 v[26:27], v[26:27], v[68:69], v[200:201]
	v_mov_b32_e32 v200, v172
	v_mov_b32_e32 v201, v136
	v_pk_mul_f32 v[202:203], v[202:203], v[66:67] op_sel:[0,1] op_sel_hi:[1,0]
	v_mov_b32_e32 v146, v157
	v_pk_mul_f32 v[32:33], v[134:135], v[68:69] op_sel:[0,1] op_sel_hi:[1,0]
	v_mov_b32_e32 v180, v165
	v_pk_fma_f32 v[200:201], v[200:201], v[66:67], v[202:203]
	v_pk_fma_f32 v[32:33], v[146:147], v[68:69], v[32:33]
	v_mov_b32_e32 v136, v173
	v_pk_mul_f32 v[68:69], v[180:181], v[66:67] op_sel:[0,1] op_sel_hi:[1,0]
	v_pk_add_f32 v[26:27], v[26:27], v[200:201]
	v_pk_fma_f32 v[66:67], v[136:137], v[66:67], v[68:69]
	v_pk_add_f32 v[26:27], v[26:27], v[188:189]
	v_pk_add_f32 v[32:33], v[32:33], v[66:67]
	v_and_b32_sdwa v67, v26, v129 dst_sel:DWORD dst_unused:UNUSED_PAD src0_sel:WORD_1 src1_sel:DWORD
	v_pk_add_f32 v[32:33], v[32:33], v[194:195]
	v_add3_u32 v68, v26, v67, s4
	v_and_b32_sdwa v67, v33, v129 dst_sel:DWORD dst_unused:UNUSED_PAD src0_sel:WORD_1 src1_sel:DWORD
	v_and_b32_sdwa v69, v32, v129 dst_sel:DWORD dst_unused:UNUSED_PAD src0_sel:WORD_1 src1_sel:DWORD
	v_and_b32_sdwa v66, v27, v129 dst_sel:DWORD dst_unused:UNUSED_PAD src0_sel:WORD_1 src1_sel:DWORD
	v_add3_u32 v67, v33, v67, s4
	v_add3_u32 v69, v32, v69, s4
	v_add3_u32 v66, v27, v66, s4
	v_and_b32_e32 v67, 0xffff0000, v67
	v_and_b32_e32 v69, 0xffff0000, v69
	v_or_b32_sdwa v67, v67, v66 dst_sel:DWORD dst_unused:UNUSED_PAD src0_sel:DWORD src1_sel:WORD_1
	v_or_b32_sdwa v66, v69, v68 dst_sel:DWORD dst_unused:UNUSED_PAD src0_sel:DWORD src1_sel:WORD_1
	global_store_dwordx2 v[30:31], v[66:67], off offset:3584
	v_add_f32_e32 v66, v76, v77
	v_add_f32_e32 v67, v70, v71
	v_add_f32_e32 v66, v67, v66
	v_add_f32_e32 v67, v80, v81
	v_add_f32_e32 v66, v66, v67
	v_add_f32_e32 v67, v86, v87
	v_add_f32_e32 v66, v66, v67
	v_add_f32_e32 v67, v162, v163
	v_pk_mul_f32 v[30:31], v[32:33], v[32:33]
	v_add_f32_e32 v66, v66, v67
	v_add_f32_e32 v67, v154, v155
	v_pk_fma_f32 v[30:31], v[26:27], v[26:27], v[30:31]
	v_add_f32_e32 v66, v66, v67
	v_add_f32_e32 v67, v144, v145
	v_add_f32_e32 v66, v66, v67
	v_add_f32_e32 v30, v30, v31
	v_add_f32_e32 v30, v66, v30
	v_mov_b64_e32 v[66:67], v[212:213]
	v_mov_b64_e32 v[68:69], v[214:215]
	ds_bpermute_b32 v31, v1, v30
	s_waitcnt lgkmcnt(0)
	v_add_f32_e32 v30, v30, v31
	ds_bpermute_b32 v31, v90, v30
	s_waitcnt lgkmcnt(0)
	v_add_f32_e32 v30, v30, v31
	ds_bpermute_b32 v31, v91, v30
	s_waitcnt lgkmcnt(0)
	v_add_f32_e32 v30, v30, v31
	ds_bpermute_b32 v31, v92, v30
	s_waitcnt lgkmcnt(0)
	v_add_f32_e32 v30, v30, v31
	ds_bpermute_b32 v31, v93, v30
	s_waitcnt lgkmcnt(0)
	v_add_f32_e32 v30, v30, v31
	ds_bpermute_b32 v31, v94, v30
	s_waitcnt lgkmcnt(0)
	v_add_f32_e32 v30, v30, v31
	v_fmamk_f32 v30, v30, 0x3a000000, v127
	v_mul_f32_e32 v31, 0x4f800000, v30
	v_cmp_gt_f32_e32 vcc, s19, v30
	s_nop 1
	v_cndmask_b32_e32 v30, v30, v31, vcc
	v_sqrt_f32_e32 v31, v30
	s_nop 0
	v_add_u32_e32 v70, -1, v31
	v_add_u32_e32 v71, 1, v31
	v_fma_f32 v76, -v70, v31, v30
	v_fma_f32 v77, -v71, v31, v30
	v_cmp_ge_f32_e64 s[8:9], 0, v76
	s_nop 1
	v_cndmask_b32_e64 v31, v31, v70, s[8:9]
	v_cmp_lt_f32_e64 s[8:9], 0, v77
	s_nop 1
	v_cndmask_b32_e64 v31, v31, v71, s[8:9]
	v_mul_f32_e32 v70, 0x37800000, v31
	v_cndmask_b32_e32 v31, v31, v70, vcc
	v_cmp_class_f32_e32 vcc, v30, v128
	v_mov_b32_e32 v71, 0
	s_nop 0
	v_cndmask_b32_e32 v30, v31, v30, vcc
	v_div_scale_f32 v31, s[0:1], v30, v30, 1.0
	v_rcp_f32_e32 v70, v31
	v_div_scale_f32 v76, vcc, 1.0, v30, 1.0
	v_fma_f32 v77, -v31, v70, 1.0
	v_fmac_f32_e32 v70, v77, v70
	v_mul_f32_e32 v77, v76, v70
	v_fma_f32 v80, -v31, v77, v76
	v_fmac_f32_e32 v77, v80, v70
	v_fma_f32 v31, -v31, v77, v76
	v_div_fmas_f32 v31, v31, v70, v77
	v_div_fixup_f32 v70, v31, v30, 1.0
	v_mul_f32_e32 v30, v70, v40
	v_mul_f32_e32 v31, v70, v54

	v_mul_f32_e32 v30, v66, v30
	v_mul_f32_e32 v31, v67, v31
	v_cvt_pk_fp8_f32 v71, v30, v31
	v_mul_f32_e32 v40, v70, v41
	v_mul_f32_e32 v30, v70, v55
	v_mul_f32_e32 v31, v68, v40
	v_mul_f32_e32 v30, v69, v30
	v_cvt_pk_fp8_f32 v71, v31, v30 op_sel:[0,0,1]
	v_mul_f32_e32 v31, v70, v56
	v_mul_f32_e32 v40, v70, v60
	v_mov_b32_e32 v30, 0
	global_store_dword v[24:25], v71, off offset:2048
	v_mov_b64_e32 v[66:67], v[216:217]
	v_mov_b64_e32 v[68:69], v[218:219]
	v_mul_f32_e32 v41, v70, v57
	v_mul_f32_e32 v37, v70, v37
	v_mul_f32_e32 v26, v70, v26
	v_mul_f32_e32 v32, v70, v32
	v_mul_f32_e32 v27, v70, v27
	s_waitcnt vmcnt(41)
	v_cvt_pk_f32_fp8_e32 v[76:77], v190

	v_mul_f32_e32 v31, v66, v31
	v_mul_f32_e32 v40, v67, v40
	v_cvt_pk_fp8_f32 v30, v31, v40
	v_mul_f32_e32 v31, v70, v61
	v_mul_f32_e32 v40, v68, v41
	v_mul_f32_e32 v31, v69, v31
	v_cvt_pk_fp8_f32 v30, v40, v31 op_sel:[0,0,1]
	v_mul_f32_e32 v31, v70, v50
	v_mul_f32_e32 v40, v70, v64
	v_mul_f32_e32 v41, v70, v51
	global_store_dword v[24:25], v30, off offset:2304
	v_mov_b64_e32 v[54:55], v[220:221]
	v_mov_b64_e32 v[56:57], v[222:223]
	v_mov_b32_e32 v30, 0
	v_mov_b32_e32 v68, 0
	ds_bpermute_b32 v50, v118, v130
	s_waitcnt lgkmcnt(0)
	v_ashrrev_i32_e32 v51, 31, v50
	v_lshlrev_b64 v[50:51], 11, v[50:51]
	v_lshl_add_u64 v[50:51], v[4:5], 0, v[50:51]

	v_mul_f32_e32 v31, v54, v31
	v_mul_f32_e32 v40, v55, v40
	v_cvt_pk_fp8_f32 v30, v31, v40
	v_mul_f32_e32 v31, v70, v65
	v_mul_f32_e32 v40, v56, v41
	v_mul_f32_e32 v31, v57, v31
	v_cvt_pk_fp8_f32 v30, v40, v31 op_sel:[0,0,1]
	v_mul_f32_e32 v31, v70, v46
	v_mul_f32_e32 v40, v70, v72
	v_mul_f32_e32 v41, v70, v47
	global_store_dword v[24:25], v30, off offset:2560
	v_mov_b64_e32 v[54:55], v[224:225]
	v_mov_b64_e32 v[56:57], v[226:227]
	v_mov_b32_e32 v30, 0
	ds_bpermute_b32 v46, v117, v130
	s_waitcnt lgkmcnt(0)
	v_ashrrev_i32_e32 v47, 31, v46
	v_lshlrev_b64 v[46:47], 11, v[46:47]
	v_lshl_add_u64 v[64:65], v[4:5], 0, v[46:47]

	v_mul_f32_e32 v31, v54, v31
	v_mul_f32_e32 v40, v55, v40
	v_cvt_pk_fp8_f32 v30, v31, v40
	v_mul_f32_e32 v31, v70, v73
	v_mul_f32_e32 v40, v56, v41
	v_mul_f32_e32 v31, v57, v31
	v_cvt_pk_fp8_f32 v30, v40, v31 op_sel:[0,0,1]
	v_mul_f32_e32 v31, v70, v42
	v_mul_f32_e32 v40, v70, v74
	v_mul_f32_e32 v41, v70, v43
	global_store_dword v[24:25], v30, off offset:2816
	v_mov_b64_e32 v[54:55], v[228:229]
	v_mov_b64_e32 v[56:57], v[230:231]
	v_mov_b32_e32 v30, 0
	s_waitcnt vmcnt(36)
	v_cvt_pk_f32_fp8_e32 v[72:73], v191

	v_mul_f32_e32 v31, v54, v31
	v_mul_f32_e32 v40, v55, v40
	v_cvt_pk_fp8_f32 v30, v31, v40
	v_mul_f32_e32 v31, v70, v75
	v_mul_f32_e32 v40, v56, v41
	v_mul_f32_e32 v31, v57, v31
	v_cvt_pk_fp8_f32 v30, v40, v31 op_sel:[0,0,1]
	v_mul_f32_e32 v31, v70, v36
	v_mul_f32_e32 v36, v70, v78
	ds_bpermute_b32 v54, v119, v130
	global_store_dword v[24:25], v30, off offset:3072
	v_mov_b64_e32 v[40:41], v[232:233]
	v_mov_b64_e32 v[42:43], v[234:235]
	v_mov_b32_e32 v30, 0
	v_cvt_pk_f32_fp8_sdwa v[74:75], v191 src0_sel:WORD_1
	s_waitcnt lgkmcnt(0)
	v_ashrrev_i32_e32 v55, 31, v54
	v_lshlrev_b64 v[54:55], 11, v[54:55]
	v_lshl_add_u64 v[66:67], v[4:5], 0, v[54:55]

	v_mul_f32_e32 v31, v40, v31
	v_mul_f32_e32 v36, v41, v36
	v_cvt_pk_fp8_f32 v30, v31, v36
	v_mul_f32_e32 v31, v70, v79
	v_mul_f32_e32 v36, v42, v37
	v_mul_f32_e32 v31, v43, v31
	v_cvt_pk_fp8_f32 v30, v36, v31 op_sel:[0,0,1]
	v_mul_f32_e32 v31, v70, v82
	v_mul_f32_e32 v36, v70, v84
	v_mul_f32_e32 v37, v70, v83
	global_store_dword v[24:25], v30, off offset:3328
	v_mov_b64_e32 v[40:41], v[236:237]
	v_mov_b64_e32 v[42:43], v[238:239]
	v_mov_b32_e32 v30, 0
	v_cvt_pk_f32_fp8_sdwa v[78:79], v190 src0_sel:WORD_1
	v_mov_b32_e32 v84, v72

	v_mul_f32_e32 v31, v40, v31
	v_mul_f32_e32 v36, v41, v36
	v_cvt_pk_fp8_f32 v30, v31, v36
	v_mul_f32_e32 v31, v70, v85
	v_mul_f32_e32 v36, v42, v37
	v_mul_f32_e32 v31, v43, v31
	v_cvt_pk_fp8_f32 v30, v36, v31 op_sel:[0,0,1]
	ds_bpermute_b32 v36, v116, v130
	v_mov_b32_e32 v85, v78
	v_mov_b32_e32 v78, v73
	global_store_dword v[24:25], v30, off offset:3584
	v_mov_b64_e32 v[40:41], v[240:241]
	v_mov_b64_e32 v[42:43], v[242:243]
	v_add_co_u32_e32 v30, vcc, s34, v20
	s_waitcnt lgkmcnt(0)
	v_ashrrev_i32_e32 v37, 31, v36
	v_addc_co_u32_e32 v31, vcc, 0, v21, vcc
	v_lshlrev_b64 v[36:37], 11, v[36:37]
	v_add_co_u32_e32 v56, vcc, s37, v20
	v_lshl_add_u64 v[60:61], v[4:5], 0, v[36:37]
	s_nop 0
	v_addc_co_u32_e32 v57, vcc, 0, v21, vcc
	v_add_co_u32_e32 v72, vcc, s35, v20

	v_mul_f32_e32 v26, v40, v26
	v_mul_f32_e32 v32, v41, v32
	v_cvt_pk_fp8_f32 v68, v26, v32
	v_mul_f32_e32 v26, v70, v33
	v_mul_f32_e32 v27, v42, v27
	v_mul_f32_e32 v26, v43, v26
	v_cvt_pk_fp8_f32 v68, v27, v26 op_sel:[0,0,1]
	s_waitcnt vmcnt(31)
	v_cvt_pk_f32_fp8_sdwa v[70:71], v193 src0_sel:WORD_1
	v_addc_co_u32_e32 v73, vcc, 0, v21, vcc
	global_store_dword v[24:25], v68, off offset:3840
	global_load_dwordx2 v[54:55], v[30:31], off offset:512
	global_load_dwordx2 v[46:47], v[30:31], off offset:1024
	global_load_dwordx2 v[42:43], v[30:31], off offset:1536
	global_load_dwordx2 v[40:41], v[30:31], off offset:2048
	global_load_dwordx2 v[36:37], v[30:31], off offset:2560
	global_load_dwordx2 v[32:33], v[30:31], off offset:3072
	global_load_dwordx2 v[26:27], v[30:31], off offset:3584
	global_load_dword v188, v[60:61], off
	global_load_dword v180, v[60:61], off offset:256
	global_load_dword v172, v[60:61], off offset:512
	global_load_dword v164, v[60:61], off offset:768
	global_load_dword v156, v[60:61], off offset:1024
	global_load_dword v147, v[60:61], off offset:1280
	global_load_dword v142, v[60:61], off offset:1536
	global_load_dword v132, v[60:61], off offset:1792
	global_load_dword v189, v[64:65], off
	global_load_dword v181, v[64:65], off offset:256
	global_load_dword v173, v[64:65], off offset:512
	global_load_dword v165, v[64:65], off offset:768
	global_load_dword v157, v[64:65], off offset:1024
	global_load_dword v152, v[64:65], off offset:1280
	global_load_dword v144, v[64:65], off offset:1536
	global_load_dword v134, v[64:65], off offset:1792
	global_load_dword v192, v[50:51], off
	global_load_dword v185, v[50:51], off offset:256
	global_load_dword v177, v[50:51], off offset:512
	global_load_dword v169, v[50:51], off offset:768
	global_load_dword v162, v[50:51], off offset:1024
	global_load_dword v154, v[50:51], off offset:1280
	global_load_dword v145, v[50:51], off offset:1536
	global_load_dword v135, v[50:51], off offset:1792
	global_load_dword v194, v[66:67], off
	global_load_dwordx2 v[60:61], v[56:57], off offset:-4096
	global_load_dword v187, v[66:67], off offset:256
	global_load_dword v179, v[66:67], off offset:512
	global_load_dword v171, v[66:67], off offset:768
	global_load_dword v163, v[66:67], off offset:1024
	global_load_dword v155, v[66:67], off offset:1280
	global_load_dword v146, v[66:67], off offset:1536
	global_load_dword v136, v[66:67], off offset:1792
	ds_bpermute_b32 v67, v112, v19
	ds_bpermute_b32 v66, v113, v19
	s_waitcnt vmcnt(63)
	v_cvt_pk_f32_fp8_e32 v[30:31], v196
	ds_bpermute_b32 v65, v114, v19
	ds_bpermute_b32 v64, v115, v19
	v_cvt_pk_f32_fp8_sdwa v[50:51], v196 src0_sel:WORD_1
	v_cvt_pk_f32_fp8_e32 v[68:69], v193
	v_mov_b32_e32 v82, v30
	v_mov_b32_e32 v83, v70
	v_mov_b32_e32 v70, v31
	v_mov_b32_e32 v80, v68
	v_mov_b32_e32 v81, v50
	s_waitcnt lgkmcnt(2)
	v_pk_mul_f32 v[82:83], v[82:83], v[66:67] op_sel:[0,1] op_sel_hi:[1,0]
	v_mov_b32_e32 v50, v69
	v_pk_mul_f32 v[30:31], v[70:71], v[66:67] op_sel:[0,1] op_sel_hi:[1,0]
	v_pk_fma_f32 v[80:81], v[80:81], v[66:67], v[82:83]
	v_mov_b32_e32 v83, v74
	v_pk_fma_f32 v[30:31], v[50:51], v[66:67], v[30:31]
	v_mov_b32_e32 v74, v77
	s_waitcnt lgkmcnt(0)
	v_pk_mul_f32 v[50:51], v[78:79], v[64:65] op_sel:[0,1] op_sel_hi:[1,0]
	v_mov_b32_e32 v82, v76
	v_pk_mul_f32 v[84:85], v[84:85], v[64:65] op_sel:[0,1] op_sel_hi:[1,0]
	v_pk_fma_f32 v[50:51], v[74:75], v[64:65], v[50:51]
	s_waitcnt vmcnt(56)
	v_lshlrev_b32_e32 v25, 16, v63
	v_lshlrev_b32_e32 v24, 16, v62
	v_and_b32_e32 v63, 0xffff0000, v63
	v_and_b32_e32 v62, 0xffff0000, v62
	v_pk_fma_f32 v[82:83], v[82:83], v[64:65], v[84:85]
	v_pk_add_f32 v[30:31], v[30:31], v[50:51]
	v_pk_add_f32 v[80:81], v[80:81], v[82:83]
	v_pk_add_f32 v[50:51], v[30:31], v[62:63]
	v_pk_add_f32 v[24:25], v[80:81], v[24:25]
	v_and_b32_sdwa v62, v51, v129 dst_sel:DWORD dst_unused:UNUSED_PAD src0_sel:WORD_1 src1_sel:DWORD
	v_and_b32_sdwa v30, v25, v129 dst_sel:DWORD dst_unused:UNUSED_PAD src0_sel:WORD_1 src1_sel:DWORD
	v_and_b32_sdwa v63, v50, v129 dst_sel:DWORD dst_unused:UNUSED_PAD src0_sel:WORD_1 src1_sel:DWORD
	v_add3_u32 v62, v51, v62, s4
	v_and_b32_sdwa v31, v24, v129 dst_sel:DWORD dst_unused:UNUSED_PAD src0_sel:WORD_1 src1_sel:DWORD
	v_add3_u32 v30, v25, v30, s4
	v_add3_u32 v63, v50, v63, s4
	v_and_b32_e32 v62, 0xffff0000, v62
	v_add3_u32 v31, v24, v31, s4
	v_and_b32_e32 v68, 0xffff0000, v63
	v_or_b32_sdwa v63, v62, v30 dst_sel:DWORD dst_unused:UNUSED_PAD src0_sel:DWORD src1_sel:WORD_1
	v_add_co_u32_e32 v30, vcc, s38, v20
	v_or_b32_sdwa v62, v68, v31 dst_sel:DWORD dst_unused:UNUSED_PAD src0_sel:DWORD src1_sel:WORD_1
	s_nop 0
	v_addc_co_u32_e32 v31, vcc, 0, v21, vcc
	global_store_dwordx2 v[30:31], v[62:63], off offset:-4096
	v_pk_mul_f32 v[62:63], v[50:51], v[50:51]
	s_nop 0
	v_pk_fma_f32 v[74:75], v[24:25], v[24:25], v[62:63]
	v_cvt_pk_f32_fp8_e32 v[62:63], v186
	v_cvt_pk_f32_fp8_sdwa v[76:77], v184 src0_sel:WORD_1
	v_cvt_pk_f32_fp8_sdwa v[68:69], v186 src0_sel:WORD_1
	v_cvt_pk_f32_fp8_e32 v[70:71], v184
	v_cvt_pk_f32_fp8_e32 v[78:79], v183
	v_cvt_pk_f32_fp8_sdwa v[84:85], v182 src0_sel:WORD_1
	v_cvt_pk_f32_fp8_sdwa v[80:81], v183 src0_sel:WORD_1
	v_cvt_pk_f32_fp8_e32 v[82:83], v182
	v_mov_b32_e32 v190, v62
	v_mov_b32_e32 v191, v76
	v_lshlrev_b32_e32 v87, 16, v59
	v_lshlrev_b32_e32 v86, 16, v58
	v_and_b32_e32 v183, 0xffff0000, v59
	v_and_b32_e32 v182, 0xffff0000, v58
	v_mov_b32_e32 v58, v70
	v_mov_b32_e32 v59, v68
	v_pk_mul_f32 v[190:191], v[190:191], v[66:67] op_sel:[0,1] op_sel_hi:[1,0]
	v_mov_b32_e32 v196, v78
	v_mov_b32_e32 v197, v84
	v_mov_b32_e32 v76, v63
	v_pk_fma_f32 v[58:59], v[58:59], v[66:67], v[190:191]
	v_mov_b32_e32 v190, v82
	v_mov_b32_e32 v191, v80
	v_pk_mul_f32 v[196:197], v[196:197], v[64:65] op_sel:[0,1] op_sel_hi:[1,0]
	v_mov_b32_e32 v68, v71
	v_pk_mul_f32 v[62:63], v[76:77], v[66:67] op_sel:[0,1] op_sel_hi:[1,0]
	v_mov_b32_e32 v84, v79
	v_pk_fma_f32 v[190:191], v[190:191], v[64:65], v[196:197]
	v_pk_fma_f32 v[62:63], v[68:69], v[66:67], v[62:63]
	v_mov_b32_e32 v80, v83
	v_pk_mul_f32 v[68:69], v[84:85], v[64:65] op_sel:[0,1] op_sel_hi:[1,0]
	v_pk_add_f32 v[58:59], v[58:59], v[190:191]
	v_pk_fma_f32 v[68:69], v[80:81], v[64:65], v[68:69]
	v_pk_add_f32 v[58:59], v[58:59], v[86:87]
	v_pk_add_f32 v[62:63], v[62:63], v[68:69]
	v_and_b32_sdwa v69, v58, v129 dst_sel:DWORD dst_unused:UNUSED_PAD src0_sel:WORD_1 src1_sel:DWORD
	v_pk_add_f32 v[62:63], v[62:63], v[182:183]
	v_add3_u32 v70, v58, v69, s4
	v_and_b32_sdwa v69, v63, v129 dst_sel:DWORD dst_unused:UNUSED_PAD src0_sel:WORD_1 src1_sel:DWORD
	v_and_b32_sdwa v71, v62, v129 dst_sel:DWORD dst_unused:UNUSED_PAD src0_sel:WORD_1 src1_sel:DWORD
	v_and_b32_sdwa v68, v59, v129 dst_sel:DWORD dst_unused:UNUSED_PAD src0_sel:WORD_1 src1_sel:DWORD
	v_add3_u32 v69, v63, v69, s4
	v_add3_u32 v71, v62, v71, s4
	v_add3_u32 v68, v59, v68, s4
	v_and_b32_e32 v69, 0xffff0000, v69
	v_and_b32_e32 v71, 0xffff0000, v71
	v_or_b32_sdwa v69, v69, v68 dst_sel:DWORD dst_unused:UNUSED_PAD src0_sel:DWORD src1_sel:WORD_1
	v_or_b32_sdwa v68, v71, v70 dst_sel:DWORD dst_unused:UNUSED_PAD src0_sel:DWORD src1_sel:WORD_1
	global_store_dwordx2 v[72:73], v[68:69], off offset:512
	v_pk_mul_f32 v[68:69], v[62:63], v[62:63]
	s_nop 0
	v_pk_fma_f32 v[80:81], v[58:59], v[58:59], v[68:69]
	v_cvt_pk_f32_fp8_e32 v[68:69], v178
	v_cvt_pk_f32_fp8_sdwa v[78:79], v176 src0_sel:WORD_1
	v_cvt_pk_f32_fp8_sdwa v[70:71], v178 src0_sel:WORD_1
	v_cvt_pk_f32_fp8_e32 v[76:77], v176
	v_cvt_pk_f32_fp8_e32 v[82:83], v175
	v_cvt_pk_f32_fp8_sdwa v[84:85], v175 src0_sel:WORD_1
	v_cvt_pk_f32_fp8_e32 v[86:87], v174
	v_cvt_pk_f32_fp8_sdwa v[174:175], v174 src0_sel:WORD_1
	v_mov_b32_e32 v196, v68
	v_mov_b32_e32 v197, v78
	v_lshlrev_b32_e32 v183, 16, v53
	v_lshlrev_b32_e32 v182, 16, v52
	v_and_b32_e32 v191, 0xffff0000, v53
	v_and_b32_e32 v190, 0xffff0000, v52
	v_mov_b32_e32 v52, v76
	v_mov_b32_e32 v53, v70
	v_pk_mul_f32 v[196:197], v[196:197], v[66:67] op_sel:[0,1] op_sel_hi:[1,0]
	v_mov_b32_e32 v200, v82
	v_mov_b32_e32 v201, v174
	v_mov_b32_e32 v78, v69
	v_pk_fma_f32 v[52:53], v[52:53], v[66:67], v[196:197]
	v_mov_b32_e32 v196, v86
	v_mov_b32_e32 v197, v84
	v_pk_mul_f32 v[200:201], v[200:201], v[64:65] op_sel:[0,1] op_sel_hi:[1,0]
	v_mov_b32_e32 v70, v77
	v_pk_mul_f32 v[68:69], v[78:79], v[66:67] op_sel:[0,1] op_sel_hi:[1,0]
	v_mov_b32_e32 v174, v83
	v_pk_fma_f32 v[196:197], v[196:197], v[64:65], v[200:201]
	v_pk_fma_f32 v[68:69], v[70:71], v[66:67], v[68:69]
	v_mov_b32_e32 v84, v87
	v_pk_mul_f32 v[70:71], v[174:175], v[64:65] op_sel:[0,1] op_sel_hi:[1,0]
	v_pk_add_f32 v[52:53], v[52:53], v[196:197]
	v_pk_fma_f32 v[70:71], v[84:85], v[64:65], v[70:71]
	v_pk_add_f32 v[52:53], v[52:53], v[182:183]
	v_pk_add_f32 v[68:69], v[68:69], v[70:71]
	v_and_b32_sdwa v71, v52, v129 dst_sel:DWORD dst_unused:UNUSED_PAD src0_sel:WORD_1 src1_sel:DWORD
	v_pk_add_f32 v[68:69], v[68:69], v[190:191]
	v_add3_u32 v76, v52, v71, s4
	v_and_b32_sdwa v71, v69, v129 dst_sel:DWORD dst_unused:UNUSED_PAD src0_sel:WORD_1 src1_sel:DWORD
	v_and_b32_sdwa v77, v68, v129 dst_sel:DWORD dst_unused:UNUSED_PAD src0_sel:WORD_1 src1_sel:DWORD
	v_and_b32_sdwa v70, v53, v129 dst_sel:DWORD dst_unused:UNUSED_PAD src0_sel:WORD_1 src1_sel:DWORD
	v_add3_u32 v71, v69, v71, s4
	v_add3_u32 v77, v68, v77, s4
	v_add3_u32 v70, v53, v70, s4
	v_and_b32_e32 v71, 0xffff0000, v71
	v_and_b32_e32 v77, 0xffff0000, v77
	v_or_b32_sdwa v71, v71, v70 dst_sel:DWORD dst_unused:UNUSED_PAD src0_sel:DWORD src1_sel:WORD_1
	v_or_b32_sdwa v70, v77, v76 dst_sel:DWORD dst_unused:UNUSED_PAD src0_sel:DWORD src1_sel:WORD_1
	global_store_dwordx2 v[72:73], v[70:71], off offset:1024
	v_pk_mul_f32 v[70:71], v[68:69], v[68:69]
	s_nop 0
	v_pk_fma_f32 v[84:85], v[52:53], v[52:53], v[70:71]
	v_cvt_pk_f32_fp8_e32 v[76:77], v170
	v_cvt_pk_f32_fp8_sdwa v[86:87], v168 src0_sel:WORD_1
	v_cvt_pk_f32_fp8_sdwa v[78:79], v170 src0_sel:WORD_1
	v_cvt_pk_f32_fp8_e32 v[82:83], v168
	v_cvt_pk_f32_fp8_e32 v[174:175], v167
	v_cvt_pk_f32_fp8_sdwa v[182:183], v167 src0_sel:WORD_1
	v_cvt_pk_f32_fp8_e32 v[190:191], v166
	v_cvt_pk_f32_fp8_sdwa v[166:167], v166 src0_sel:WORD_1
	v_mov_b32_e32 v200, v76
	v_mov_b32_e32 v201, v86
	v_mov_b32_e32 v196, v82
	v_mov_b32_e32 v197, v78
	v_pk_mul_f32 v[200:201], v[200:201], v[66:67] op_sel:[0,1] op_sel_hi:[1,0]
	v_mov_b32_e32 v202, v174
	v_mov_b32_e32 v203, v166
	v_mov_b32_e32 v86, v77
	v_pk_fma_f32 v[196:197], v[196:197], v[66:67], v[200:201]
	v_mov_b32_e32 v200, v190
	v_mov_b32_e32 v201, v182
	v_pk_mul_f32 v[202:203], v[202:203], v[64:65] op_sel:[0,1] op_sel_hi:[1,0]
	v_mov_b32_e32 v78, v83
	v_pk_mul_f32 v[76:77], v[86:87], v[66:67] op_sel:[0,1] op_sel_hi:[1,0]
	v_mov_b32_e32 v166, v175
	v_pk_fma_f32 v[200:201], v[200:201], v[64:65], v[202:203]
	v_pk_fma_f32 v[76:77], v[78:79], v[66:67], v[76:77]
	v_mov_b32_e32 v182, v191
	v_pk_mul_f32 v[78:79], v[166:167], v[64:65] op_sel:[0,1] op_sel_hi:[1,0]
	v_lshlrev_b32_e32 v71, 16, v49
	v_lshlrev_b32_e32 v70, 16, v48
	v_pk_add_f32 v[196:197], v[196:197], v[200:201]
	v_pk_fma_f32 v[78:79], v[182:183], v[64:65], v[78:79]
	v_and_b32_e32 v49, 0xffff0000, v49
	v_and_b32_e32 v48, 0xffff0000, v48
	v_pk_add_f32 v[70:71], v[196:197], v[70:71]
	v_pk_add_f32 v[76:77], v[76:77], v[78:79]
	s_nop 0
	v_pk_add_f32 v[76:77], v[76:77], v[48:49]
	v_and_b32_sdwa v49, v70, v129 dst_sel:DWORD dst_unused:UNUSED_PAD src0_sel:WORD_1 src1_sel:DWORD
	v_add3_u32 v78, v70, v49, s4
	v_and_b32_sdwa v49, v77, v129 dst_sel:DWORD dst_unused:UNUSED_PAD src0_sel:WORD_1 src1_sel:DWORD
	v_and_b32_sdwa v79, v76, v129 dst_sel:DWORD dst_unused:UNUSED_PAD src0_sel:WORD_1 src1_sel:DWORD
	v_and_b32_sdwa v48, v71, v129 dst_sel:DWORD dst_unused:UNUSED_PAD src0_sel:WORD_1 src1_sel:DWORD
	v_add3_u32 v49, v77, v49, s4
	v_add3_u32 v79, v76, v79, s4
	v_add3_u32 v48, v71, v48, s4
	v_and_b32_e32 v49, 0xffff0000, v49
	v_and_b32_e32 v79, 0xffff0000, v79
	v_or_b32_sdwa v49, v49, v48 dst_sel:DWORD dst_unused:UNUSED_PAD src0_sel:DWORD src1_sel:WORD_1
	v_or_b32_sdwa v48, v79, v78 dst_sel:DWORD dst_unused:UNUSED_PAD src0_sel:DWORD src1_sel:WORD_1
	global_store_dwordx2 v[72:73], v[48:49], off offset:1536
	v_pk_mul_f32 v[48:49], v[76:77], v[76:77]
	s_nop 0
	v_pk_fma_f32 v[48:49], v[70:71], v[70:71], v[48:49]
	v_cvt_pk_f32_fp8_e32 v[78:79], v161
	v_cvt_pk_f32_fp8_sdwa v[82:83], v161 src0_sel:WORD_1
	v_cvt_pk_f32_fp8_e32 v[86:87], v160
	v_cvt_pk_f32_fp8_sdwa v[160:161], v160 src0_sel:WORD_1
	v_cvt_pk_f32_fp8_e32 v[166:167], v159
	v_cvt_pk_f32_fp8_sdwa v[174:175], v159 src0_sel:WORD_1
	v_cvt_pk_f32_fp8_e32 v[182:183], v158
	v_cvt_pk_f32_fp8_sdwa v[158:159], v158 src0_sel:WORD_1
	v_mov_b32_e32 v200, v78
	v_mov_b32_e32 v201, v160
	v_lshlrev_b32_e32 v191, 16, v45
	v_lshlrev_b32_e32 v190, 16, v44
	v_and_b32_e32 v197, 0xffff0000, v45
	v_and_b32_e32 v196, 0xffff0000, v44
	v_mov_b32_e32 v44, v86
	v_mov_b32_e32 v45, v82
	v_pk_mul_f32 v[200:201], v[200:201], v[66:67] op_sel:[0,1] op_sel_hi:[1,0]
	v_mov_b32_e32 v202, v166
	v_mov_b32_e32 v203, v158
	v_mov_b32_e32 v160, v79
	v_pk_fma_f32 v[44:45], v[44:45], v[66:67], v[200:201]
	v_mov_b32_e32 v200, v182
	v_mov_b32_e32 v201, v174
	v_pk_mul_f32 v[202:203], v[202:203], v[64:65] op_sel:[0,1] op_sel_hi:[1,0]
	v_mov_b32_e32 v82, v87
	v_pk_mul_f32 v[78:79], v[160:161], v[66:67] op_sel:[0,1] op_sel_hi:[1,0]
	v_mov_b32_e32 v158, v167
	v_pk_fma_f32 v[200:201], v[200:201], v[64:65], v[202:203]
	v_pk_fma_f32 v[78:79], v[82:83], v[66:67], v[78:79]
	v_mov_b32_e32 v174, v183
	v_pk_mul_f32 v[82:83], v[158:159], v[64:65] op_sel:[0,1] op_sel_hi:[1,0]
	v_pk_add_f32 v[44:45], v[44:45], v[200:201]
	v_pk_fma_f32 v[82:83], v[174:175], v[64:65], v[82:83]
	v_pk_add_f32 v[44:45], v[44:45], v[190:191]
	v_pk_add_f32 v[78:79], v[78:79], v[82:83]
	v_and_b32_sdwa v83, v44, v129 dst_sel:DWORD dst_unused:UNUSED_PAD src0_sel:WORD_1 src1_sel:DWORD
	v_pk_add_f32 v[78:79], v[78:79], v[196:197]
	v_add3_u32 v86, v44, v83, s4
	v_and_b32_sdwa v83, v79, v129 dst_sel:DWORD dst_unused:UNUSED_PAD src0_sel:WORD_1 src1_sel:DWORD
	v_and_b32_sdwa v87, v78, v129 dst_sel:DWORD dst_unused:UNUSED_PAD src0_sel:WORD_1 src1_sel:DWORD
	v_and_b32_sdwa v82, v45, v129 dst_sel:DWORD dst_unused:UNUSED_PAD src0_sel:WORD_1 src1_sel:DWORD
	v_add3_u32 v83, v79, v83, s4
	v_add3_u32 v87, v78, v87, s4
	v_add3_u32 v82, v45, v82, s4
	v_and_b32_e32 v83, 0xffff0000, v83
	v_and_b32_e32 v87, 0xffff0000, v87
	v_or_b32_sdwa v83, v83, v82 dst_sel:DWORD dst_unused:UNUSED_PAD src0_sel:DWORD src1_sel:WORD_1
	v_or_b32_sdwa v82, v87, v86 dst_sel:DWORD dst_unused:UNUSED_PAD src0_sel:DWORD src1_sel:WORD_1
	global_store_dwordx2 v[72:73], v[82:83], off offset:2048
	v_pk_mul_f32 v[82:83], v[78:79], v[78:79]
	s_nop 0
	v_pk_fma_f32 v[158:159], v[44:45], v[44:45], v[82:83]
	v_cvt_pk_f32_fp8_e32 v[82:83], v153
	v_cvt_pk_f32_fp8_sdwa v[166:167], v151 src0_sel:WORD_1
	v_cvt_pk_f32_fp8_sdwa v[86:87], v153 src0_sel:WORD_1
	v_cvt_pk_f32_fp8_e32 v[160:161], v151
	v_cvt_pk_f32_fp8_e32 v[174:175], v150
	v_cvt_pk_f32_fp8_e32 v[182:183], v149
	v_cvt_pk_f32_fp8_sdwa v[148:149], v149 src0_sel:WORD_1
	v_cvt_pk_f32_fp8_sdwa v[150:151], v150 src0_sel:WORD_1
	v_mov_b32_e32 v200, v82
	v_mov_b32_e32 v201, v166
	v_lshlrev_b32_e32 v191, 16, v39
	v_lshlrev_b32_e32 v190, 16, v38
	v_and_b32_e32 v197, 0xffff0000, v39
	v_and_b32_e32 v196, 0xffff0000, v38
	v_mov_b32_e32 v38, v160
	v_mov_b32_e32 v39, v86
	v_pk_mul_f32 v[200:201], v[200:201], v[66:67] op_sel:[0,1] op_sel_hi:[1,0]
	v_mov_b32_e32 v202, v174
	v_mov_b32_e32 v203, v148
	v_mov_b32_e32 v166, v83
	v_pk_fma_f32 v[38:39], v[38:39], v[66:67], v[200:201]
	v_mov_b32_e32 v200, v182
	v_mov_b32_e32 v201, v150
	v_pk_mul_f32 v[202:203], v[202:203], v[64:65] op_sel:[0,1] op_sel_hi:[1,0]
	v_mov_b32_e32 v86, v161
	v_pk_mul_f32 v[82:83], v[166:167], v[66:67] op_sel:[0,1] op_sel_hi:[1,0]
	v_mov_b32_e32 v148, v175
	v_pk_fma_f32 v[200:201], v[200:201], v[64:65], v[202:203]
	v_pk_fma_f32 v[82:83], v[86:87], v[66:67], v[82:83]
	v_mov_b32_e32 v150, v183
	v_pk_mul_f32 v[86:87], v[148:149], v[64:65] op_sel:[0,1] op_sel_hi:[1,0]
	v_pk_add_f32 v[38:39], v[38:39], v[200:201]
	v_pk_fma_f32 v[86:87], v[150:151], v[64:65], v[86:87]
	v_pk_add_f32 v[38:39], v[38:39], v[190:191]
	v_pk_add_f32 v[82:83], v[82:83], v[86:87]
	v_and_b32_sdwa v87, v38, v129 dst_sel:DWORD dst_unused:UNUSED_PAD src0_sel:WORD_1 src1_sel:DWORD
	v_pk_add_f32 v[82:83], v[82:83], v[196:197]
	v_add3_u32 v137, v38, v87, s4
	v_and_b32_sdwa v87, v83, v129 dst_sel:DWORD dst_unused:UNUSED_PAD src0_sel:WORD_1 src1_sel:DWORD
	v_and_b32_sdwa v138, v82, v129 dst_sel:DWORD dst_unused:UNUSED_PAD src0_sel:WORD_1 src1_sel:DWORD
	v_and_b32_sdwa v86, v39, v129 dst_sel:DWORD dst_unused:UNUSED_PAD src0_sel:WORD_1 src1_sel:DWORD
	v_add3_u32 v87, v83, v87, s4
	v_add3_u32 v138, v82, v138, s4
	v_add3_u32 v86, v39, v86, s4
	v_and_b32_e32 v87, 0xffff0000, v87
	v_and_b32_e32 v138, 0xffff0000, v138
	v_or_b32_sdwa v87, v87, v86 dst_sel:DWORD dst_unused:UNUSED_PAD src0_sel:DWORD src1_sel:WORD_1
	v_or_b32_sdwa v86, v138, v137 dst_sel:DWORD dst_unused:UNUSED_PAD src0_sel:DWORD src1_sel:WORD_1
	global_store_dwordx2 v[72:73], v[86:87], off offset:2560
	v_pk_mul_f32 v[86:87], v[82:83], v[82:83]
	s_nop 0
	v_pk_fma_f32 v[148:149], v[38:39], v[38:39], v[86:87]
	v_cvt_pk_f32_fp8_e32 v[86:87], v143
	v_cvt_pk_f32_fp8_sdwa v[166:167], v141 src0_sel:WORD_1
	v_cvt_pk_f32_fp8_sdwa v[150:151], v143 src0_sel:WORD_1
	v_cvt_pk_f32_fp8_e32 v[160:161], v141
	v_cvt_pk_f32_fp8_e32 v[174:175], v140
	v_cvt_pk_f32_fp8_e32 v[182:183], v139
	v_cvt_pk_f32_fp8_sdwa v[138:139], v139 src0_sel:WORD_1
	v_cvt_pk_f32_fp8_sdwa v[140:141], v140 src0_sel:WORD_1
	v_mov_b32_e32 v200, v86
	v_mov_b32_e32 v201, v166
	v_lshlrev_b32_e32 v191, 16, v35
	v_lshlrev_b32_e32 v190, 16, v34
	v_and_b32_e32 v197, 0xffff0000, v35
	v_and_b32_e32 v196, 0xffff0000, v34
	v_mov_b32_e32 v34, v160
	v_mov_b32_e32 v35, v150
	v_pk_mul_f32 v[200:201], v[200:201], v[66:67] op_sel:[0,1] op_sel_hi:[1,0]
	v_mov_b32_e32 v203, v138
	v_mov_b32_e32 v166, v87
	v_mov_b32_e32 v138, v175
	v_pk_fma_f32 v[34:35], v[34:35], v[66:67], v[200:201]
	v_mov_b32_e32 v201, v140
	v_mov_b32_e32 v202, v174
	v_mov_b32_e32 v150, v161
	v_pk_mul_f32 v[86:87], v[166:167], v[66:67] op_sel:[0,1] op_sel_hi:[1,0]
	v_mov_b32_e32 v140, v183
	v_pk_mul_f32 v[138:139], v[138:139], v[64:65] op_sel:[0,1] op_sel_hi:[1,0]
	v_mov_b32_e32 v200, v182
	v_pk_mul_f32 v[202:203], v[202:203], v[64:65] op_sel:[0,1] op_sel_hi:[1,0]
	v_pk_fma_f32 v[86:87], v[150:151], v[66:67], v[86:87]
	v_pk_fma_f32 v[138:139], v[140:141], v[64:65], v[138:139]
	v_pk_fma_f32 v[200:201], v[200:201], v[64:65], v[202:203]
	v_pk_add_f32 v[86:87], v[86:87], v[138:139]
	v_pk_add_f32 v[34:35], v[34:35], v[200:201]
	v_pk_add_f32 v[86:87], v[86:87], v[196:197]
	v_pk_add_f32 v[34:35], v[34:35], v[190:191]
	v_and_b32_sdwa v139, v87, v129 dst_sel:DWORD dst_unused:UNUSED_PAD src0_sel:WORD_1 src1_sel:DWORD
	v_and_b32_sdwa v140, v86, v129 dst_sel:DWORD dst_unused:UNUSED_PAD src0_sel:WORD_1 src1_sel:DWORD
	v_and_b32_sdwa v137, v35, v129 dst_sel:DWORD dst_unused:UNUSED_PAD src0_sel:WORD_1 src1_sel:DWORD
	v_and_b32_sdwa v138, v34, v129 dst_sel:DWORD dst_unused:UNUSED_PAD src0_sel:WORD_1 src1_sel:DWORD
	v_add3_u32 v139, v87, v139, s4
	v_add3_u32 v140, v86, v140, s4
	v_add3_u32 v138, v34, v138, s4
	v_add3_u32 v137, v35, v137, s4
	v_and_b32_e32 v139, 0xffff0000, v139
	v_and_b32_e32 v140, 0xffff0000, v140
	v_or_b32_sdwa v139, v139, v137 dst_sel:DWORD dst_unused:UNUSED_PAD src0_sel:DWORD src1_sel:WORD_1
	v_or_b32_sdwa v138, v140, v138 dst_sel:DWORD dst_unused:UNUSED_PAD src0_sel:DWORD src1_sel:WORD_1
	global_store_dwordx2 v[72:73], v[138:139], off offset:3072
	v_pk_mul_f32 v[138:139], v[86:87], v[86:87]
	s_nop 0
	v_pk_fma_f32 v[138:139], v[34:35], v[34:35], v[138:139]
	v_cvt_pk_f32_fp8_e32 v[140:141], v133
	v_cvt_pk_f32_fp8_sdwa v[166:167], v131 src0_sel:WORD_1
	v_cvt_pk_f32_fp8_sdwa v[150:151], v133 src0_sel:WORD_1
	v_cvt_pk_f32_fp8_e32 v[160:161], v131
	v_cvt_pk_f32_fp8_e32 v[174:175], v89
	v_cvt_pk_f32_fp8_sdwa v[182:183], v89 src0_sel:WORD_1
	v_cvt_pk_f32_fp8_e32 v[190:191], v88
	v_cvt_pk_f32_fp8_sdwa v[88:89], v88 src0_sel:WORD_1
	v_mov_b32_e32 v202, v140
	v_mov_b32_e32 v203, v166
	v_lshlrev_b32_e32 v197, 16, v29
	v_lshlrev_b32_e32 v196, 16, v28
	v_and_b32_e32 v201, 0xffff0000, v29
	v_and_b32_e32 v200, 0xffff0000, v28
	v_mov_b32_e32 v28, v160
	v_mov_b32_e32 v29, v150
	v_pk_mul_f32 v[202:203], v[202:203], v[66:67] op_sel:[0,1] op_sel_hi:[1,0]
	v_mov_b32_e32 v204, v174
	v_mov_b32_e32 v205, v88
	v_pk_fma_f32 v[28:29], v[28:29], v[66:67], v[202:203]
	v_mov_b32_e32 v202, v190
	v_mov_b32_e32 v203, v182
	v_pk_mul_f32 v[204:205], v[204:205], v[64:65] op_sel:[0,1] op_sel_hi:[1,0]
	v_mov_b32_e32 v166, v141
	v_mov_b32_e32 v88, v175
	v_pk_fma_f32 v[202:203], v[202:203], v[64:65], v[204:205]
	v_mov_b32_e32 v150, v161
	v_pk_mul_f32 v[140:141], v[166:167], v[66:67] op_sel:[0,1] op_sel_hi:[1,0]
	v_mov_b32_e32 v182, v191
	v_pk_mul_f32 v[88:89], v[88:89], v[64:65] op_sel:[0,1] op_sel_hi:[1,0]
	v_pk_add_f32 v[28:29], v[28:29], v[202:203]
	v_pk_fma_f32 v[66:67], v[150:151], v[66:67], v[140:141]
	v_pk_fma_f32 v[64:65], v[182:183], v[64:65], v[88:89]
	v_pk_add_f32 v[28:29], v[28:29], v[196:197]
	v_pk_add_f32 v[64:65], v[66:67], v[64:65]
	v_and_b32_sdwa v67, v28, v129 dst_sel:DWORD dst_unused:UNUSED_PAD src0_sel:WORD_1 src1_sel:DWORD
	v_pk_add_f32 v[64:65], v[64:65], v[200:201]
	v_add3_u32 v88, v28, v67, s4
	v_and_b32_sdwa v67, v65, v129 dst_sel:DWORD dst_unused:UNUSED_PAD src0_sel:WORD_1 src1_sel:DWORD
	v_and_b32_sdwa v89, v64, v129 dst_sel:DWORD dst_unused:UNUSED_PAD src0_sel:WORD_1 src1_sel:DWORD
	v_and_b32_sdwa v66, v29, v129 dst_sel:DWORD dst_unused:UNUSED_PAD src0_sel:WORD_1 src1_sel:DWORD
	v_add3_u32 v67, v65, v67, s4
	v_add3_u32 v89, v64, v89, s4
	v_add3_u32 v66, v29, v66, s4
	v_and_b32_e32 v67, 0xffff0000, v67
	v_and_b32_e32 v89, 0xffff0000, v89
	v_or_b32_sdwa v67, v67, v66 dst_sel:DWORD dst_unused:UNUSED_PAD src0_sel:DWORD src1_sel:WORD_1
	v_or_b32_sdwa v66, v89, v88 dst_sel:DWORD dst_unused:UNUSED_PAD src0_sel:DWORD src1_sel:WORD_1
	global_store_dwordx2 v[72:73], v[66:67], off offset:3584
	v_add_f32_e32 v72, v80, v81
	v_add_f32_e32 v73, v74, v75
	v_add_f32_e32 v72, v73, v72
	v_add_f32_e32 v73, v84, v85
	v_add_f32_e32 v72, v72, v73
	v_add_f32_e32 v48, v48, v49
	v_add_f32_e32 v48, v72, v48
	v_add_f32_e32 v49, v158, v159
	v_pk_mul_f32 v[66:67], v[64:65], v[64:65]
	v_add_f32_e32 v48, v48, v49
	v_add_f32_e32 v49, v148, v149
	v_pk_fma_f32 v[66:67], v[28:29], v[28:29], v[66:67]
	v_add_f32_e32 v48, v48, v49
	v_add_f32_e32 v49, v138, v139
	v_add_f32_e32 v48, v48, v49
	v_add_f32_e32 v49, v66, v67
	v_add_f32_e32 v48, v48, v49
	v_mov_b64_e32 v[72:73], v[212:213]
	v_mov_b64_e32 v[74:75], v[214:215]
	ds_bpermute_b32 v49, v1, v48
	s_waitcnt lgkmcnt(0)
	v_add_f32_e32 v48, v48, v49
	ds_bpermute_b32 v49, v90, v48
	s_waitcnt lgkmcnt(0)
	v_add_f32_e32 v48, v48, v49
	ds_bpermute_b32 v49, v91, v48
	s_waitcnt lgkmcnt(0)
	v_add_f32_e32 v48, v48, v49
	ds_bpermute_b32 v49, v92, v48
	s_waitcnt lgkmcnt(0)
	v_add_f32_e32 v48, v48, v49
	ds_bpermute_b32 v49, v93, v48
	s_waitcnt lgkmcnt(0)
	v_add_f32_e32 v48, v48, v49
	ds_bpermute_b32 v49, v94, v48
	s_waitcnt lgkmcnt(0)
	v_add_f32_e32 v48, v48, v49
	v_fmamk_f32 v48, v48, 0x3a000000, v127
	v_mul_f32_e32 v49, 0x4f800000, v48
	v_cmp_gt_f32_e32 vcc, s19, v48
	s_nop 1
	v_cndmask_b32_e32 v48, v48, v49, vcc
	v_sqrt_f32_e32 v49, v48
	s_nop 0
	v_add_u32_e32 v66, -1, v49
	v_add_u32_e32 v67, 1, v49
	v_fma_f32 v80, -v66, v49, v48
	v_fma_f32 v81, -v67, v49, v48
	v_cmp_ge_f32_e64 s[8:9], 0, v80
	s_nop 1
	v_cndmask_b32_e64 v49, v49, v66, s[8:9]
	v_cmp_lt_f32_e64 s[8:9], 0, v81
	s_nop 1
	v_cndmask_b32_e64 v49, v49, v67, s[8:9]
	v_mul_f32_e32 v66, 0x37800000, v49
	v_cndmask_b32_e32 v49, v49, v66, vcc
	v_cmp_class_f32_e32 vcc, v48, v128
	v_mov_b32_e32 v67, 0
	s_nop 0
	v_cndmask_b32_e32 v48, v49, v48, vcc
	v_div_scale_f32 v49, s[0:1], v48, v48, 1.0
	v_rcp_f32_e32 v66, v49
	v_div_scale_f32 v80, vcc, 1.0, v48, 1.0
	v_fma_f32 v81, -v49, v66, 1.0
	v_fmac_f32_e32 v66, v81, v66
	v_mul_f32_e32 v81, v80, v66
	v_fma_f32 v84, -v49, v81, v80
	v_fmac_f32_e32 v81, v84, v66
	v_fma_f32 v49, -v49, v81, v80
	v_div_fmas_f32 v49, v49, v66, v81
	v_div_fixup_f32 v66, v49, v48, 1.0
	v_mul_f32_e32 v24, v66, v24
	v_mul_f32_e32 v48, v66, v50

	v_mul_f32_e32 v24, v72, v24
	v_mul_f32_e32 v48, v73, v48
	v_cvt_pk_fp8_f32 v67, v24, v48
	v_mul_f32_e32 v25, v66, v25
	v_mul_f32_e32 v24, v66, v51
	v_mul_f32_e32 v25, v74, v25
	v_mul_f32_e32 v24, v75, v24
	v_cvt_pk_fp8_f32 v67, v25, v24 op_sel:[0,0,1]
	v_add_co_u32_e32 v24, vcc, s41, v22
	v_mul_f32_e32 v58, v66, v58
	s_nop 0
	v_addc_co_u32_e32 v25, vcc, 0, v23, vcc
	global_store_dword v[24:25], v67, off offset:-4096
	v_mov_b64_e32 v[48:49], v[216:217]
	v_mov_b64_e32 v[50:51], v[218:219]
	v_mul_f32_e32 v62, v66, v62
	v_mov_b32_e32 v67, 0
	v_mul_f32_e32 v59, v66, v59
	v_mul_f32_e32 v45, v66, v45
	v_mul_f32_e32 v39, v66, v39
	v_mul_f32_e32 v35, v66, v35
	v_mul_f32_e32 v28, v66, v28
	v_mul_f32_e32 v29, v66, v29
	s_waitcnt vmcnt(17)
	v_cvt_pk_f32_fp8_sdwa v[80:81], v194 src0_sel:WORD_1

	v_mul_f32_e32 v48, v48, v58
	v_mul_f32_e32 v49, v49, v62
	v_cvt_pk_fp8_f32 v67, v48, v49
	v_mul_f32_e32 v48, v66, v63
	v_mul_f32_e32 v49, v50, v59
	v_mul_f32_e32 v48, v51, v48
	v_cvt_pk_fp8_f32 v67, v49, v48 op_sel:[0,0,1]
	v_add_co_u32_e32 v48, vcc, s36, v22
	v_mul_f32_e32 v50, v66, v68
	s_nop 0
	v_addc_co_u32_e32 v49, vcc, 0, v23, vcc
	global_store_dword v[48:49], v67, off offset:256
	v_mov_b64_e32 v[72:73], v[220:221]
	v_mov_b64_e32 v[74:75], v[222:223]
	v_mul_f32_e32 v23, v66, v52
	v_mov_b32_e32 v22, 0
	v_mul_f32_e32 v51, v66, v53
	v_mul_f32_e32 v58, v66, v76
	v_mul_f32_e32 v59, v66, v71
	ds_bpermute_b32 v67, v116, v19
	v_cvt_pk_f32_fp8_e32 v[62:63], v188
	v_mov_b32_e32 v84, v62

	v_mul_f32_e32 v23, v72, v23
	v_mul_f32_e32 v50, v73, v50
	v_cvt_pk_fp8_f32 v22, v23, v50
	v_mul_f32_e32 v23, v66, v69
	v_mul_f32_e32 v50, v74, v51
	v_mul_f32_e32 v23, v75, v23
	v_cvt_pk_fp8_f32 v22, v50, v23 op_sel:[0,0,1]
	v_mul_f32_e32 v23, v66, v70
	v_cvt_pk_f32_fp8_sdwa v[72:73], v189 src0_sel:WORD_1
	v_cvt_pk_f32_fp8_sdwa v[68:69], v188 src0_sel:WORD_1
	global_store_dword v[48:49], v22, off offset:512
	v_mov_b64_e32 v[50:51], v[224:225]
	v_mov_b64_e32 v[52:53], v[226:227]
	v_mov_b32_e32 v22, 0
	v_cvt_pk_f32_fp8_e32 v[70:71], v189
	v_cvt_pk_f32_fp8_e32 v[74:75], v192
	v_mov_b32_e32 v85, v72
	v_mov_b32_e32 v72, v63

	v_mul_f32_e32 v23, v50, v23
	v_mul_f32_e32 v50, v51, v58
	v_cvt_pk_fp8_f32 v22, v23, v50
	v_mul_f32_e32 v23, v66, v77
	v_mul_f32_e32 v50, v52, v59
	v_mul_f32_e32 v23, v53, v23
	v_cvt_pk_fp8_f32 v22, v50, v23 op_sel:[0,0,1]
	v_mul_f32_e32 v23, v66, v44
	v_mul_f32_e32 v44, v66, v78
	v_mul_f32_e32 v59, v66, v64
	global_store_dword v[48:49], v22, off offset:768
	v_mov_b64_e32 v[50:51], v[228:229]
	v_mov_b64_e32 v[52:53], v[230:231]
	v_mov_b32_e32 v22, 0
	v_mov_b32_e32 v58, 0
	ds_bpermute_b32 v64, v119, v19
	v_cvt_pk_f32_fp8_sdwa v[76:77], v192 src0_sel:WORD_1

	v_mul_f32_e32 v23, v50, v23
	v_mul_f32_e32 v44, v51, v44
	v_cvt_pk_fp8_f32 v22, v23, v44
	v_mul_f32_e32 v23, v66, v79
	v_mul_f32_e32 v44, v52, v45
	v_mul_f32_e32 v23, v53, v23
	v_cvt_pk_fp8_f32 v22, v44, v23 op_sel:[0,0,1]
	v_mul_f32_e32 v23, v66, v38
	v_mul_f32_e32 v38, v66, v82
	ds_bpermute_b32 v44, v123, v130
	global_store_dword v[48:49], v22, off offset:1024
	v_mov_b64_e32 v[50:51], v[232:233]
	v_mov_b64_e32 v[52:53], v[234:235]
	v_mov_b32_e32 v22, 0
	v_cvt_pk_f32_fp8_e32 v[78:79], v194
	s_waitcnt lgkmcnt(0)
	v_ashrrev_i32_e32 v45, 31, v44
	v_lshlrev_b64 v[44:45], 11, v[44:45]
	v_mov_b32_e32 v82, v70

	v_mul_f32_e32 v23, v50, v23
	v_mul_f32_e32 v38, v51, v38
	v_cvt_pk_fp8_f32 v22, v23, v38
	v_mul_f32_e32 v23, v66, v83
	v_mul_f32_e32 v38, v52, v39
	v_mul_f32_e32 v23, v53, v23
	v_cvt_pk_fp8_f32 v22, v38, v23 op_sel:[0,0,1]
	v_mul_f32_e32 v23, v66, v34
	v_mul_f32_e32 v34, v66, v86
	ds_bpermute_b32 v38, v122, v130
	global_store_dword v[48:49], v22, off offset:1280
	v_mov_b64_e32 v[50:51], v[236:237]
	v_mov_b64_e32 v[52:53], v[238:239]
	v_mov_b32_e32 v22, 0
	v_mov_b32_e32 v83, v68
	s_waitcnt lgkmcnt(0)
	v_ashrrev_i32_e32 v39, 31, v38
	v_lshlrev_b64 v[38:39], 11, v[38:39]
	v_mov_b32_e32 v86, v74
	v_mov_b32_e32 v68, v71

	v_mul_f32_e32 v23, v50, v23
	v_mul_f32_e32 v34, v51, v34
	v_cvt_pk_fp8_f32 v22, v23, v34
	v_mul_f32_e32 v23, v66, v87
	v_mul_f32_e32 v34, v52, v35
	v_mul_f32_e32 v23, v53, v23
	v_cvt_pk_fp8_f32 v22, v34, v23 op_sel:[0,0,1]
	ds_bpermute_b32 v34, v121, v130
	v_mov_b32_e32 v87, v80
	v_mov_b32_e32 v80, v75
	global_store_dword v[48:49], v22, off offset:1536
	v_mov_b64_e32 v[50:51], v[240:241]
	v_mov_b64_e32 v[52:53], v[242:243]
	ds_bpermute_b32 v22, v120, v130
	s_waitcnt lgkmcnt(1)
	v_ashrrev_i32_e32 v35, 31, v34
	v_lshlrev_b64 v[34:35], 11, v[34:35]
	s_waitcnt lgkmcnt(0)
	v_ashrrev_i32_e32 v23, 31, v22
	v_lshlrev_b64 v[22:23], 11, v[22:23]
	v_lshl_add_u64 v[22:23], v[4:5], 0, v[22:23]

	v_mul_f32_e32 v28, v50, v28
	v_mul_f32_e32 v50, v51, v59
	v_cvt_pk_fp8_f32 v58, v28, v50
	v_mul_f32_e32 v28, v66, v65
	v_mul_f32_e32 v29, v52, v29
	v_mul_f32_e32 v28, v53, v28
	v_cvt_pk_fp8_f32 v58, v29, v28 op_sel:[0,0,1]
	v_lshl_add_u64 v[28:29], v[4:5], 0, v[34:35]
	v_lshl_add_u64 v[34:35], v[4:5], 0, v[38:39]
	v_lshl_add_u64 v[38:39], v[4:5], 0, v[44:45]
	global_store_dword v[48:49], v58, off offset:1792
	global_load_dword v183, v[22:23], off
	global_load_dword v175, v[22:23], off offset:256
	global_load_dword v167, v[22:23], off offset:512
	global_load_dword v159, v[22:23], off offset:768
	global_load_dword v150, v[22:23], off offset:1024
	global_load_dword v141, v[22:23], off offset:1280
	global_load_dword v137, v[22:23], off offset:1536
	global_load_dword v88, v[22:23], off offset:1792
	global_load_dword v184, v[28:29], off
	global_load_dword v176, v[28:29], off offset:256
	global_load_dword v168, v[28:29], off offset:512
	global_load_dword v160, v[28:29], off offset:768
	global_load_dword v151, v[28:29], off offset:1024
	global_load_dword v143, v[28:29], off offset:1280
	global_load_dword v138, v[28:29], off offset:1536
	global_load_dword v89, v[28:29], off offset:1792
	global_load_dword v186, v[34:35], off
	global_load_dword v178, v[34:35], off offset:256
	global_load_dword v170, v[34:35], off offset:512
	global_load_dword v161, v[34:35], off offset:768
	global_load_dword v153, v[34:35], off offset:1024
	global_load_dword v148, v[34:35], off offset:1280
	global_load_dword v139, v[34:35], off offset:1536
	global_load_dword v131, v[34:35], off offset:1792
	global_load_dword v190, v[38:39], off
	global_load_dword v182, v[38:39], off offset:256
	global_load_dword v174, v[38:39], off offset:512
	global_load_dword v166, v[38:39], off offset:768
	global_load_dword v158, v[38:39], off offset:1024
	global_load_dword v149, v[38:39], off offset:1280
	global_load_dword v140, v[38:39], off offset:1536
	global_load_dword v133, v[38:39], off offset:1792
	global_load_dwordx2 v[22:23], v[56:57], off offset:3584
	global_load_dwordx2 v[28:29], v[56:57], off offset:3072
	global_load_dwordx2 v[34:35], v[56:57], off offset:2560
	s_nop 0
	global_load_dwordx2 v[38:39], v[56:57], off offset:2048
	global_load_dwordx2 v[44:45], v[56:57], off offset:1536
	global_load_dwordx2 v[50:51], v[56:57], off offset:1024
	global_load_dwordx2 v[52:53], v[56:57], off offset:512
	s_nop 0
	global_load_dwordx2 v[56:57], v[56:57], off
	ds_bpermute_b32 v66, v117, v19
	ds_bpermute_b32 v65, v118, v19
	s_waitcnt vmcnt(63)
	v_lshlrev_b32_e32 v59, 16, v61
	v_lshlrev_b32_e32 v58, 16, v60
	v_and_b32_e32 v61, 0xffff0000, v61
	s_waitcnt lgkmcnt(1)
	v_pk_mul_f32 v[84:85], v[84:85], v[66:67] op_sel:[0,1] op_sel_hi:[1,0]
	s_waitcnt lgkmcnt(0)
	v_pk_mul_f32 v[86:87], v[86:87], v[64:65] op_sel:[0,1] op_sel_hi:[1,0]
	v_pk_fma_f32 v[82:83], v[82:83], v[66:67], v[84:85]
	v_mov_b32_e32 v84, v78
	v_mov_b32_e32 v85, v76
	v_pk_mul_f32 v[62:63], v[72:73], v[66:67] op_sel:[0,1] op_sel_hi:[1,0]
	v_pk_fma_f32 v[84:85], v[84:85], v[64:65], v[86:87]
	v_pk_fma_f32 v[62:63], v[68:69], v[66:67], v[62:63]
	v_mov_b32_e32 v76, v79
	v_pk_mul_f32 v[68:69], v[80:81], v[64:65] op_sel:[0,1] op_sel_hi:[1,0]
	v_pk_add_f32 v[82:83], v[82:83], v[84:85]
	v_pk_fma_f32 v[68:69], v[76:77], v[64:65], v[68:69]
	v_and_b32_e32 v60, 0xffff0000, v60
	v_pk_add_f32 v[58:59], v[82:83], v[58:59]
	v_pk_add_f32 v[62:63], v[62:63], v[68:69]
	s_nop 0
	v_pk_add_f32 v[60:61], v[62:63], v[60:61]
	v_and_b32_sdwa v63, v58, v129 dst_sel:DWORD dst_unused:UNUSED_PAD src0_sel:WORD_1 src1_sel:DWORD
	v_add3_u32 v68, v58, v63, s4
	v_and_b32_sdwa v63, v61, v129 dst_sel:DWORD dst_unused:UNUSED_PAD src0_sel:WORD_1 src1_sel:DWORD
	v_and_b32_sdwa v69, v60, v129 dst_sel:DWORD dst_unused:UNUSED_PAD src0_sel:WORD_1 src1_sel:DWORD
	v_and_b32_sdwa v62, v59, v129 dst_sel:DWORD dst_unused:UNUSED_PAD src0_sel:WORD_1 src1_sel:DWORD
	v_add3_u32 v63, v61, v63, s4
	v_add3_u32 v69, v60, v69, s4
	v_add3_u32 v62, v59, v62, s4
	v_and_b32_e32 v63, 0xffff0000, v63
	v_and_b32_e32 v69, 0xffff0000, v69
	v_or_b32_sdwa v63, v63, v62 dst_sel:DWORD dst_unused:UNUSED_PAD src0_sel:DWORD src1_sel:WORD_1
	v_or_b32_sdwa v62, v69, v68 dst_sel:DWORD dst_unused:UNUSED_PAD src0_sel:DWORD src1_sel:WORD_1
	global_store_dwordx2 v[30:31], v[62:63], off
	v_pk_mul_f32 v[62:63], v[60:61], v[60:61]
	s_nop 0
	v_pk_fma_f32 v[70:71], v[58:59], v[58:59], v[62:63]
	v_cvt_pk_f32_fp8_e32 v[62:63], v180
	v_cvt_pk_f32_fp8_sdwa v[74:75], v181 src0_sel:WORD_1
	v_cvt_pk_f32_fp8_sdwa v[68:69], v180 src0_sel:WORD_1
	v_cvt_pk_f32_fp8_e32 v[72:73], v181
	v_cvt_pk_f32_fp8_e32 v[76:77], v185
	s_waitcnt vmcnt(63)
	v_cvt_pk_f32_fp8_sdwa v[82:83], v187 src0_sel:WORD_1
	v_cvt_pk_f32_fp8_sdwa v[78:79], v185 src0_sel:WORD_1
	v_cvt_pk_f32_fp8_e32 v[80:81], v187
	v_mov_b32_e32 v180, v62
	v_mov_b32_e32 v181, v74
	v_lshlrev_b32_e32 v85, 16, v55
	v_lshlrev_b32_e32 v84, 16, v54
	v_and_b32_e32 v87, 0xffff0000, v55
	v_and_b32_e32 v86, 0xffff0000, v54
	v_mov_b32_e32 v54, v72
	v_mov_b32_e32 v55, v68
	v_pk_mul_f32 v[180:181], v[180:181], v[66:67] op_sel:[0,1] op_sel_hi:[1,0]
	v_mov_b32_e32 v188, v76
	v_mov_b32_e32 v189, v82
	v_mov_b32_e32 v74, v63
	v_pk_fma_f32 v[54:55], v[54:55], v[66:67], v[180:181]
	v_mov_b32_e32 v180, v80
	v_mov_b32_e32 v181, v78
	v_pk_mul_f32 v[188:189], v[188:189], v[64:65] op_sel:[0,1] op_sel_hi:[1,0]
	v_mov_b32_e32 v68, v73
	v_pk_mul_f32 v[62:63], v[74:75], v[66:67] op_sel:[0,1] op_sel_hi:[1,0]
	v_mov_b32_e32 v82, v77
	v_pk_fma_f32 v[180:181], v[180:181], v[64:65], v[188:189]
	v_pk_fma_f32 v[62:63], v[68:69], v[66:67], v[62:63]
	v_mov_b32_e32 v78, v81
	v_pk_mul_f32 v[68:69], v[82:83], v[64:65] op_sel:[0,1] op_sel_hi:[1,0]
	v_pk_add_f32 v[54:55], v[54:55], v[180:181]
	v_pk_fma_f32 v[68:69], v[78:79], v[64:65], v[68:69]
	v_pk_add_f32 v[54:55], v[54:55], v[84:85]
	v_pk_add_f32 v[62:63], v[62:63], v[68:69]
	v_and_b32_sdwa v69, v54, v129 dst_sel:DWORD dst_unused:UNUSED_PAD src0_sel:WORD_1 src1_sel:DWORD
	v_pk_add_f32 v[62:63], v[62:63], v[86:87]
	v_add3_u32 v72, v54, v69, s4
	v_and_b32_sdwa v69, v63, v129 dst_sel:DWORD dst_unused:UNUSED_PAD src0_sel:WORD_1 src1_sel:DWORD
	v_and_b32_sdwa v73, v62, v129 dst_sel:DWORD dst_unused:UNUSED_PAD src0_sel:WORD_1 src1_sel:DWORD
	v_and_b32_sdwa v68, v55, v129 dst_sel:DWORD dst_unused:UNUSED_PAD src0_sel:WORD_1 src1_sel:DWORD
	v_add3_u32 v69, v63, v69, s4
	v_add3_u32 v73, v62, v73, s4
	v_add3_u32 v68, v55, v68, s4
	v_and_b32_e32 v69, 0xffff0000, v69
	v_and_b32_e32 v73, 0xffff0000, v73
	v_or_b32_sdwa v69, v69, v68 dst_sel:DWORD dst_unused:UNUSED_PAD src0_sel:DWORD src1_sel:WORD_1
	v_or_b32_sdwa v68, v73, v72 dst_sel:DWORD dst_unused:UNUSED_PAD src0_sel:DWORD src1_sel:WORD_1
	global_store_dwordx2 v[30:31], v[68:69], off offset:512
	v_pk_mul_f32 v[68:69], v[62:63], v[62:63]
	s_nop 0
	v_pk_fma_f32 v[76:77], v[54:55], v[54:55], v[68:69]
	v_cvt_pk_f32_fp8_e32 v[68:69], v172
	v_cvt_pk_f32_fp8_sdwa v[78:79], v173 src0_sel:WORD_1
	v_cvt_pk_f32_fp8_sdwa v[72:73], v172 src0_sel:WORD_1
	v_cvt_pk_f32_fp8_e32 v[74:75], v173
	v_cvt_pk_f32_fp8_e32 v[80:81], v177
	s_waitcnt vmcnt(63)
	v_cvt_pk_f32_fp8_sdwa v[86:87], v179 src0_sel:WORD_1
	v_cvt_pk_f32_fp8_sdwa v[82:83], v177 src0_sel:WORD_1
	v_cvt_pk_f32_fp8_e32 v[84:85], v179
	v_mov_b32_e32 v188, v68
	v_mov_b32_e32 v189, v78
	v_lshlrev_b32_e32 v173, 16, v47
	v_lshlrev_b32_e32 v172, 16, v46
	v_and_b32_e32 v181, 0xffff0000, v47
	v_and_b32_e32 v180, 0xffff0000, v46
	v_mov_b32_e32 v46, v74
	v_mov_b32_e32 v47, v72
	v_pk_mul_f32 v[188:189], v[188:189], v[66:67] op_sel:[0,1] op_sel_hi:[1,0]
	v_mov_b32_e32 v192, v80
	v_mov_b32_e32 v193, v86
	v_mov_b32_e32 v78, v69
	v_pk_fma_f32 v[46:47], v[46:47], v[66:67], v[188:189]
	v_mov_b32_e32 v188, v84
	v_mov_b32_e32 v189, v82
	v_pk_mul_f32 v[192:193], v[192:193], v[64:65] op_sel:[0,1] op_sel_hi:[1,0]
	v_mov_b32_e32 v72, v75
	v_pk_mul_f32 v[68:69], v[78:79], v[66:67] op_sel:[0,1] op_sel_hi:[1,0]
	v_mov_b32_e32 v86, v81
	v_pk_fma_f32 v[188:189], v[188:189], v[64:65], v[192:193]
	v_pk_fma_f32 v[68:69], v[72:73], v[66:67], v[68:69]
	v_mov_b32_e32 v82, v85
	v_pk_mul_f32 v[72:73], v[86:87], v[64:65] op_sel:[0,1] op_sel_hi:[1,0]
	v_pk_add_f32 v[46:47], v[46:47], v[188:189]
	v_pk_fma_f32 v[72:73], v[82:83], v[64:65], v[72:73]
	v_pk_add_f32 v[46:47], v[46:47], v[172:173]
	v_pk_add_f32 v[68:69], v[68:69], v[72:73]
	v_and_b32_sdwa v73, v46, v129 dst_sel:DWORD dst_unused:UNUSED_PAD src0_sel:WORD_1 src1_sel:DWORD
	v_pk_add_f32 v[68:69], v[68:69], v[180:181]
	v_add3_u32 v74, v46, v73, s4
	v_and_b32_sdwa v73, v69, v129 dst_sel:DWORD dst_unused:UNUSED_PAD src0_sel:WORD_1 src1_sel:DWORD
	v_and_b32_sdwa v75, v68, v129 dst_sel:DWORD dst_unused:UNUSED_PAD src0_sel:WORD_1 src1_sel:DWORD
	v_and_b32_sdwa v72, v47, v129 dst_sel:DWORD dst_unused:UNUSED_PAD src0_sel:WORD_1 src1_sel:DWORD
	v_add3_u32 v73, v69, v73, s4
	v_add3_u32 v75, v68, v75, s4
	v_add3_u32 v72, v47, v72, s4
	v_and_b32_e32 v73, 0xffff0000, v73
	v_and_b32_e32 v75, 0xffff0000, v75
	v_or_b32_sdwa v73, v73, v72 dst_sel:DWORD dst_unused:UNUSED_PAD src0_sel:DWORD src1_sel:WORD_1
	v_or_b32_sdwa v72, v75, v74 dst_sel:DWORD dst_unused:UNUSED_PAD src0_sel:DWORD src1_sel:WORD_1
	global_store_dwordx2 v[30:31], v[72:73], off offset:1024
	v_pk_mul_f32 v[72:73], v[68:69], v[68:69]
	s_nop 0
	v_pk_fma_f32 v[80:81], v[46:47], v[46:47], v[72:73]
	v_cvt_pk_f32_fp8_e32 v[72:73], v164
	v_cvt_pk_f32_fp8_sdwa v[82:83], v165 src0_sel:WORD_1
	v_cvt_pk_f32_fp8_sdwa v[74:75], v164 src0_sel:WORD_1
	v_cvt_pk_f32_fp8_e32 v[78:79], v165
	v_cvt_pk_f32_fp8_e32 v[84:85], v169
	s_waitcnt vmcnt(63)
	v_cvt_pk_f32_fp8_sdwa v[172:173], v171 src0_sel:WORD_1
	v_cvt_pk_f32_fp8_sdwa v[86:87], v169 src0_sel:WORD_1
	v_cvt_pk_f32_fp8_e32 v[164:165], v171
	v_mov_b32_e32 v192, v72
	v_mov_b32_e32 v193, v82
	v_lshlrev_b32_e32 v181, 16, v43
	v_lshlrev_b32_e32 v180, 16, v42
	v_and_b32_e32 v189, 0xffff0000, v43
	v_and_b32_e32 v188, 0xffff0000, v42
	v_mov_b32_e32 v42, v78
	v_mov_b32_e32 v43, v74
	v_pk_mul_f32 v[192:193], v[192:193], v[66:67] op_sel:[0,1] op_sel_hi:[1,0]
	v_mov_b32_e32 v194, v84
	v_mov_b32_e32 v195, v172
	v_mov_b32_e32 v82, v73
	v_pk_fma_f32 v[42:43], v[42:43], v[66:67], v[192:193]
	v_mov_b32_e32 v192, v164
	v_mov_b32_e32 v193, v86
	v_pk_mul_f32 v[194:195], v[194:195], v[64:65] op_sel:[0,1] op_sel_hi:[1,0]
	v_mov_b32_e32 v74, v79
	v_pk_mul_f32 v[72:73], v[82:83], v[66:67] op_sel:[0,1] op_sel_hi:[1,0]
	v_mov_b32_e32 v172, v85
	v_pk_fma_f32 v[192:193], v[192:193], v[64:65], v[194:195]
	v_pk_fma_f32 v[72:73], v[74:75], v[66:67], v[72:73]
	v_mov_b32_e32 v86, v165
	v_pk_mul_f32 v[74:75], v[172:173], v[64:65] op_sel:[0,1] op_sel_hi:[1,0]
	v_pk_add_f32 v[42:43], v[42:43], v[192:193]
	v_pk_fma_f32 v[74:75], v[86:87], v[64:65], v[74:75]
	v_pk_add_f32 v[42:43], v[42:43], v[180:181]
	v_pk_add_f32 v[72:73], v[72:73], v[74:75]
	v_and_b32_sdwa v75, v42, v129 dst_sel:DWORD dst_unused:UNUSED_PAD src0_sel:WORD_1 src1_sel:DWORD
	v_pk_add_f32 v[72:73], v[72:73], v[188:189]
	v_add3_u32 v78, v42, v75, s4
	v_and_b32_sdwa v75, v73, v129 dst_sel:DWORD dst_unused:UNUSED_PAD src0_sel:WORD_1 src1_sel:DWORD
	v_and_b32_sdwa v79, v72, v129 dst_sel:DWORD dst_unused:UNUSED_PAD src0_sel:WORD_1 src1_sel:DWORD
	v_and_b32_sdwa v74, v43, v129 dst_sel:DWORD dst_unused:UNUSED_PAD src0_sel:WORD_1 src1_sel:DWORD
	v_add3_u32 v75, v73, v75, s4
	v_add3_u32 v79, v72, v79, s4
	v_add3_u32 v74, v43, v74, s4
	v_and_b32_e32 v75, 0xffff0000, v75
	v_and_b32_e32 v79, 0xffff0000, v79
	v_or_b32_sdwa v75, v75, v74 dst_sel:DWORD dst_unused:UNUSED_PAD src0_sel:DWORD src1_sel:WORD_1
	v_or_b32_sdwa v74, v79, v78 dst_sel:DWORD dst_unused:UNUSED_PAD src0_sel:DWORD src1_sel:WORD_1
	global_store_dwordx2 v[30:31], v[74:75], off offset:1536
	v_pk_mul_f32 v[74:75], v[72:73], v[72:73]
	s_nop 0
	v_pk_fma_f32 v[86:87], v[42:43], v[42:43], v[74:75]
	v_cvt_pk_f32_fp8_e32 v[74:75], v156
	v_cvt_pk_f32_fp8_sdwa v[84:85], v157 src0_sel:WORD_1
	v_cvt_pk_f32_fp8_sdwa v[78:79], v156 src0_sel:WORD_1
	v_cvt_pk_f32_fp8_e32 v[82:83], v157
	v_cvt_pk_f32_fp8_e32 v[156:157], v162
	v_cvt_pk_f32_fp8_sdwa v[164:165], v162 src0_sel:WORD_1
	s_waitcnt vmcnt(63)
	v_cvt_pk_f32_fp8_e32 v[172:173], v163
	v_cvt_pk_f32_fp8_sdwa v[162:163], v163 src0_sel:WORD_1
	v_mov_b32_e32 v192, v74
	v_mov_b32_e32 v193, v84
	v_lshlrev_b32_e32 v181, 16, v41
	v_lshlrev_b32_e32 v180, 16, v40
	v_and_b32_e32 v189, 0xffff0000, v41
	v_and_b32_e32 v188, 0xffff0000, v40
	v_mov_b32_e32 v40, v82
	v_mov_b32_e32 v41, v78
	v_pk_mul_f32 v[192:193], v[192:193], v[66:67] op_sel:[0,1] op_sel_hi:[1,0]
	v_mov_b32_e32 v194, v156
	v_mov_b32_e32 v195, v162
	v_mov_b32_e32 v84, v75
	v_pk_fma_f32 v[40:41], v[40:41], v[66:67], v[192:193]
	v_mov_b32_e32 v192, v172
	v_mov_b32_e32 v193, v164
	v_pk_mul_f32 v[194:195], v[194:195], v[64:65] op_sel:[0,1] op_sel_hi:[1,0]
	v_mov_b32_e32 v78, v83
	v_pk_mul_f32 v[74:75], v[84:85], v[66:67] op_sel:[0,1] op_sel_hi:[1,0]
	v_mov_b32_e32 v162, v157
	v_pk_fma_f32 v[192:193], v[192:193], v[64:65], v[194:195]
	v_pk_fma_f32 v[74:75], v[78:79], v[66:67], v[74:75]
	v_mov_b32_e32 v164, v173
	v_pk_mul_f32 v[78:79], v[162:163], v[64:65] op_sel:[0,1] op_sel_hi:[1,0]
	v_pk_add_f32 v[40:41], v[40:41], v[192:193]
	v_pk_fma_f32 v[78:79], v[164:165], v[64:65], v[78:79]
	v_pk_add_f32 v[40:41], v[40:41], v[180:181]
	v_pk_add_f32 v[74:75], v[74:75], v[78:79]
	v_and_b32_sdwa v79, v40, v129 dst_sel:DWORD dst_unused:UNUSED_PAD src0_sel:WORD_1 src1_sel:DWORD
	v_pk_add_f32 v[74:75], v[74:75], v[188:189]
	v_add3_u32 v82, v40, v79, s4
	v_and_b32_sdwa v79, v75, v129 dst_sel:DWORD dst_unused:UNUSED_PAD src0_sel:WORD_1 src1_sel:DWORD
	v_and_b32_sdwa v83, v74, v129 dst_sel:DWORD dst_unused:UNUSED_PAD src0_sel:WORD_1 src1_sel:DWORD
	v_and_b32_sdwa v78, v41, v129 dst_sel:DWORD dst_unused:UNUSED_PAD src0_sel:WORD_1 src1_sel:DWORD
	v_add3_u32 v79, v75, v79, s4
	v_add3_u32 v83, v74, v83, s4
	v_add3_u32 v78, v41, v78, s4
	v_and_b32_e32 v79, 0xffff0000, v79
	v_and_b32_e32 v83, 0xffff0000, v83
	v_or_b32_sdwa v79, v79, v78 dst_sel:DWORD dst_unused:UNUSED_PAD src0_sel:DWORD src1_sel:WORD_1
	v_or_b32_sdwa v78, v83, v82 dst_sel:DWORD dst_unused:UNUSED_PAD src0_sel:DWORD src1_sel:WORD_1
	global_store_dwordx2 v[30:31], v[78:79], off offset:2048
	v_pk_mul_f32 v[78:79], v[74:75], v[74:75]
	s_nop 0
	v_pk_fma_f32 v[156:157], v[40:41], v[40:41], v[78:79]
	v_cvt_pk_f32_fp8_e32 v[78:79], v147
	v_cvt_pk_f32_fp8_sdwa v[162:163], v152 src0_sel:WORD_1
	v_cvt_pk_f32_fp8_sdwa v[82:83], v147 src0_sel:WORD_1
	v_cvt_pk_f32_fp8_e32 v[84:85], v152
	v_cvt_pk_f32_fp8_e32 v[164:165], v154
	v_cvt_pk_f32_fp8_sdwa v[172:173], v154 src0_sel:WORD_1
	s_waitcnt vmcnt(63)
	v_cvt_pk_f32_fp8_e32 v[180:181], v155
	v_cvt_pk_f32_fp8_sdwa v[154:155], v155 src0_sel:WORD_1
	v_mov_b32_e32 v194, v78
	v_mov_b32_e32 v195, v162
	v_lshlrev_b32_e32 v189, 16, v37
	v_lshlrev_b32_e32 v188, 16, v36
	v_and_b32_e32 v193, 0xffff0000, v37
	v_and_b32_e32 v192, 0xffff0000, v36
	v_mov_b32_e32 v36, v84
	v_mov_b32_e32 v37, v82
	v_pk_mul_f32 v[194:195], v[194:195], v[66:67] op_sel:[0,1] op_sel_hi:[1,0]
	v_mov_b32_e32 v196, v164
	v_mov_b32_e32 v197, v154
	v_mov_b32_e32 v162, v79
	v_pk_fma_f32 v[36:37], v[36:37], v[66:67], v[194:195]
	v_mov_b32_e32 v194, v180
	v_mov_b32_e32 v195, v172
	v_pk_mul_f32 v[196:197], v[196:197], v[64:65] op_sel:[0,1] op_sel_hi:[1,0]
	v_mov_b32_e32 v82, v85
	v_pk_mul_f32 v[78:79], v[162:163], v[66:67] op_sel:[0,1] op_sel_hi:[1,0]
	v_mov_b32_e32 v154, v165
	v_pk_fma_f32 v[194:195], v[194:195], v[64:65], v[196:197]
	v_pk_fma_f32 v[78:79], v[82:83], v[66:67], v[78:79]
	v_mov_b32_e32 v172, v181
	v_pk_mul_f32 v[82:83], v[154:155], v[64:65] op_sel:[0,1] op_sel_hi:[1,0]
	v_pk_add_f32 v[36:37], v[36:37], v[194:195]
	v_pk_fma_f32 v[82:83], v[172:173], v[64:65], v[82:83]
	v_pk_add_f32 v[36:37], v[36:37], v[188:189]
	v_pk_add_f32 v[78:79], v[78:79], v[82:83]
	v_and_b32_sdwa v83, v36, v129 dst_sel:DWORD dst_unused:UNUSED_PAD src0_sel:WORD_1 src1_sel:DWORD
	v_pk_add_f32 v[78:79], v[78:79], v[192:193]
	v_add3_u32 v84, v36, v83, s4
	v_and_b32_sdwa v83, v79, v129 dst_sel:DWORD dst_unused:UNUSED_PAD src0_sel:WORD_1 src1_sel:DWORD
	v_and_b32_sdwa v85, v78, v129 dst_sel:DWORD dst_unused:UNUSED_PAD src0_sel:WORD_1 src1_sel:DWORD
	v_and_b32_sdwa v82, v37, v129 dst_sel:DWORD dst_unused:UNUSED_PAD src0_sel:WORD_1 src1_sel:DWORD
	v_add3_u32 v83, v79, v83, s4
	v_add3_u32 v85, v78, v85, s4
	v_add3_u32 v82, v37, v82, s4
	v_and_b32_e32 v83, 0xffff0000, v83
	v_and_b32_e32 v85, 0xffff0000, v85
	v_or_b32_sdwa v83, v83, v82 dst_sel:DWORD dst_unused:UNUSED_PAD src0_sel:DWORD src1_sel:WORD_1
	v_or_b32_sdwa v82, v85, v84 dst_sel:DWORD dst_unused:UNUSED_PAD src0_sel:DWORD src1_sel:WORD_1
	global_store_dwordx2 v[30:31], v[82:83], off offset:2560
	v_pk_mul_f32 v[82:83], v[78:79], v[78:79]
	s_nop 0
	v_pk_fma_f32 v[154:155], v[36:37], v[36:37], v[82:83]
	v_cvt_pk_f32_fp8_e32 v[84:85], v142
	v_cvt_pk_f32_fp8_sdwa v[172:173], v144 src0_sel:WORD_1
	v_cvt_pk_f32_fp8_sdwa v[162:163], v142 src0_sel:WORD_1
	v_cvt_pk_f32_fp8_e32 v[164:165], v144
	v_cvt_pk_f32_fp8_e32 v[180:181], v145
	s_waitcnt vmcnt(63)
	v_cvt_pk_f32_fp8_e32 v[188:189], v146
	v_cvt_pk_f32_fp8_sdwa v[146:147], v146 src0_sel:WORD_1
	v_cvt_pk_f32_fp8_sdwa v[144:145], v145 src0_sel:WORD_1
	v_mov_b32_e32 v194, v84
	v_mov_b32_e32 v195, v172
	v_mov_b32_e32 v192, v164
	v_mov_b32_e32 v193, v162
	v_pk_mul_f32 v[194:195], v[194:195], v[66:67] op_sel:[0,1] op_sel_hi:[1,0]
	v_mov_b32_e32 v196, v180
	v_mov_b32_e32 v197, v146
	v_pk_fma_f32 v[192:193], v[192:193], v[66:67], v[194:195]
	v_mov_b32_e32 v194, v188
	v_mov_b32_e32 v195, v144
	v_pk_mul_f32 v[196:197], v[196:197], v[64:65] op_sel:[0,1] op_sel_hi:[1,0]
	v_mov_b32_e32 v172, v85
	v_mov_b32_e32 v146, v181
	v_pk_fma_f32 v[194:195], v[194:195], v[64:65], v[196:197]
	v_mov_b32_e32 v162, v165
	v_pk_mul_f32 v[84:85], v[172:173], v[66:67] op_sel:[0,1] op_sel_hi:[1,0]
	v_mov_b32_e32 v144, v189
	v_pk_mul_f32 v[146:147], v[146:147], v[64:65] op_sel:[0,1] op_sel_hi:[1,0]
	v_lshlrev_b32_e32 v83, 16, v33
	v_lshlrev_b32_e32 v82, 16, v32
	v_pk_add_f32 v[192:193], v[192:193], v[194:195]
	v_pk_fma_f32 v[84:85], v[162:163], v[66:67], v[84:85]
	v_pk_fma_f32 v[144:145], v[144:145], v[64:65], v[146:147]
	v_and_b32_e32 v33, 0xffff0000, v33
	v_and_b32_e32 v32, 0xffff0000, v32
	v_pk_add_f32 v[82:83], v[192:193], v[82:83]
	v_pk_add_f32 v[84:85], v[84:85], v[144:145]
	s_nop 0
	v_pk_add_f32 v[84:85], v[84:85], v[32:33]
	v_and_b32_sdwa v33, v82, v129 dst_sel:DWORD dst_unused:UNUSED_PAD src0_sel:WORD_1 src1_sel:DWORD
	v_add3_u32 v142, v82, v33, s4
	v_and_b32_sdwa v33, v85, v129 dst_sel:DWORD dst_unused:UNUSED_PAD src0_sel:WORD_1 src1_sel:DWORD
	v_and_b32_sdwa v144, v84, v129 dst_sel:DWORD dst_unused:UNUSED_PAD src0_sel:WORD_1 src1_sel:DWORD
	v_and_b32_sdwa v32, v83, v129 dst_sel:DWORD dst_unused:UNUSED_PAD src0_sel:WORD_1 src1_sel:DWORD
	v_add3_u32 v33, v85, v33, s4
	v_add3_u32 v144, v84, v144, s4
	v_add3_u32 v32, v83, v32, s4
	v_and_b32_e32 v33, 0xffff0000, v33
	v_and_b32_e32 v144, 0xffff0000, v144
	v_or_b32_sdwa v33, v33, v32 dst_sel:DWORD dst_unused:UNUSED_PAD src0_sel:DWORD src1_sel:WORD_1
	v_or_b32_sdwa v32, v144, v142 dst_sel:DWORD dst_unused:UNUSED_PAD src0_sel:DWORD src1_sel:WORD_1
	global_store_dwordx2 v[30:31], v[32:33], off offset:3072
	v_pk_mul_f32 v[32:33], v[84:85], v[84:85]
	s_nop 0
	v_pk_fma_f32 v[144:145], v[82:83], v[82:83], v[32:33]
	v_cvt_pk_f32_fp8_e32 v[32:33], v132
	v_cvt_pk_f32_fp8_sdwa v[164:165], v134 src0_sel:WORD_1
	v_cvt_pk_f32_fp8_sdwa v[146:147], v132 src0_sel:WORD_1
	v_cvt_pk_f32_fp8_e32 v[162:163], v134
	v_cvt_pk_f32_fp8_e32 v[172:173], v135
	s_waitcnt vmcnt(63)
	v_cvt_pk_f32_fp8_sdwa v[188:189], v136 src0_sel:WORD_1
	v_cvt_pk_f32_fp8_sdwa v[134:135], v135 src0_sel:WORD_1
	v_cvt_pk_f32_fp8_e32 v[180:181], v136
	v_mov_b32_e32 v196, v32
	v_mov_b32_e32 v197, v164
	v_lshlrev_b32_e32 v193, 16, v27
	v_lshlrev_b32_e32 v192, 16, v26
	v_and_b32_e32 v195, 0xffff0000, v27
	v_and_b32_e32 v194, 0xffff0000, v26
	v_mov_b32_e32 v26, v162
	v_mov_b32_e32 v27, v146
	v_pk_mul_f32 v[196:197], v[196:197], v[66:67] op_sel:[0,1] op_sel_hi:[1,0]
	v_mov_b32_e32 v200, v172
	v_mov_b32_e32 v201, v188
	v_mov_b32_e32 v164, v33
	v_pk_fma_f32 v[26:27], v[26:27], v[66:67], v[196:197]
	v_mov_b32_e32 v196, v180
	v_mov_b32_e32 v197, v134
	v_pk_mul_f32 v[200:201], v[200:201], v[64:65] op_sel:[0,1] op_sel_hi:[1,0]
	v_mov_b32_e32 v146, v163
	v_pk_mul_f32 v[32:33], v[164:165], v[66:67] op_sel:[0,1] op_sel_hi:[1,0]
	v_mov_b32_e32 v188, v173
	v_pk_fma_f32 v[196:197], v[196:197], v[64:65], v[200:201]
	v_pk_fma_f32 v[32:33], v[146:147], v[66:67], v[32:33]
	v_mov_b32_e32 v134, v181
	v_pk_mul_f32 v[66:67], v[188:189], v[64:65] op_sel:[0,1] op_sel_hi:[1,0]
	v_pk_add_f32 v[26:27], v[26:27], v[196:197]
	v_pk_fma_f32 v[64:65], v[134:135], v[64:65], v[66:67]
	v_pk_add_f32 v[26:27], v[26:27], v[192:193]
	v_pk_add_f32 v[32:33], v[32:33], v[64:65]
	v_and_b32_sdwa v65, v26, v129 dst_sel:DWORD dst_unused:UNUSED_PAD src0_sel:WORD_1 src1_sel:DWORD
	v_pk_add_f32 v[32:33], v[32:33], v[194:195]
	v_add3_u32 v66, v26, v65, s4
	v_and_b32_sdwa v65, v33, v129 dst_sel:DWORD dst_unused:UNUSED_PAD src0_sel:WORD_1 src1_sel:DWORD
	v_and_b32_sdwa v67, v32, v129 dst_sel:DWORD dst_unused:UNUSED_PAD src0_sel:WORD_1 src1_sel:DWORD
	v_and_b32_sdwa v64, v27, v129 dst_sel:DWORD dst_unused:UNUSED_PAD src0_sel:WORD_1 src1_sel:DWORD
	v_add3_u32 v65, v33, v65, s4
	v_add3_u32 v67, v32, v67, s4
	v_add3_u32 v64, v27, v64, s4
	v_and_b32_e32 v65, 0xffff0000, v65
	v_and_b32_e32 v67, 0xffff0000, v67
	v_or_b32_sdwa v65, v65, v64 dst_sel:DWORD dst_unused:UNUSED_PAD src0_sel:DWORD src1_sel:WORD_1
	v_or_b32_sdwa v64, v67, v66 dst_sel:DWORD dst_unused:UNUSED_PAD src0_sel:DWORD src1_sel:WORD_1
	global_store_dwordx2 v[30:31], v[64:65], off offset:3584
	v_add_f32_e32 v64, v76, v77
	v_add_f32_e32 v65, v70, v71
	v_add_f32_e32 v64, v65, v64
	v_add_f32_e32 v65, v80, v81
	v_add_f32_e32 v64, v64, v65
	v_add_f32_e32 v65, v86, v87
	v_add_f32_e32 v64, v64, v65
	v_add_f32_e32 v65, v156, v157
	v_pk_mul_f32 v[30:31], v[32:33], v[32:33]
	v_add_f32_e32 v64, v64, v65
	v_add_f32_e32 v65, v154, v155
	v_pk_fma_f32 v[30:31], v[26:27], v[26:27], v[30:31]
	v_add_f32_e32 v64, v64, v65
	v_add_f32_e32 v65, v144, v145
	v_add_f32_e32 v64, v64, v65
	v_add_f32_e32 v30, v30, v31
	v_add_f32_e32 v30, v64, v30
	v_mov_b64_e32 v[64:65], v[212:213]
	v_mov_b64_e32 v[66:67], v[214:215]
	ds_bpermute_b32 v31, v1, v30
	s_waitcnt lgkmcnt(0)
	v_add_f32_e32 v30, v30, v31
	ds_bpermute_b32 v31, v90, v30
	s_waitcnt lgkmcnt(0)
	v_add_f32_e32 v30, v30, v31
	ds_bpermute_b32 v31, v91, v30
	s_waitcnt lgkmcnt(0)
	v_add_f32_e32 v30, v30, v31
	ds_bpermute_b32 v31, v92, v30
	s_waitcnt lgkmcnt(0)
	v_add_f32_e32 v30, v30, v31
	ds_bpermute_b32 v31, v93, v30
	s_waitcnt lgkmcnt(0)
	v_add_f32_e32 v30, v30, v31
	ds_bpermute_b32 v31, v94, v30
	s_waitcnt lgkmcnt(0)
	v_add_f32_e32 v30, v30, v31
	v_fmamk_f32 v30, v30, 0x3a000000, v127
	v_mul_f32_e32 v31, 0x4f800000, v30
	v_cmp_gt_f32_e32 vcc, s19, v30
	s_nop 1
	v_cndmask_b32_e32 v30, v30, v31, vcc
	v_sqrt_f32_e32 v31, v30
	s_nop 0
	v_add_u32_e32 v70, -1, v31
	v_add_u32_e32 v71, 1, v31
	v_fma_f32 v76, -v70, v31, v30
	v_fma_f32 v77, -v71, v31, v30
	v_cmp_ge_f32_e64 s[8:9], 0, v76
	s_nop 1
	v_cndmask_b32_e64 v31, v31, v70, s[8:9]
	v_cmp_lt_f32_e64 s[8:9], 0, v77
	s_nop 1
	v_cndmask_b32_e64 v31, v31, v71, s[8:9]
	v_mul_f32_e32 v70, 0x37800000, v31
	v_cndmask_b32_e32 v31, v31, v70, vcc
	v_cmp_class_f32_e32 vcc, v30, v128
	v_mov_b32_e32 v71, 0
	s_nop 0
	v_cndmask_b32_e32 v30, v31, v30, vcc
	v_div_scale_f32 v31, s[0:1], v30, v30, 1.0
	v_rcp_f32_e32 v70, v31
	v_div_scale_f32 v76, vcc, 1.0, v30, 1.0
	v_fma_f32 v77, -v31, v70, 1.0
	v_fmac_f32_e32 v70, v77, v70
	v_mul_f32_e32 v77, v76, v70
	v_fma_f32 v80, -v31, v77, v76
	v_fmac_f32_e32 v77, v80, v70
	v_fma_f32 v31, -v31, v77, v76
	v_div_fmas_f32 v31, v31, v70, v77
	v_div_fixup_f32 v70, v31, v30, 1.0
	v_mul_f32_e32 v30, v70, v58
	v_mul_f32_e32 v31, v70, v60

	v_mul_f32_e32 v30, v64, v30
	v_mul_f32_e32 v31, v65, v31
	v_cvt_pk_fp8_f32 v71, v30, v31
	v_mul_f32_e32 v58, v70, v59
	v_mul_f32_e32 v30, v70, v61
	v_mul_f32_e32 v31, v66, v58
	v_mul_f32_e32 v30, v67, v30
	v_cvt_pk_fp8_f32 v71, v31, v30 op_sel:[0,0,1]
	v_mul_f32_e32 v31, v70, v54
	v_mul_f32_e32 v54, v70, v62
	v_mov_b32_e32 v30, 0
	global_store_dword v[48:49], v71, off offset:2048
	v_mov_b64_e32 v[58:59], v[216:217]
	v_mov_b64_e32 v[60:61], v[218:219]
	v_mul_f32_e32 v55, v70, v55
	v_mul_f32_e32 v47, v70, v47
	v_mul_f32_e32 v43, v70, v43
	v_mul_f32_e32 v41, v70, v41
	v_mul_f32_e32 v37, v70, v37
	v_mul_f32_e32 v26, v70, v26
	v_mov_b32_e32 v66, 0
	v_mul_f32_e32 v27, v70, v27
	s_waitcnt vmcnt(24)
	v_cvt_pk_f32_fp8_sdwa v[76:77], v190 src0_sel:WORD_1

	v_mul_f32_e32 v31, v58, v31
	v_mul_f32_e32 v54, v59, v54
	v_cvt_pk_fp8_f32 v30, v31, v54
	v_mul_f32_e32 v31, v70, v63
	v_mul_f32_e32 v54, v60, v55
	v_mul_f32_e32 v31, v61, v31
	v_cvt_pk_fp8_f32 v30, v54, v31 op_sel:[0,0,1]
	v_mul_f32_e32 v31, v70, v46
	v_mul_f32_e32 v46, v70, v68
	ds_bpermute_b32 v54, v126, v130
	global_store_dword v[48:49], v30, off offset:2304
	v_mov_b64_e32 v[58:59], v[220:221]
	v_mov_b64_e32 v[60:61], v[222:223]
	v_mov_b32_e32 v30, 0
	s_waitcnt lgkmcnt(0)
	v_ashrrev_i32_e32 v55, 31, v54
	v_lshlrev_b64 v[54:55], 11, v[54:55]
	v_lshl_add_u64 v[54:55], v[4:5], 0, v[54:55]

	v_mul_f32_e32 v31, v58, v31
	v_mul_f32_e32 v46, v59, v46
	v_cvt_pk_fp8_f32 v30, v31, v46
	v_mul_f32_e32 v31, v70, v69
	v_mul_f32_e32 v46, v60, v47
	v_mul_f32_e32 v31, v61, v31
	v_cvt_pk_fp8_f32 v30, v46, v31 op_sel:[0,0,1]
	v_mul_f32_e32 v31, v70, v42
	v_mul_f32_e32 v42, v70, v72
	ds_bpermute_b32 v46, v125, v130
	global_store_dword v[48:49], v30, off offset:2560
	v_mov_b64_e32 v[58:59], v[224:225]
	v_mov_b64_e32 v[60:61], v[226:227]
	v_mov_b32_e32 v30, 0
	v_cvt_pk_f32_fp8_sdwa v[68:69], v184 src0_sel:WORD_1
	s_waitcnt lgkmcnt(0)
	v_ashrrev_i32_e32 v47, 31, v46
	v_lshlrev_b64 v[46:47], 11, v[46:47]
	v_lshl_add_u64 v[64:65], v[4:5], 0, v[46:47]
	v_mov_b32_e32 v81, v68

	v_mul_f32_e32 v31, v58, v31
	v_mul_f32_e32 v42, v59, v42
	v_cvt_pk_fp8_f32 v30, v31, v42
	v_mul_f32_e32 v31, v70, v73
	v_mul_f32_e32 v42, v60, v43
	v_mul_f32_e32 v31, v61, v31
	v_cvt_pk_fp8_f32 v30, v42, v31 op_sel:[0,0,1]
	v_mul_f32_e32 v31, v70, v40
	v_mul_f32_e32 v40, v70, v74
	v_cvt_pk_f32_fp8_sdwa v[72:73], v186 src0_sel:WORD_1
	global_store_dword v[48:49], v30, off offset:2816
	v_mov_b64_e32 v[58:59], v[228:229]
	v_mov_b64_e32 v[60:61], v[230:231]
	v_mov_b32_e32 v30, 0

	v_mul_f32_e32 v31, v58, v31
	v_mul_f32_e32 v40, v59, v40
	v_cvt_pk_fp8_f32 v30, v31, v40
	v_mul_f32_e32 v31, v70, v75
	v_mul_f32_e32 v40, v60, v41
	v_mul_f32_e32 v31, v61, v31
	v_cvt_pk_fp8_f32 v30, v40, v31 op_sel:[0,0,1]
	v_mul_f32_e32 v31, v70, v36
	v_mul_f32_e32 v36, v70, v78
	v_add_co_u32_e32 v58, vcc, s39, v20
	global_store_dword v[48:49], v30, off offset:3072
	v_mov_b64_e32 v[40:41], v[232:233]
	v_mov_b64_e32 v[42:43], v[234:235]
	v_mov_b32_e32 v30, 0
	v_addc_co_u32_e32 v59, vcc, 0, v21, vcc
	v_cvt_pk_f32_fp8_e32 v[74:75], v190

	v_mul_f32_e32 v31, v40, v31
	v_mul_f32_e32 v36, v41, v36
	v_cvt_pk_fp8_f32 v30, v31, v36
	v_mul_f32_e32 v31, v70, v79
	v_mul_f32_e32 v36, v42, v37
	v_mul_f32_e32 v31, v43, v31
	v_cvt_pk_fp8_f32 v30, v36, v31 op_sel:[0,0,1]
	v_mul_f32_e32 v31, v70, v82
	v_mul_f32_e32 v36, v70, v84
	v_mul_f32_e32 v37, v70, v83
	global_store_dword v[48:49], v30, off offset:3328
	v_mov_b64_e32 v[40:41], v[236:237]
	v_mov_b64_e32 v[42:43], v[238:239]
	v_mov_b32_e32 v30, 0
	v_mov_b32_e32 v83, v76

	v_mul_f32_e32 v31, v40, v31
	v_mul_f32_e32 v36, v41, v36
	v_cvt_pk_fp8_f32 v30, v31, v36
	v_mul_f32_e32 v31, v70, v85
	v_mul_f32_e32 v36, v42, v37
	v_mul_f32_e32 v31, v43, v31
	v_cvt_pk_fp8_f32 v30, v36, v31 op_sel:[0,0,1]
	ds_bpermute_b32 v36, v124, v130
	global_store_dword v[48:49], v30, off offset:3584
	v_mov_b64_e32 v[40:41], v[240:241]
	v_mov_b64_e32 v[42:43], v[242:243]
	ds_bpermute_b32 v30, v96, v130
	s_waitcnt lgkmcnt(1)
	v_ashrrev_i32_e32 v37, 31, v36
	v_lshlrev_b64 v[36:37], 11, v[36:37]
	v_lshl_add_u64 v[62:63], v[4:5], 0, v[36:37]
	s_waitcnt lgkmcnt(0)
	v_ashrrev_i32_e32 v31, 31, v30
	v_lshlrev_b64 v[30:31], 11, v[30:31]
	v_lshl_add_u64 v[60:61], v[4:5], 0, v[30:31]
	v_mul_f32_e32 v30, v70, v32

	v_mul_f32_e32 v26, v40, v26
	v_mul_f32_e32 v30, v41, v30
	v_cvt_pk_fp8_f32 v66, v26, v30
	v_mul_f32_e32 v26, v70, v33
	v_mul_f32_e32 v27, v42, v27
	v_mul_f32_e32 v26, v43, v26
	v_cvt_pk_fp8_f32 v66, v27, v26 op_sel:[0,0,1]
	v_cvt_pk_f32_fp8_e32 v[70:71], v186
	global_store_dword v[48:49], v66, off offset:3840
	global_load_dwordx2 v[48:49], v[58:59], off
	s_nop 0
	global_load_dwordx2 v[46:47], v[58:59], off offset:512
	global_load_dwordx2 v[42:43], v[58:59], off offset:1024
	global_load_dwordx2 v[40:41], v[58:59], off offset:1536
	global_load_dwordx2 v[36:37], v[58:59], off offset:2048
	global_load_dwordx2 v[32:33], v[58:59], off offset:2560
	global_load_dwordx2 v[30:31], v[58:59], off offset:3072
	global_load_dwordx2 v[26:27], v[58:59], off offset:3584
	global_load_dword v181, v[60:61], off
	global_load_dword v173, v[60:61], off offset:256
	global_load_dword v165, v[60:61], off offset:512
	global_load_dword v157, v[60:61], off offset:768
	global_load_dword v152, v[60:61], off offset:1024
	global_load_dword v144, v[60:61], off offset:1280
	global_load_dword v134, v[60:61], off offset:1536
	global_load_dword v86, v[60:61], off offset:1792
	global_load_dword v185, v[62:63], off
	global_load_dword v177, v[62:63], off offset:256
	global_load_dword v169, v[62:63], off offset:512
	global_load_dword v162, v[62:63], off offset:768
	global_load_dword v154, v[62:63], off offset:1024
	global_load_dword v145, v[62:63], off offset:1280
	global_load_dword v135, v[62:63], off offset:1536
	global_load_dword v87, v[62:63], off offset:1792
	global_load_dword v187, v[64:65], off
	global_load_dword v179, v[64:65], off offset:256
	global_load_dword v171, v[64:65], off offset:512
	global_load_dword v163, v[64:65], off offset:768
	global_load_dword v155, v[64:65], off offset:1024
	global_load_dword v146, v[64:65], off offset:1280
	global_load_dword v136, v[64:65], off offset:1536
	global_load_dword v130, v[64:65], off offset:1792
	global_load_dword v188, v[54:55], off
	global_load_dword v180, v[54:55], off offset:256
	global_load_dword v172, v[54:55], off offset:512
	global_load_dword v164, v[54:55], off offset:768
	global_load_dword v156, v[54:55], off offset:1024
	global_load_dword v147, v[54:55], off offset:1280
	global_load_dword v142, v[54:55], off offset:1536
	global_load_dword v132, v[54:55], off offset:1792
	ds_bpermute_b32 v63, v120, v19
	ds_bpermute_b32 v62, v121, v19
	v_cvt_pk_f32_fp8_e32 v[58:59], v183
	ds_bpermute_b32 v61, v122, v19
	ds_bpermute_b32 v60, v123, v19
	v_cvt_pk_f32_fp8_sdwa v[64:65], v183 src0_sel:WORD_1
	v_cvt_pk_f32_fp8_e32 v[66:67], v184
	v_mov_b32_e32 v80, v58
	s_waitcnt lgkmcnt(2)
	v_pk_mul_f32 v[80:81], v[80:81], v[62:63] op_sel:[0,1] op_sel_hi:[1,0]
	v_mov_b32_e32 v79, v64
	v_mov_b32_e32 v78, v66
	v_mov_b32_e32 v82, v70
	v_mov_b32_e32 v68, v59
	v_pk_fma_f32 v[78:79], v[78:79], v[62:63], v[80:81]
	v_mov_b32_e32 v80, v74
	v_mov_b32_e32 v81, v72
	s_waitcnt lgkmcnt(0)
	v_pk_mul_f32 v[82:83], v[82:83], v[60:61] op_sel:[0,1] op_sel_hi:[1,0]
	v_mov_b32_e32 v64, v67
	v_pk_mul_f32 v[58:59], v[68:69], v[62:63] op_sel:[0,1] op_sel_hi:[1,0]
	v_mov_b32_e32 v76, v71
	v_pk_fma_f32 v[80:81], v[80:81], v[60:61], v[82:83]
	v_pk_fma_f32 v[58:59], v[64:65], v[62:63], v[58:59]
	v_mov_b32_e32 v72, v75
	v_pk_mul_f32 v[64:65], v[76:77], v[60:61] op_sel:[0,1] op_sel_hi:[1,0]
	s_waitcnt vmcnt(56)
	v_lshlrev_b32_e32 v55, 16, v57
	v_lshlrev_b32_e32 v54, 16, v56
	v_pk_add_f32 v[78:79], v[78:79], v[80:81]
	v_pk_fma_f32 v[64:65], v[72:73], v[60:61], v[64:65]
	v_and_b32_e32 v57, 0xffff0000, v57
	v_and_b32_e32 v56, 0xffff0000, v56
	v_pk_add_f32 v[54:55], v[78:79], v[54:55]
	v_pk_add_f32 v[58:59], v[58:59], v[64:65]
	v_add_co_u32_e32 v66, vcc, s40, v20
	v_pk_add_f32 v[56:57], v[58:59], v[56:57]
	v_and_b32_sdwa v59, v54, v129 dst_sel:DWORD dst_unused:UNUSED_PAD src0_sel:WORD_1 src1_sel:DWORD
	v_add3_u32 v64, v54, v59, s4
	v_and_b32_sdwa v59, v57, v129 dst_sel:DWORD dst_unused:UNUSED_PAD src0_sel:WORD_1 src1_sel:DWORD
	v_and_b32_sdwa v65, v56, v129 dst_sel:DWORD dst_unused:UNUSED_PAD src0_sel:WORD_1 src1_sel:DWORD
	v_and_b32_sdwa v58, v55, v129 dst_sel:DWORD dst_unused:UNUSED_PAD src0_sel:WORD_1 src1_sel:DWORD
	v_add3_u32 v59, v57, v59, s4
	v_add3_u32 v65, v56, v65, s4
	v_addc_co_u32_e32 v67, vcc, 0, v21, vcc
	v_add3_u32 v58, v55, v58, s4
	v_and_b32_e32 v59, 0xffff0000, v59
	v_and_b32_e32 v65, 0xffff0000, v65
	v_add_co_u32_e32 v20, vcc, s42, v20
	v_or_b32_sdwa v59, v59, v58 dst_sel:DWORD dst_unused:UNUSED_PAD src0_sel:DWORD src1_sel:WORD_1
	v_or_b32_sdwa v58, v65, v64 dst_sel:DWORD dst_unused:UNUSED_PAD src0_sel:DWORD src1_sel:WORD_1
	v_addc_co_u32_e32 v21, vcc, 0, v21, vcc
	global_store_dwordx2 v[20:21], v[58:59], off offset:-4096
	v_pk_mul_f32 v[58:59], v[56:57], v[56:57]
	s_nop 0
	v_pk_fma_f32 v[68:69], v[54:55], v[54:55], v[58:59]
	v_cvt_pk_f32_fp8_e32 v[58:59], v175
	v_cvt_pk_f32_fp8_sdwa v[72:73], v176 src0_sel:WORD_1
	v_cvt_pk_f32_fp8_sdwa v[64:65], v175 src0_sel:WORD_1
	v_cvt_pk_f32_fp8_e32 v[70:71], v176
	v_cvt_pk_f32_fp8_e32 v[74:75], v178
	v_cvt_pk_f32_fp8_sdwa v[80:81], v182 src0_sel:WORD_1
	v_cvt_pk_f32_fp8_sdwa v[76:77], v178 src0_sel:WORD_1
	v_cvt_pk_f32_fp8_e32 v[78:79], v182
	v_mov_b32_e32 v182, v58
	v_mov_b32_e32 v183, v72
	v_lshlrev_b32_e32 v83, 16, v53
	v_lshlrev_b32_e32 v82, 16, v52
	v_and_b32_e32 v85, 0xffff0000, v53
	v_and_b32_e32 v84, 0xffff0000, v52
	v_mov_b32_e32 v52, v70
	v_mov_b32_e32 v53, v64
	v_pk_mul_f32 v[182:183], v[182:183], v[62:63] op_sel:[0,1] op_sel_hi:[1,0]
	v_mov_b32_e32 v190, v74
	v_mov_b32_e32 v191, v80
	v_mov_b32_e32 v72, v59
	v_pk_fma_f32 v[52:53], v[52:53], v[62:63], v[182:183]
	v_mov_b32_e32 v182, v78
	v_mov_b32_e32 v183, v76
	v_pk_mul_f32 v[190:191], v[190:191], v[60:61] op_sel:[0,1] op_sel_hi:[1,0]
	v_mov_b32_e32 v64, v71
	v_pk_mul_f32 v[58:59], v[72:73], v[62:63] op_sel:[0,1] op_sel_hi:[1,0]
	v_mov_b32_e32 v80, v75
	v_pk_fma_f32 v[182:183], v[182:183], v[60:61], v[190:191]
	v_pk_fma_f32 v[58:59], v[64:65], v[62:63], v[58:59]
	v_mov_b32_e32 v76, v79
	v_pk_mul_f32 v[64:65], v[80:81], v[60:61] op_sel:[0,1] op_sel_hi:[1,0]
	v_pk_add_f32 v[52:53], v[52:53], v[182:183]
	v_pk_fma_f32 v[64:65], v[76:77], v[60:61], v[64:65]
	v_pk_add_f32 v[52:53], v[52:53], v[82:83]
	v_pk_add_f32 v[58:59], v[58:59], v[64:65]
	v_and_b32_sdwa v65, v52, v129 dst_sel:DWORD dst_unused:UNUSED_PAD src0_sel:WORD_1 src1_sel:DWORD
	v_pk_add_f32 v[58:59], v[58:59], v[84:85]
	v_add3_u32 v70, v52, v65, s4
	v_and_b32_sdwa v65, v59, v129 dst_sel:DWORD dst_unused:UNUSED_PAD src0_sel:WORD_1 src1_sel:DWORD
	v_and_b32_sdwa v71, v58, v129 dst_sel:DWORD dst_unused:UNUSED_PAD src0_sel:WORD_1 src1_sel:DWORD
	v_and_b32_sdwa v64, v53, v129 dst_sel:DWORD dst_unused:UNUSED_PAD src0_sel:WORD_1 src1_sel:DWORD
	v_add3_u32 v65, v59, v65, s4
	v_add3_u32 v71, v58, v71, s4
	v_add3_u32 v64, v53, v64, s4
	v_and_b32_e32 v65, 0xffff0000, v65
	v_and_b32_e32 v71, 0xffff0000, v71
	v_or_b32_sdwa v65, v65, v64 dst_sel:DWORD dst_unused:UNUSED_PAD src0_sel:DWORD src1_sel:WORD_1
	v_or_b32_sdwa v64, v71, v70 dst_sel:DWORD dst_unused:UNUSED_PAD src0_sel:DWORD src1_sel:WORD_1
	global_store_dwordx2 v[66:67], v[64:65], off offset:512
	v_pk_mul_f32 v[64:65], v[58:59], v[58:59]
	s_nop 0
	v_pk_fma_f32 v[74:75], v[52:53], v[52:53], v[64:65]
	v_cvt_pk_f32_fp8_e32 v[64:65], v167
	v_cvt_pk_f32_fp8_sdwa v[76:77], v168 src0_sel:WORD_1
	v_cvt_pk_f32_fp8_sdwa v[70:71], v167 src0_sel:WORD_1
	v_cvt_pk_f32_fp8_e32 v[72:73], v168
	v_cvt_pk_f32_fp8_e32 v[78:79], v170
	v_cvt_pk_f32_fp8_sdwa v[84:85], v174 src0_sel:WORD_1
	v_cvt_pk_f32_fp8_sdwa v[80:81], v170 src0_sel:WORD_1
	v_cvt_pk_f32_fp8_e32 v[82:83], v174
	v_mov_b32_e32 v190, v64
	v_mov_b32_e32 v191, v76
	v_lshlrev_b32_e32 v175, 16, v51
	v_lshlrev_b32_e32 v174, 16, v50
	v_and_b32_e32 v183, 0xffff0000, v51
	v_and_b32_e32 v182, 0xffff0000, v50
	v_mov_b32_e32 v50, v72
	v_mov_b32_e32 v51, v70
	v_pk_mul_f32 v[190:191], v[190:191], v[62:63] op_sel:[0,1] op_sel_hi:[1,0]
	v_mov_b32_e32 v192, v78
	v_mov_b32_e32 v193, v84
	v_mov_b32_e32 v76, v65
	v_pk_fma_f32 v[50:51], v[50:51], v[62:63], v[190:191]
	v_mov_b32_e32 v190, v82
	v_mov_b32_e32 v191, v80
	v_pk_mul_f32 v[192:193], v[192:193], v[60:61] op_sel:[0,1] op_sel_hi:[1,0]
	v_mov_b32_e32 v70, v73
	v_pk_mul_f32 v[64:65], v[76:77], v[62:63] op_sel:[0,1] op_sel_hi:[1,0]
	v_mov_b32_e32 v84, v79
	v_pk_fma_f32 v[190:191], v[190:191], v[60:61], v[192:193]
	v_pk_fma_f32 v[64:65], v[70:71], v[62:63], v[64:65]
	v_mov_b32_e32 v80, v83
	v_pk_mul_f32 v[70:71], v[84:85], v[60:61] op_sel:[0,1] op_sel_hi:[1,0]
	v_pk_add_f32 v[50:51], v[50:51], v[190:191]
	v_pk_fma_f32 v[70:71], v[80:81], v[60:61], v[70:71]
	v_pk_add_f32 v[50:51], v[50:51], v[174:175]
	v_pk_add_f32 v[64:65], v[64:65], v[70:71]
	v_and_b32_sdwa v71, v50, v129 dst_sel:DWORD dst_unused:UNUSED_PAD src0_sel:WORD_1 src1_sel:DWORD
	v_pk_add_f32 v[64:65], v[64:65], v[182:183]
	v_add3_u32 v72, v50, v71, s4
	v_and_b32_sdwa v71, v65, v129 dst_sel:DWORD dst_unused:UNUSED_PAD src0_sel:WORD_1 src1_sel:DWORD
	v_and_b32_sdwa v73, v64, v129 dst_sel:DWORD dst_unused:UNUSED_PAD src0_sel:WORD_1 src1_sel:DWORD
	v_and_b32_sdwa v70, v51, v129 dst_sel:DWORD dst_unused:UNUSED_PAD src0_sel:WORD_1 src1_sel:DWORD
	v_add3_u32 v71, v65, v71, s4
	v_add3_u32 v73, v64, v73, s4
	v_add3_u32 v70, v51, v70, s4
	v_and_b32_e32 v71, 0xffff0000, v71
	v_and_b32_e32 v73, 0xffff0000, v73
	v_or_b32_sdwa v71, v71, v70 dst_sel:DWORD dst_unused:UNUSED_PAD src0_sel:DWORD src1_sel:WORD_1
	v_or_b32_sdwa v70, v73, v72 dst_sel:DWORD dst_unused:UNUSED_PAD src0_sel:DWORD src1_sel:WORD_1
	global_store_dwordx2 v[66:67], v[70:71], off offset:1024
	v_pk_mul_f32 v[70:71], v[64:65], v[64:65]
	s_nop 0
	v_pk_fma_f32 v[80:81], v[50:51], v[50:51], v[70:71]
	v_cvt_pk_f32_fp8_e32 v[70:71], v159
	v_cvt_pk_f32_fp8_sdwa v[78:79], v160 src0_sel:WORD_1
	v_cvt_pk_f32_fp8_sdwa v[72:73], v159 src0_sel:WORD_1
	v_cvt_pk_f32_fp8_e32 v[76:77], v160
	v_cvt_pk_f32_fp8_e32 v[82:83], v161
	v_cvt_pk_f32_fp8_sdwa v[84:85], v161 src0_sel:WORD_1
	v_cvt_pk_f32_fp8_e32 v[160:161], v166
	v_cvt_pk_f32_fp8_sdwa v[166:167], v166 src0_sel:WORD_1
	v_mov_b32_e32 v190, v70
	v_mov_b32_e32 v191, v78
	v_lshlrev_b32_e32 v175, 16, v45
	v_lshlrev_b32_e32 v174, 16, v44
	v_and_b32_e32 v183, 0xffff0000, v45
	v_and_b32_e32 v182, 0xffff0000, v44
	v_mov_b32_e32 v44, v76
	v_mov_b32_e32 v45, v72
	v_pk_mul_f32 v[190:191], v[190:191], v[62:63] op_sel:[0,1] op_sel_hi:[1,0]
	v_mov_b32_e32 v192, v82
	v_mov_b32_e32 v193, v166
	v_mov_b32_e32 v78, v71
	v_pk_fma_f32 v[44:45], v[44:45], v[62:63], v[190:191]
	v_mov_b32_e32 v190, v160
	v_mov_b32_e32 v191, v84
	v_pk_mul_f32 v[192:193], v[192:193], v[60:61] op_sel:[0,1] op_sel_hi:[1,0]
	v_mov_b32_e32 v72, v77
	v_pk_mul_f32 v[70:71], v[78:79], v[62:63] op_sel:[0,1] op_sel_hi:[1,0]
	v_mov_b32_e32 v166, v83
	v_pk_fma_f32 v[190:191], v[190:191], v[60:61], v[192:193]
	v_pk_fma_f32 v[70:71], v[72:73], v[62:63], v[70:71]
	v_mov_b32_e32 v84, v161
	v_pk_mul_f32 v[72:73], v[166:167], v[60:61] op_sel:[0,1] op_sel_hi:[1,0]
	v_pk_add_f32 v[44:45], v[44:45], v[190:191]
	v_pk_fma_f32 v[72:73], v[84:85], v[60:61], v[72:73]
	v_pk_add_f32 v[44:45], v[44:45], v[174:175]
	v_pk_add_f32 v[70:71], v[70:71], v[72:73]
	v_and_b32_sdwa v73, v44, v129 dst_sel:DWORD dst_unused:UNUSED_PAD src0_sel:WORD_1 src1_sel:DWORD
	v_pk_add_f32 v[70:71], v[70:71], v[182:183]
	v_add3_u32 v76, v44, v73, s4
	v_and_b32_sdwa v73, v71, v129 dst_sel:DWORD dst_unused:UNUSED_PAD src0_sel:WORD_1 src1_sel:DWORD
	v_and_b32_sdwa v77, v70, v129 dst_sel:DWORD dst_unused:UNUSED_PAD src0_sel:WORD_1 src1_sel:DWORD
	v_and_b32_sdwa v72, v45, v129 dst_sel:DWORD dst_unused:UNUSED_PAD src0_sel:WORD_1 src1_sel:DWORD
	v_add3_u32 v73, v71, v73, s4
	v_add3_u32 v77, v70, v77, s4
	v_add3_u32 v72, v45, v72, s4
	v_and_b32_e32 v73, 0xffff0000, v73
	v_and_b32_e32 v77, 0xffff0000, v77
	v_or_b32_sdwa v73, v73, v72 dst_sel:DWORD dst_unused:UNUSED_PAD src0_sel:DWORD src1_sel:WORD_1
	v_or_b32_sdwa v72, v77, v76 dst_sel:DWORD dst_unused:UNUSED_PAD src0_sel:DWORD src1_sel:WORD_1
	global_store_dwordx2 v[66:67], v[72:73], off offset:1536
	v_pk_mul_f32 v[72:73], v[70:71], v[70:71]
	s_nop 0
	v_pk_fma_f32 v[84:85], v[44:45], v[44:45], v[72:73]
	v_cvt_pk_f32_fp8_e32 v[72:73], v150
	v_cvt_pk_f32_fp8_sdwa v[82:83], v151 src0_sel:WORD_1
	v_cvt_pk_f32_fp8_sdwa v[76:77], v150 src0_sel:WORD_1
	v_cvt_pk_f32_fp8_e32 v[78:79], v151
	v_cvt_pk_f32_fp8_e32 v[150:151], v153
	v_cvt_pk_f32_fp8_e32 v[166:167], v158
	v_cvt_pk_f32_fp8_sdwa v[158:159], v158 src0_sel:WORD_1
	v_cvt_pk_f32_fp8_sdwa v[160:161], v153 src0_sel:WORD_1
	v_mov_b32_e32 v190, v72
	v_mov_b32_e32 v191, v82
	v_lshlrev_b32_e32 v175, 16, v39
	v_lshlrev_b32_e32 v174, 16, v38
	v_and_b32_e32 v183, 0xffff0000, v39
	v_and_b32_e32 v182, 0xffff0000, v38
	v_mov_b32_e32 v38, v78
	v_mov_b32_e32 v39, v76
	v_pk_mul_f32 v[190:191], v[190:191], v[62:63] op_sel:[0,1] op_sel_hi:[1,0]
	v_mov_b32_e32 v192, v150
	v_mov_b32_e32 v193, v158
	v_mov_b32_e32 v82, v73
	v_pk_fma_f32 v[38:39], v[38:39], v[62:63], v[190:191]
	v_mov_b32_e32 v190, v166
	v_mov_b32_e32 v191, v160
	v_pk_mul_f32 v[192:193], v[192:193], v[60:61] op_sel:[0,1] op_sel_hi:[1,0]
	v_mov_b32_e32 v76, v79
	v_pk_mul_f32 v[72:73], v[82:83], v[62:63] op_sel:[0,1] op_sel_hi:[1,0]
	v_mov_b32_e32 v158, v151
	v_pk_fma_f32 v[190:191], v[190:191], v[60:61], v[192:193]
	v_pk_fma_f32 v[72:73], v[76:77], v[62:63], v[72:73]
	v_mov_b32_e32 v160, v167
	v_pk_mul_f32 v[76:77], v[158:159], v[60:61] op_sel:[0,1] op_sel_hi:[1,0]
	v_pk_add_f32 v[38:39], v[38:39], v[190:191]
	v_pk_fma_f32 v[76:77], v[160:161], v[60:61], v[76:77]
	v_pk_add_f32 v[38:39], v[38:39], v[174:175]
	v_pk_add_f32 v[72:73], v[72:73], v[76:77]
	v_and_b32_sdwa v77, v38, v129 dst_sel:DWORD dst_unused:UNUSED_PAD src0_sel:WORD_1 src1_sel:DWORD
	v_pk_add_f32 v[72:73], v[72:73], v[182:183]
	v_add3_u32 v78, v38, v77, s4
	v_and_b32_sdwa v77, v73, v129 dst_sel:DWORD dst_unused:UNUSED_PAD src0_sel:WORD_1 src1_sel:DWORD
	v_and_b32_sdwa v79, v72, v129 dst_sel:DWORD dst_unused:UNUSED_PAD src0_sel:WORD_1 src1_sel:DWORD
	v_and_b32_sdwa v76, v39, v129 dst_sel:DWORD dst_unused:UNUSED_PAD src0_sel:WORD_1 src1_sel:DWORD
	v_add3_u32 v77, v73, v77, s4
	v_add3_u32 v79, v72, v79, s4
	v_add3_u32 v76, v39, v76, s4
	v_and_b32_e32 v77, 0xffff0000, v77
	v_and_b32_e32 v79, 0xffff0000, v79
	v_or_b32_sdwa v77, v77, v76 dst_sel:DWORD dst_unused:UNUSED_PAD src0_sel:DWORD src1_sel:WORD_1
	v_or_b32_sdwa v76, v79, v78 dst_sel:DWORD dst_unused:UNUSED_PAD src0_sel:DWORD src1_sel:WORD_1
	global_store_dwordx2 v[66:67], v[76:77], off offset:2048
	v_pk_mul_f32 v[76:77], v[72:73], v[72:73]
	s_nop 0
	v_pk_fma_f32 v[150:151], v[38:39], v[38:39], v[76:77]
	v_cvt_pk_f32_fp8_e32 v[76:77], v141
	v_cvt_pk_f32_fp8_sdwa v[158:159], v143 src0_sel:WORD_1
	v_cvt_pk_f32_fp8_sdwa v[78:79], v141 src0_sel:WORD_1
	v_cvt_pk_f32_fp8_e32 v[82:83], v143
	v_cvt_pk_f32_fp8_e32 v[160:161], v148
	v_cvt_pk_f32_fp8_sdwa v[166:167], v148 src0_sel:WORD_1
	v_cvt_pk_f32_fp8_e32 v[174:175], v149
	v_cvt_pk_f32_fp8_sdwa v[148:149], v149 src0_sel:WORD_1
	v_mov_b32_e32 v192, v76
	v_mov_b32_e32 v193, v158
	v_lshlrev_b32_e32 v183, 16, v35
	v_lshlrev_b32_e32 v182, 16, v34
	v_and_b32_e32 v191, 0xffff0000, v35
	v_and_b32_e32 v190, 0xffff0000, v34
	v_mov_b32_e32 v34, v82
	v_mov_b32_e32 v35, v78
	v_pk_mul_f32 v[192:193], v[192:193], v[62:63] op_sel:[0,1] op_sel_hi:[1,0]
	v_mov_b32_e32 v194, v160
	v_mov_b32_e32 v195, v148
	v_mov_b32_e32 v158, v77
	v_pk_fma_f32 v[34:35], v[34:35], v[62:63], v[192:193]
	v_mov_b32_e32 v192, v174
	v_mov_b32_e32 v193, v166
	v_pk_mul_f32 v[194:195], v[194:195], v[60:61] op_sel:[0,1] op_sel_hi:[1,0]
	v_mov_b32_e32 v78, v83
	v_pk_mul_f32 v[76:77], v[158:159], v[62:63] op_sel:[0,1] op_sel_hi:[1,0]
	v_mov_b32_e32 v148, v161
	v_pk_fma_f32 v[192:193], v[192:193], v[60:61], v[194:195]
	v_pk_fma_f32 v[76:77], v[78:79], v[62:63], v[76:77]
	v_mov_b32_e32 v166, v175
	v_pk_mul_f32 v[78:79], v[148:149], v[60:61] op_sel:[0,1] op_sel_hi:[1,0]
	v_pk_add_f32 v[34:35], v[34:35], v[192:193]
	v_pk_fma_f32 v[78:79], v[166:167], v[60:61], v[78:79]
	v_pk_add_f32 v[34:35], v[34:35], v[182:183]
	v_pk_add_f32 v[76:77], v[76:77], v[78:79]
	s_nop 0
	v_pk_add_f32 v[78:79], v[76:77], v[190:191]
	v_and_b32_sdwa v77, v34, v129 dst_sel:DWORD dst_unused:UNUSED_PAD src0_sel:WORD_1 src1_sel:DWORD
	v_add3_u32 v82, v34, v77, s4
	v_and_b32_sdwa v77, v79, v129 dst_sel:DWORD dst_unused:UNUSED_PAD src0_sel:WORD_1 src1_sel:DWORD
	v_and_b32_sdwa v83, v78, v129 dst_sel:DWORD dst_unused:UNUSED_PAD src0_sel:WORD_1 src1_sel:DWORD
	v_and_b32_sdwa v76, v35, v129 dst_sel:DWORD dst_unused:UNUSED_PAD src0_sel:WORD_1 src1_sel:DWORD
	v_add3_u32 v77, v79, v77, s4
	v_add3_u32 v83, v78, v83, s4
	v_add3_u32 v76, v35, v76, s4
	v_and_b32_e32 v77, 0xffff0000, v77
	v_and_b32_e32 v83, 0xffff0000, v83
	v_or_b32_sdwa v77, v77, v76 dst_sel:DWORD dst_unused:UNUSED_PAD src0_sel:DWORD src1_sel:WORD_1
	v_or_b32_sdwa v76, v83, v82 dst_sel:DWORD dst_unused:UNUSED_PAD src0_sel:DWORD src1_sel:WORD_1
	global_store_dwordx2 v[66:67], v[76:77], off offset:2560
	v_pk_mul_f32 v[76:77], v[78:79], v[78:79]
	s_nop 0
	v_pk_fma_f32 v[148:149], v[34:35], v[34:35], v[76:77]
	v_cvt_pk_f32_fp8_e32 v[76:77], v137
	v_cvt_pk_f32_fp8_sdwa v[160:161], v138 src0_sel:WORD_1
	v_cvt_pk_f32_fp8_sdwa v[82:83], v137 src0_sel:WORD_1
	v_cvt_pk_f32_fp8_e32 v[158:159], v138
	v_cvt_pk_f32_fp8_e32 v[166:167], v139
	v_cvt_pk_f32_fp8_e32 v[174:175], v140
	v_cvt_pk_f32_fp8_sdwa v[140:141], v140 src0_sel:WORD_1
	v_cvt_pk_f32_fp8_sdwa v[138:139], v139 src0_sel:WORD_1
	v_mov_b32_e32 v192, v76
	v_mov_b32_e32 v193, v160
	v_lshlrev_b32_e32 v183, 16, v29
	v_lshlrev_b32_e32 v182, 16, v28
	v_and_b32_e32 v191, 0xffff0000, v29
	v_and_b32_e32 v190, 0xffff0000, v28
	v_mov_b32_e32 v28, v158
	v_mov_b32_e32 v29, v82
	v_pk_mul_f32 v[192:193], v[192:193], v[62:63] op_sel:[0,1] op_sel_hi:[1,0]
	v_mov_b32_e32 v194, v166
	v_mov_b32_e32 v195, v140
	v_mov_b32_e32 v160, v77
	v_pk_fma_f32 v[28:29], v[28:29], v[62:63], v[192:193]
	v_mov_b32_e32 v192, v174
	v_mov_b32_e32 v193, v138
	v_pk_mul_f32 v[194:195], v[194:195], v[60:61] op_sel:[0,1] op_sel_hi:[1,0]
	v_mov_b32_e32 v82, v159
	v_pk_mul_f32 v[76:77], v[160:161], v[62:63] op_sel:[0,1] op_sel_hi:[1,0]
	v_mov_b32_e32 v140, v167
	v_pk_fma_f32 v[192:193], v[192:193], v[60:61], v[194:195]
	v_pk_fma_f32 v[76:77], v[82:83], v[62:63], v[76:77]
	v_mov_b32_e32 v138, v175
	v_pk_mul_f32 v[82:83], v[140:141], v[60:61] op_sel:[0,1] op_sel_hi:[1,0]
	v_pk_add_f32 v[28:29], v[28:29], v[192:193]
	v_pk_fma_f32 v[82:83], v[138:139], v[60:61], v[82:83]
	v_pk_add_f32 v[28:29], v[28:29], v[182:183]
	v_pk_add_f32 v[76:77], v[76:77], v[82:83]
	s_nop 0
	v_pk_add_f32 v[82:83], v[76:77], v[190:191]
	v_and_b32_sdwa v77, v28, v129 dst_sel:DWORD dst_unused:UNUSED_PAD src0_sel:WORD_1 src1_sel:DWORD
	v_add3_u32 v137, v28, v77, s4
	v_and_b32_sdwa v77, v83, v129 dst_sel:DWORD dst_unused:UNUSED_PAD src0_sel:WORD_1 src1_sel:DWORD
	v_and_b32_sdwa v138, v82, v129 dst_sel:DWORD dst_unused:UNUSED_PAD src0_sel:WORD_1 src1_sel:DWORD
	v_and_b32_sdwa v76, v29, v129 dst_sel:DWORD dst_unused:UNUSED_PAD src0_sel:WORD_1 src1_sel:DWORD
	v_add3_u32 v77, v83, v77, s4
	v_add3_u32 v138, v82, v138, s4
	v_add3_u32 v76, v29, v76, s4
	v_and_b32_e32 v77, 0xffff0000, v77
	v_and_b32_e32 v138, 0xffff0000, v138
	v_or_b32_sdwa v77, v77, v76 dst_sel:DWORD dst_unused:UNUSED_PAD src0_sel:DWORD src1_sel:WORD_1
	v_or_b32_sdwa v76, v138, v137 dst_sel:DWORD dst_unused:UNUSED_PAD src0_sel:DWORD src1_sel:WORD_1
	global_store_dwordx2 v[66:67], v[76:77], off offset:3072
	v_pk_mul_f32 v[76:77], v[82:83], v[82:83]
	s_nop 0
	v_pk_fma_f32 v[138:139], v[28:29], v[28:29], v[76:77]
	v_cvt_pk_f32_fp8_e32 v[140:141], v88
	v_cvt_pk_f32_fp8_sdwa v[158:159], v88 src0_sel:WORD_1
	v_cvt_pk_f32_fp8_e32 v[160:161], v89
	v_cvt_pk_f32_fp8_sdwa v[88:89], v89 src0_sel:WORD_1
	v_cvt_pk_f32_fp8_e32 v[166:167], v131
	v_cvt_pk_f32_fp8_sdwa v[190:191], v133 src0_sel:WORD_1
	v_cvt_pk_f32_fp8_sdwa v[174:175], v131 src0_sel:WORD_1
	v_cvt_pk_f32_fp8_e32 v[182:183], v133
	v_mov_b32_e32 v194, v140
	v_mov_b32_e32 v195, v88
	v_mov_b32_e32 v192, v160
	v_mov_b32_e32 v193, v158
	v_pk_mul_f32 v[194:195], v[194:195], v[62:63] op_sel:[0,1] op_sel_hi:[1,0]
	v_mov_b32_e32 v196, v166
	v_mov_b32_e32 v197, v190
	v_mov_b32_e32 v88, v141
	v_pk_fma_f32 v[192:193], v[192:193], v[62:63], v[194:195]
	v_mov_b32_e32 v194, v182
	v_mov_b32_e32 v195, v174
	v_pk_mul_f32 v[196:197], v[196:197], v[60:61] op_sel:[0,1] op_sel_hi:[1,0]
	v_mov_b32_e32 v158, v161
	v_pk_mul_f32 v[88:89], v[88:89], v[62:63] op_sel:[0,1] op_sel_hi:[1,0]
	v_mov_b32_e32 v190, v167
	v_pk_fma_f32 v[194:195], v[194:195], v[60:61], v[196:197]
	v_pk_fma_f32 v[62:63], v[158:159], v[62:63], v[88:89]
	v_mov_b32_e32 v174, v183
	v_pk_mul_f32 v[88:89], v[190:191], v[60:61] op_sel:[0,1] op_sel_hi:[1,0]
	v_lshlrev_b32_e32 v77, 16, v23
	v_lshlrev_b32_e32 v76, 16, v22
	v_pk_add_f32 v[192:193], v[192:193], v[194:195]
	v_pk_fma_f32 v[60:61], v[174:175], v[60:61], v[88:89]
	v_and_b32_e32 v23, 0xffff0000, v23
	v_and_b32_e32 v22, 0xffff0000, v22
	v_pk_add_f32 v[76:77], v[192:193], v[76:77]
	v_pk_add_f32 v[60:61], v[62:63], v[60:61]
	s_nop 0
	v_pk_add_f32 v[60:61], v[60:61], v[22:23]
	v_and_b32_sdwa v23, v76, v129 dst_sel:DWORD dst_unused:UNUSED_PAD src0_sel:WORD_1 src1_sel:DWORD
	v_add3_u32 v62, v76, v23, s4
	v_and_b32_sdwa v23, v61, v129 dst_sel:DWORD dst_unused:UNUSED_PAD src0_sel:WORD_1 src1_sel:DWORD
	v_and_b32_sdwa v63, v60, v129 dst_sel:DWORD dst_unused:UNUSED_PAD src0_sel:WORD_1 src1_sel:DWORD
	v_and_b32_sdwa v22, v77, v129 dst_sel:DWORD dst_unused:UNUSED_PAD src0_sel:WORD_1 src1_sel:DWORD
	v_add3_u32 v23, v61, v23, s4
	v_add3_u32 v63, v60, v63, s4
	v_add3_u32 v22, v77, v22, s4
	v_and_b32_e32 v23, 0xffff0000, v23
	v_and_b32_e32 v63, 0xffff0000, v63
	v_or_b32_sdwa v23, v23, v22 dst_sel:DWORD dst_unused:UNUSED_PAD src0_sel:DWORD src1_sel:WORD_1
	v_or_b32_sdwa v22, v63, v62 dst_sel:DWORD dst_unused:UNUSED_PAD src0_sel:DWORD src1_sel:WORD_1
	v_add_f32_e32 v62, v74, v75
	v_add_f32_e32 v63, v68, v69
	v_add_f32_e32 v62, v63, v62
	v_add_f32_e32 v63, v80, v81
	v_add_f32_e32 v62, v62, v63
	v_add_f32_e32 v63, v84, v85
	v_add_f32_e32 v62, v62, v63
	v_add_f32_e32 v63, v150, v151
	global_store_dwordx2 v[66:67], v[22:23], off offset:3584
	v_pk_mul_f32 v[22:23], v[60:61], v[60:61]
	v_add_f32_e32 v62, v62, v63
	v_add_f32_e32 v63, v148, v149
	v_pk_fma_f32 v[22:23], v[76:77], v[76:77], v[22:23]
	v_add_f32_e32 v62, v62, v63
	v_add_f32_e32 v63, v138, v139
	v_add_f32_e32 v62, v62, v63
	v_add_f32_e32 v22, v22, v23
	v_add_f32_e32 v22, v62, v22
	v_mov_b64_e32 v[66:67], v[212:213]
	v_mov_b64_e32 v[68:69], v[214:215]
	ds_bpermute_b32 v23, v1, v22
	s_waitcnt lgkmcnt(0)
	v_add_f32_e32 v22, v22, v23
	ds_bpermute_b32 v23, v90, v22
	s_waitcnt lgkmcnt(0)
	v_add_f32_e32 v22, v22, v23
	ds_bpermute_b32 v23, v91, v22
	s_waitcnt lgkmcnt(0)
	v_add_f32_e32 v22, v22, v23
	ds_bpermute_b32 v23, v92, v22
	s_waitcnt lgkmcnt(0)
	v_add_f32_e32 v22, v22, v23
	ds_bpermute_b32 v23, v93, v22
	s_waitcnt lgkmcnt(0)
	v_add_f32_e32 v22, v22, v23
	ds_bpermute_b32 v23, v94, v22
	s_waitcnt lgkmcnt(0)
	v_add_f32_e32 v22, v22, v23
	v_fmamk_f32 v22, v22, 0x3a000000, v127
	v_mul_f32_e32 v23, 0x4f800000, v22
	v_cmp_gt_f32_e32 vcc, s19, v22
	s_nop 1
	v_cndmask_b32_e32 v22, v22, v23, vcc
	v_sqrt_f32_e32 v23, v22
	s_nop 0
	v_add_u32_e32 v62, -1, v23
	v_add_u32_e32 v63, 1, v23
	v_fma_f32 v74, -v62, v23, v22
	v_fma_f32 v75, -v63, v23, v22
	v_cmp_ge_f32_e64 s[8:9], 0, v74
	s_nop 1
	v_cndmask_b32_e64 v23, v23, v62, s[8:9]
	v_cmp_lt_f32_e64 s[8:9], 0, v75
	s_nop 1
	v_cndmask_b32_e64 v23, v23, v63, s[8:9]
	v_mul_f32_e32 v62, 0x37800000, v23
	v_cndmask_b32_e32 v23, v23, v62, vcc
	v_cmp_class_f32_e32 vcc, v22, v128
	v_mov_b32_e32 v63, 0
	s_nop 0
	v_cndmask_b32_e32 v22, v23, v22, vcc
	v_div_scale_f32 v23, s[0:1], v22, v22, 1.0
	v_rcp_f32_e32 v62, v23
	v_div_scale_f32 v74, vcc, 1.0, v22, 1.0
	v_fma_f32 v75, -v23, v62, 1.0
	v_fmac_f32_e32 v62, v75, v62
	v_mul_f32_e32 v75, v74, v62
	v_fma_f32 v80, -v23, v75, v74
	v_fmac_f32_e32 v75, v80, v62
	v_fma_f32 v23, -v23, v75, v74
	v_div_fmas_f32 v23, v23, v62, v75
	v_div_fixup_f32 v80, v23, v22, 1.0
	v_mul_f32_e32 v22, v80, v54
	v_mul_f32_e32 v23, v80, v56

	v_mul_f32_e32 v22, v66, v22
	v_mul_f32_e32 v23, v67, v23
	v_cvt_pk_fp8_f32 v63, v22, v23
	v_mul_f32_e32 v54, v80, v55
	v_mul_f32_e32 v22, v80, v57
	v_mul_f32_e32 v23, v68, v54
	v_mul_f32_e32 v22, v69, v22
	v_cvt_pk_fp8_f32 v63, v23, v22 op_sel:[0,0,1]
	v_mul_f32_e32 v23, v80, v52
	v_mul_f32_e32 v52, v80, v58
	v_mov_b32_e32 v22, 0
	global_store_dword v[24:25], v63, off
	v_mov_b64_e32 v[54:55], v[216:217]
	v_mov_b64_e32 v[56:57], v[218:219]
	v_mul_f32_e32 v53, v80, v53
	v_mul_f32_e32 v51, v80, v51
	v_mul_f32_e32 v45, v80, v45
	v_mul_f32_e32 v39, v80, v39
	v_mul_f32_e32 v35, v80, v35
	v_mul_f32_e32 v29, v80, v29
	s_waitcnt vmcnt(16)
	v_cvt_pk_f32_fp8_e32 v[62:63], v188
	v_lshlrev_b32_e32 v67, 16, v49
	v_lshlrev_b32_e32 v66, 16, v48
	v_and_b32_e32 v49, 0xffff0000, v49
	v_and_b32_e32 v48, 0xffff0000, v48

	v_mul_f32_e32 v23, v54, v23
	v_mul_f32_e32 v52, v55, v52
	v_cvt_pk_fp8_f32 v22, v23, v52
	v_mul_f32_e32 v23, v80, v59
	v_mul_f32_e32 v52, v56, v53
	v_mul_f32_e32 v23, v57, v23
	v_cvt_pk_fp8_f32 v22, v52, v23 op_sel:[0,0,1]
	v_mul_f32_e32 v23, v80, v50
	v_mul_f32_e32 v50, v80, v64
	v_cvt_pk_f32_fp8_e32 v[56:57], v187
	global_store_dword v[24:25], v22, off offset:256
	v_mov_b64_e32 v[52:53], v[220:221]
	v_mov_b64_e32 v[54:55], v[222:223]
	v_mov_b32_e32 v22, 0
	v_cvt_pk_f32_fp8_sdwa v[58:59], v187 src0_sel:WORD_1
	v_mov_b32_e32 v74, v56

	v_mul_f32_e32 v23, v52, v23
	v_mul_f32_e32 v50, v53, v50
	v_cvt_pk_fp8_f32 v22, v23, v50
	v_mul_f32_e32 v23, v80, v65
	v_mul_f32_e32 v50, v54, v51
	v_mul_f32_e32 v23, v55, v23
	v_cvt_pk_fp8_f32 v22, v50, v23 op_sel:[0,0,1]
	v_mul_f32_e32 v23, v80, v44
	v_mul_f32_e32 v44, v80, v70
	v_cvt_pk_f32_fp8_sdwa v[64:65], v188 src0_sel:WORD_1
	global_store_dword v[24:25], v22, off offset:512
	v_mov_b64_e32 v[50:51], v[224:225]
	v_mov_b64_e32 v[52:53], v[226:227]
	v_mov_b32_e32 v22, 0
	v_mov_b32_e32 v75, v64
	v_mov_b32_e32 v64, v57

	v_mul_f32_e32 v23, v50, v23
	v_mul_f32_e32 v44, v51, v44
	v_cvt_pk_fp8_f32 v22, v23, v44
	v_mul_f32_e32 v23, v80, v71
	v_mul_f32_e32 v44, v52, v45
	v_mul_f32_e32 v23, v53, v23
	v_cvt_pk_fp8_f32 v22, v44, v23 op_sel:[0,0,1]
	v_mul_f32_e32 v23, v80, v38
	v_mul_f32_e32 v38, v80, v72
	ds_bpermute_b32 v45, v125, v19
	global_store_dword v[24:25], v22, off offset:768
	v_mov_b64_e32 v[50:51], v[228:229]
	v_mov_b64_e32 v[52:53], v[230:231]
	v_mov_b32_e32 v22, 0
	ds_bpermute_b32 v44, v126, v19
	v_mov_b32_e32 v72, v62
	s_waitcnt lgkmcnt(0)
	v_pk_mul_f32 v[56:57], v[64:65], v[44:45] op_sel:[0,1] op_sel_hi:[1,0]

	v_mul_f32_e32 v23, v50, v23
	v_mul_f32_e32 v38, v51, v38
	v_cvt_pk_fp8_f32 v22, v23, v38
	v_mul_f32_e32 v23, v80, v73
	v_mul_f32_e32 v38, v52, v39
	v_mul_f32_e32 v23, v53, v23
	v_cvt_pk_fp8_f32 v22, v38, v23 op_sel:[0,0,1]
	v_mul_f32_e32 v23, v80, v34
	v_mul_f32_e32 v34, v80, v78
	v_cvt_pk_f32_fp8_sdwa v[38:39], v185 src0_sel:WORD_1
	global_store_dword v[24:25], v22, off offset:1024
	v_mov_b64_e32 v[50:51], v[232:233]
	v_mov_b64_e32 v[52:53], v[234:235]
	v_mov_b32_e32 v22, 0
	v_mov_b32_e32 v71, v38
	v_mov_b32_e32 v73, v58
	v_mov_b32_e32 v58, v63
	v_mov_b32_e32 v78, 0

	v_mul_f32_e32 v23, v50, v23
	v_mul_f32_e32 v34, v51, v34
	v_cvt_pk_fp8_f32 v22, v23, v34
	v_mul_f32_e32 v23, v80, v79
	v_mul_f32_e32 v34, v52, v35
	v_mul_f32_e32 v23, v53, v23
	v_cvt_pk_fp8_f32 v22, v34, v23 op_sel:[0,0,1]
	v_mul_f32_e32 v23, v80, v28
	v_mul_f32_e32 v28, v80, v82
	v_cvt_pk_f32_fp8_e32 v[34:35], v185
	global_store_dword v[24:25], v22, off offset:1280
	v_mov_b64_e32 v[50:51], v[236:237]
	v_mov_b64_e32 v[52:53], v[238:239]
	v_mov_b32_e32 v22, 0
	v_mov_b32_e32 v68, v34

	v_mul_f32_e32 v23, v50, v23
	v_mul_f32_e32 v28, v51, v28
	v_cvt_pk_fp8_f32 v22, v23, v28
	v_mul_f32_e32 v23, v80, v83
	v_mul_f32_e32 v28, v52, v29
	v_mul_f32_e32 v23, v53, v23
	v_cvt_pk_fp8_f32 v22, v28, v23 op_sel:[0,0,1]
	ds_bpermute_b32 v51, v96, v19
	ds_bpermute_b32 v50, v124, v19
	v_cvt_pk_f32_fp8_sdwa v[28:29], v181 src0_sel:WORD_1
	global_store_dword v[24:25], v22, off offset:1536
	v_mov_b64_e32 v[52:53], v[240:241]
	v_mov_b64_e32 v[54:55], v[242:243]
	v_cvt_pk_f32_fp8_e32 v[22:23], v181
	v_mov_b32_e32 v69, v28
	v_mov_b32_e32 v28, v35
	v_pk_mul_f32 v[34:35], v[74:75], v[44:45] op_sel:[0,1] op_sel_hi:[1,0]
	v_mov_b32_e32 v70, v22
	v_mov_b32_e32 v38, v23
	s_waitcnt lgkmcnt(0)
	v_pk_mul_f32 v[22:23], v[70:71], v[50:51] op_sel:[0,1] op_sel_hi:[1,0]
	v_pk_mul_f32 v[38:39], v[38:39], v[50:51] op_sel:[0,1] op_sel_hi:[1,0]
	v_pk_fma_f32 v[22:23], v[68:69], v[50:51], v[22:23]
	v_pk_fma_f32 v[34:35], v[72:73], v[44:45], v[34:35]
	v_pk_fma_f32 v[28:29], v[28:29], v[50:51], v[38:39]
	v_pk_fma_f32 v[38:39], v[58:59], v[44:45], v[56:57]
	v_pk_add_f32 v[22:23], v[22:23], v[34:35]
	v_pk_add_f32 v[34:35], v[28:29], v[38:39]
	v_pk_add_f32 v[28:29], v[22:23], v[66:67]
	v_pk_add_f32 v[22:23], v[34:35], v[48:49]
	v_mul_f32_e32 v49, v80, v76
	v_mul_f32_e32 v56, v80, v60
	v_mul_f32_e32 v57, v80, v77
	v_and_b32_sdwa v39, v23, v129 dst_sel:DWORD dst_unused:UNUSED_PAD src0_sel:WORD_1 src1_sel:DWORD
	v_and_b32_sdwa v48, v22, v129 dst_sel:DWORD dst_unused:UNUSED_PAD src0_sel:WORD_1 src1_sel:DWORD
	v_and_b32_sdwa v19, v29, v129 dst_sel:DWORD dst_unused:UNUSED_PAD src0_sel:WORD_1 src1_sel:DWORD
	v_and_b32_sdwa v38, v28, v129 dst_sel:DWORD dst_unused:UNUSED_PAD src0_sel:WORD_1 src1_sel:DWORD
	v_add3_u32 v39, v23, v39, s4
	v_add3_u32 v48, v22, v48, s4
	v_pk_mul_f32 v[34:35], v[22:23], v[22:23]
	v_add3_u32 v38, v28, v38, s4
	v_add3_u32 v19, v29, v19, s4
	v_and_b32_e32 v39, 0xffff0000, v39
	v_and_b32_e32 v48, 0xffff0000, v48
	v_or_b32_sdwa v39, v39, v19 dst_sel:DWORD dst_unused:UNUSED_PAD src0_sel:DWORD src1_sel:WORD_1
	v_or_b32_sdwa v38, v48, v38 dst_sel:DWORD dst_unused:UNUSED_PAD src0_sel:DWORD src1_sel:WORD_1

	v_mul_f32_e32 v49, v52, v49
	v_mul_f32_e32 v52, v53, v56
	v_cvt_pk_fp8_f32 v78, v49, v52
	v_mul_f32_e32 v49, v80, v61
	v_mul_f32_e32 v52, v54, v57
	v_mul_f32_e32 v49, v55, v49
	v_cvt_pk_fp8_f32 v78, v52, v49 op_sel:[0,0,1]
	global_store_dword v[24:25], v78, off offset:1792
	global_store_dwordx2 v[20:21], v[38:39], off
	v_pk_fma_f32 v[48:49], v[28:29], v[28:29], v[34:35]
	v_cvt_pk_f32_fp8_e32 v[38:39], v173
	v_cvt_pk_f32_fp8_sdwa v[56:57], v177 src0_sel:WORD_1
	v_cvt_pk_f32_fp8_sdwa v[52:53], v173 src0_sel:WORD_1
	v_cvt_pk_f32_fp8_e32 v[54:55], v177
	v_cvt_pk_f32_fp8_e32 v[58:59], v179
	s_waitcnt vmcnt(23)
	v_cvt_pk_f32_fp8_sdwa v[64:65], v180 src0_sel:WORD_1
	v_cvt_pk_f32_fp8_sdwa v[60:61], v179 src0_sel:WORD_1
	v_cvt_pk_f32_fp8_e32 v[62:63], v180
	v_mov_b32_e32 v68, v38
	v_mov_b32_e32 v69, v56
	v_mov_b32_e32 v56, v39
	v_mov_b32_e32 v66, v54
	v_mov_b32_e32 v67, v52
	v_pk_mul_f32 v[68:69], v[68:69], v[50:51] op_sel:[0,1] op_sel_hi:[1,0]
	v_mov_b32_e32 v71, v64
	v_mov_b32_e32 v52, v55
	v_pk_mul_f32 v[38:39], v[56:57], v[50:51] op_sel:[0,1] op_sel_hi:[1,0]
	v_mov_b32_e32 v64, v59
	v_pk_fma_f32 v[66:67], v[66:67], v[50:51], v[68:69]
	v_mov_b32_e32 v69, v60
	v_mov_b32_e32 v70, v58
	v_pk_fma_f32 v[38:39], v[52:53], v[50:51], v[38:39]
	v_mov_b32_e32 v60, v63
	v_pk_mul_f32 v[52:53], v[64:65], v[44:45] op_sel:[0,1] op_sel_hi:[1,0]
	v_mov_b32_e32 v68, v62
	v_pk_mul_f32 v[70:71], v[70:71], v[44:45] op_sel:[0,1] op_sel_hi:[1,0]
	v_pk_fma_f32 v[52:53], v[60:61], v[44:45], v[52:53]
	v_lshlrev_b32_e32 v35, 16, v47
	v_lshlrev_b32_e32 v34, 16, v46
	v_and_b32_e32 v47, 0xffff0000, v47
	v_and_b32_e32 v46, 0xffff0000, v46
	v_pk_fma_f32 v[68:69], v[68:69], v[44:45], v[70:71]
	v_pk_add_f32 v[38:39], v[38:39], v[52:53]
	v_pk_add_f32 v[66:67], v[66:67], v[68:69]
	v_pk_add_f32 v[38:39], v[38:39], v[46:47]
	v_pk_add_f32 v[34:35], v[66:67], v[34:35]
	v_and_b32_sdwa v47, v39, v129 dst_sel:DWORD dst_unused:UNUSED_PAD src0_sel:WORD_1 src1_sel:DWORD
	v_and_b32_sdwa v52, v38, v129 dst_sel:DWORD dst_unused:UNUSED_PAD src0_sel:WORD_1 src1_sel:DWORD
	v_and_b32_sdwa v19, v35, v129 dst_sel:DWORD dst_unused:UNUSED_PAD src0_sel:WORD_1 src1_sel:DWORD
	v_and_b32_sdwa v46, v34, v129 dst_sel:DWORD dst_unused:UNUSED_PAD src0_sel:WORD_1 src1_sel:DWORD
	v_add3_u32 v47, v39, v47, s4
	v_add3_u32 v52, v38, v52, s4
	v_add3_u32 v46, v34, v46, s4
	v_add3_u32 v19, v35, v19, s4
	v_and_b32_e32 v47, 0xffff0000, v47
	v_and_b32_e32 v52, 0xffff0000, v52
	v_or_b32_sdwa v47, v47, v19 dst_sel:DWORD dst_unused:UNUSED_PAD src0_sel:DWORD src1_sel:WORD_1
	v_or_b32_sdwa v46, v52, v46 dst_sel:DWORD dst_unused:UNUSED_PAD src0_sel:DWORD src1_sel:WORD_1
	global_store_dwordx2 v[20:21], v[46:47], off offset:512
	v_pk_mul_f32 v[46:47], v[38:39], v[38:39]
	s_nop 0
	v_pk_fma_f32 v[56:57], v[34:35], v[34:35], v[46:47]
	v_cvt_pk_f32_fp8_e32 v[46:47], v165
	v_cvt_pk_f32_fp8_sdwa v[58:59], v169 src0_sel:WORD_1
	v_cvt_pk_f32_fp8_sdwa v[52:53], v165 src0_sel:WORD_1
	v_cvt_pk_f32_fp8_e32 v[54:55], v169
	v_cvt_pk_f32_fp8_e32 v[60:61], v171
	s_waitcnt vmcnt(23)
	v_cvt_pk_f32_fp8_sdwa v[66:67], v172 src0_sel:WORD_1
	v_cvt_pk_f32_fp8_sdwa v[62:63], v171 src0_sel:WORD_1
	v_cvt_pk_f32_fp8_e32 v[64:65], v172
	v_mov_b32_e32 v72, v46
	v_mov_b32_e32 v73, v58
	v_mov_b32_e32 v58, v47
	v_lshlrev_b32_e32 v69, 16, v43
	v_lshlrev_b32_e32 v68, 16, v42
	v_and_b32_e32 v71, 0xffff0000, v43
	v_and_b32_e32 v70, 0xffff0000, v42
	v_mov_b32_e32 v42, v54
	v_mov_b32_e32 v43, v52
	v_pk_mul_f32 v[72:73], v[72:73], v[50:51] op_sel:[0,1] op_sel_hi:[1,0]
	v_mov_b32_e32 v75, v66
	v_mov_b32_e32 v52, v55
	v_pk_mul_f32 v[46:47], v[58:59], v[50:51] op_sel:[0,1] op_sel_hi:[1,0]
	v_mov_b32_e32 v66, v61
	v_pk_fma_f32 v[42:43], v[42:43], v[50:51], v[72:73]
	v_mov_b32_e32 v73, v62
	v_mov_b32_e32 v74, v60
	v_pk_fma_f32 v[46:47], v[52:53], v[50:51], v[46:47]
	v_mov_b32_e32 v62, v65
	v_pk_mul_f32 v[52:53], v[66:67], v[44:45] op_sel:[0,1] op_sel_hi:[1,0]
	v_mov_b32_e32 v72, v64
	v_pk_mul_f32 v[74:75], v[74:75], v[44:45] op_sel:[0,1] op_sel_hi:[1,0]
	v_pk_fma_f32 v[52:53], v[62:63], v[44:45], v[52:53]
	v_pk_fma_f32 v[72:73], v[72:73], v[44:45], v[74:75]
	v_pk_add_f32 v[46:47], v[46:47], v[52:53]
	v_pk_add_f32 v[42:43], v[42:43], v[72:73]
	v_pk_add_f32 v[46:47], v[46:47], v[70:71]
	v_pk_add_f32 v[42:43], v[42:43], v[68:69]
	v_and_b32_sdwa v53, v47, v129 dst_sel:DWORD dst_unused:UNUSED_PAD src0_sel:WORD_1 src1_sel:DWORD
	v_and_b32_sdwa v54, v46, v129 dst_sel:DWORD dst_unused:UNUSED_PAD src0_sel:WORD_1 src1_sel:DWORD
	v_and_b32_sdwa v19, v43, v129 dst_sel:DWORD dst_unused:UNUSED_PAD src0_sel:WORD_1 src1_sel:DWORD
	v_and_b32_sdwa v52, v42, v129 dst_sel:DWORD dst_unused:UNUSED_PAD src0_sel:WORD_1 src1_sel:DWORD
	v_add3_u32 v53, v47, v53, s4
	v_add3_u32 v54, v46, v54, s4
	v_add3_u32 v52, v42, v52, s4
	v_add3_u32 v19, v43, v19, s4
	v_and_b32_e32 v53, 0xffff0000, v53
	v_and_b32_e32 v54, 0xffff0000, v54
	v_or_b32_sdwa v53, v53, v19 dst_sel:DWORD dst_unused:UNUSED_PAD src0_sel:DWORD src1_sel:WORD_1
	v_or_b32_sdwa v52, v54, v52 dst_sel:DWORD dst_unused:UNUSED_PAD src0_sel:DWORD src1_sel:WORD_1
	global_store_dwordx2 v[20:21], v[52:53], off offset:1024
	v_pk_mul_f32 v[52:53], v[46:47], v[46:47]
	s_nop 0
	v_pk_fma_f32 v[60:61], v[42:43], v[42:43], v[52:53]
	v_cvt_pk_f32_fp8_e32 v[52:53], v157
	v_cvt_pk_f32_fp8_sdwa v[62:63], v162 src0_sel:WORD_1
	v_cvt_pk_f32_fp8_sdwa v[54:55], v157 src0_sel:WORD_1
	v_cvt_pk_f32_fp8_e32 v[58:59], v162
	v_cvt_pk_f32_fp8_e32 v[64:65], v163
	s_waitcnt vmcnt(23)
	v_cvt_pk_f32_fp8_sdwa v[70:71], v164 src0_sel:WORD_1
	v_cvt_pk_f32_fp8_sdwa v[66:67], v163 src0_sel:WORD_1
	v_cvt_pk_f32_fp8_e32 v[68:69], v164
	v_mov_b32_e32 v76, v52
	v_mov_b32_e32 v77, v62
	v_mov_b32_e32 v62, v53
	v_lshlrev_b32_e32 v73, 16, v41
	v_lshlrev_b32_e32 v72, 16, v40
	v_and_b32_e32 v75, 0xffff0000, v41
	v_and_b32_e32 v74, 0xffff0000, v40
	v_mov_b32_e32 v40, v58
	v_mov_b32_e32 v41, v54
	v_pk_mul_f32 v[76:77], v[76:77], v[50:51] op_sel:[0,1] op_sel_hi:[1,0]
	v_mov_b32_e32 v79, v70
	v_mov_b32_e32 v54, v59
	v_pk_mul_f32 v[52:53], v[62:63], v[50:51] op_sel:[0,1] op_sel_hi:[1,0]
	v_mov_b32_e32 v70, v65
	v_pk_fma_f32 v[40:41], v[40:41], v[50:51], v[76:77]
	v_mov_b32_e32 v77, v66
	v_mov_b32_e32 v78, v64
	v_pk_fma_f32 v[52:53], v[54:55], v[50:51], v[52:53]
	v_mov_b32_e32 v66, v69
	v_pk_mul_f32 v[54:55], v[70:71], v[44:45] op_sel:[0,1] op_sel_hi:[1,0]
	v_mov_b32_e32 v76, v68
	v_pk_mul_f32 v[78:79], v[78:79], v[44:45] op_sel:[0,1] op_sel_hi:[1,0]
	v_pk_fma_f32 v[54:55], v[66:67], v[44:45], v[54:55]
	v_pk_fma_f32 v[76:77], v[76:77], v[44:45], v[78:79]
	v_pk_add_f32 v[52:53], v[52:53], v[54:55]
	v_pk_add_f32 v[40:41], v[40:41], v[76:77]
	v_pk_add_f32 v[52:53], v[52:53], v[74:75]
	v_pk_add_f32 v[40:41], v[40:41], v[72:73]
	v_and_b32_sdwa v55, v53, v129 dst_sel:DWORD dst_unused:UNUSED_PAD src0_sel:WORD_1 src1_sel:DWORD
	v_and_b32_sdwa v58, v52, v129 dst_sel:DWORD dst_unused:UNUSED_PAD src0_sel:WORD_1 src1_sel:DWORD
	v_and_b32_sdwa v19, v41, v129 dst_sel:DWORD dst_unused:UNUSED_PAD src0_sel:WORD_1 src1_sel:DWORD
	v_and_b32_sdwa v54, v40, v129 dst_sel:DWORD dst_unused:UNUSED_PAD src0_sel:WORD_1 src1_sel:DWORD
	v_add3_u32 v55, v53, v55, s4
	v_add3_u32 v58, v52, v58, s4
	v_add3_u32 v54, v40, v54, s4
	v_add3_u32 v19, v41, v19, s4
	v_and_b32_e32 v55, 0xffff0000, v55
	v_and_b32_e32 v58, 0xffff0000, v58
	v_or_b32_sdwa v55, v55, v19 dst_sel:DWORD dst_unused:UNUSED_PAD src0_sel:DWORD src1_sel:WORD_1
	v_or_b32_sdwa v54, v58, v54 dst_sel:DWORD dst_unused:UNUSED_PAD src0_sel:DWORD src1_sel:WORD_1
	global_store_dwordx2 v[20:21], v[54:55], off offset:1536
	v_pk_mul_f32 v[54:55], v[52:53], v[52:53]
	s_nop 0
	v_pk_fma_f32 v[64:65], v[40:41], v[40:41], v[54:55]
	v_cvt_pk_f32_fp8_e32 v[54:55], v152
	v_cvt_pk_f32_fp8_sdwa v[66:67], v154 src0_sel:WORD_1
	v_cvt_pk_f32_fp8_sdwa v[58:59], v152 src0_sel:WORD_1
	v_cvt_pk_f32_fp8_e32 v[62:63], v154
	v_cvt_pk_f32_fp8_e32 v[68:69], v155
	s_waitcnt vmcnt(23)
	v_cvt_pk_f32_fp8_sdwa v[74:75], v156 src0_sel:WORD_1
	v_cvt_pk_f32_fp8_sdwa v[70:71], v155 src0_sel:WORD_1
	v_cvt_pk_f32_fp8_e32 v[72:73], v156
	v_mov_b32_e32 v80, v54
	v_mov_b32_e32 v81, v66
	v_mov_b32_e32 v66, v55
	v_lshlrev_b32_e32 v77, 16, v37
	v_lshlrev_b32_e32 v76, 16, v36
	v_and_b32_e32 v79, 0xffff0000, v37
	v_and_b32_e32 v78, 0xffff0000, v36
	v_mov_b32_e32 v36, v62
	v_mov_b32_e32 v37, v58
	v_pk_mul_f32 v[80:81], v[80:81], v[50:51] op_sel:[0,1] op_sel_hi:[1,0]
	v_mov_b32_e32 v83, v74
	v_mov_b32_e32 v58, v63
	v_pk_mul_f32 v[54:55], v[66:67], v[50:51] op_sel:[0,1] op_sel_hi:[1,0]
	v_mov_b32_e32 v74, v69
	v_pk_fma_f32 v[36:37], v[36:37], v[50:51], v[80:81]
	v_mov_b32_e32 v81, v70
	v_mov_b32_e32 v82, v68
	v_pk_fma_f32 v[54:55], v[58:59], v[50:51], v[54:55]
	v_mov_b32_e32 v70, v73
	v_pk_mul_f32 v[58:59], v[74:75], v[44:45] op_sel:[0,1] op_sel_hi:[1,0]
	v_mov_b32_e32 v80, v72
	v_pk_mul_f32 v[82:83], v[82:83], v[44:45] op_sel:[0,1] op_sel_hi:[1,0]
	v_pk_fma_f32 v[58:59], v[70:71], v[44:45], v[58:59]
	v_pk_fma_f32 v[80:81], v[80:81], v[44:45], v[82:83]
	v_pk_add_f32 v[54:55], v[54:55], v[58:59]
	v_pk_add_f32 v[36:37], v[36:37], v[80:81]
	v_pk_add_f32 v[54:55], v[54:55], v[78:79]
	v_pk_add_f32 v[36:37], v[36:37], v[76:77]
	v_and_b32_sdwa v59, v55, v129 dst_sel:DWORD dst_unused:UNUSED_PAD src0_sel:WORD_1 src1_sel:DWORD
	v_and_b32_sdwa v62, v54, v129 dst_sel:DWORD dst_unused:UNUSED_PAD src0_sel:WORD_1 src1_sel:DWORD
	v_and_b32_sdwa v19, v37, v129 dst_sel:DWORD dst_unused:UNUSED_PAD src0_sel:WORD_1 src1_sel:DWORD
	v_and_b32_sdwa v58, v36, v129 dst_sel:DWORD dst_unused:UNUSED_PAD src0_sel:WORD_1 src1_sel:DWORD
	v_add3_u32 v59, v55, v59, s4
	v_add3_u32 v62, v54, v62, s4
	v_add3_u32 v58, v36, v58, s4
	v_add3_u32 v19, v37, v19, s4
	v_and_b32_e32 v59, 0xffff0000, v59
	v_and_b32_e32 v62, 0xffff0000, v62
	v_or_b32_sdwa v59, v59, v19 dst_sel:DWORD dst_unused:UNUSED_PAD src0_sel:DWORD src1_sel:WORD_1
	v_or_b32_sdwa v58, v62, v58 dst_sel:DWORD dst_unused:UNUSED_PAD src0_sel:DWORD src1_sel:WORD_1
	global_store_dwordx2 v[20:21], v[58:59], off offset:2048
	v_pk_mul_f32 v[58:59], v[54:55], v[54:55]
	s_nop 0
	v_pk_fma_f32 v[66:67], v[36:37], v[36:37], v[58:59]
	v_cvt_pk_f32_fp8_e32 v[58:59], v144
	v_cvt_pk_f32_fp8_sdwa v[70:71], v145 src0_sel:WORD_1
	v_cvt_pk_f32_fp8_sdwa v[62:63], v144 src0_sel:WORD_1
	v_cvt_pk_f32_fp8_e32 v[68:69], v145
	v_cvt_pk_f32_fp8_e32 v[72:73], v146
	s_waitcnt vmcnt(23)
	v_cvt_pk_f32_fp8_sdwa v[78:79], v147 src0_sel:WORD_1
	v_cvt_pk_f32_fp8_sdwa v[74:75], v146 src0_sel:WORD_1
	v_cvt_pk_f32_fp8_e32 v[76:77], v147
	v_mov_b32_e32 v84, v58
	v_mov_b32_e32 v85, v70
	v_mov_b32_e32 v70, v59
	v_lshlrev_b32_e32 v81, 16, v33
	v_lshlrev_b32_e32 v80, 16, v32
	v_and_b32_e32 v83, 0xffff0000, v33
	v_and_b32_e32 v82, 0xffff0000, v32
	v_mov_b32_e32 v32, v68
	v_mov_b32_e32 v33, v62
	v_pk_mul_f32 v[84:85], v[84:85], v[50:51] op_sel:[0,1] op_sel_hi:[1,0]
	v_mov_b32_e32 v89, v78
	v_mov_b32_e32 v62, v69
	v_pk_mul_f32 v[58:59], v[70:71], v[50:51] op_sel:[0,1] op_sel_hi:[1,0]
	v_mov_b32_e32 v78, v73
	v_pk_fma_f32 v[32:33], v[32:33], v[50:51], v[84:85]
	v_mov_b32_e32 v85, v74
	v_mov_b32_e32 v88, v72
	v_pk_fma_f32 v[58:59], v[62:63], v[50:51], v[58:59]
	v_mov_b32_e32 v74, v77
	v_pk_mul_f32 v[62:63], v[78:79], v[44:45] op_sel:[0,1] op_sel_hi:[1,0]
	v_mov_b32_e32 v84, v76
	v_pk_mul_f32 v[88:89], v[88:89], v[44:45] op_sel:[0,1] op_sel_hi:[1,0]
	v_pk_fma_f32 v[62:63], v[74:75], v[44:45], v[62:63]
	v_pk_fma_f32 v[84:85], v[84:85], v[44:45], v[88:89]
	v_pk_add_f32 v[58:59], v[58:59], v[62:63]
	v_pk_add_f32 v[32:33], v[32:33], v[84:85]
	v_pk_add_f32 v[58:59], v[58:59], v[82:83]
	v_pk_add_f32 v[32:33], v[32:33], v[80:81]
	v_and_b32_sdwa v63, v59, v129 dst_sel:DWORD dst_unused:UNUSED_PAD src0_sel:WORD_1 src1_sel:DWORD
	v_and_b32_sdwa v68, v58, v129 dst_sel:DWORD dst_unused:UNUSED_PAD src0_sel:WORD_1 src1_sel:DWORD
	v_and_b32_sdwa v19, v33, v129 dst_sel:DWORD dst_unused:UNUSED_PAD src0_sel:WORD_1 src1_sel:DWORD
	v_and_b32_sdwa v62, v32, v129 dst_sel:DWORD dst_unused:UNUSED_PAD src0_sel:WORD_1 src1_sel:DWORD
	v_add3_u32 v63, v59, v63, s4
	v_add3_u32 v68, v58, v68, s4
	v_add3_u32 v62, v32, v62, s4
	v_add3_u32 v19, v33, v19, s4
	v_and_b32_e32 v63, 0xffff0000, v63
	v_and_b32_e32 v68, 0xffff0000, v68
	v_or_b32_sdwa v63, v63, v19 dst_sel:DWORD dst_unused:UNUSED_PAD src0_sel:DWORD src1_sel:WORD_1
	v_or_b32_sdwa v62, v68, v62 dst_sel:DWORD dst_unused:UNUSED_PAD src0_sel:DWORD src1_sel:WORD_1
	global_store_dwordx2 v[20:21], v[62:63], off offset:2560
	v_pk_mul_f32 v[62:63], v[58:59], v[58:59]
	s_nop 0
	v_pk_fma_f32 v[68:69], v[32:33], v[32:33], v[62:63]
	v_cvt_pk_f32_fp8_e32 v[62:63], v134
	v_cvt_pk_f32_fp8_sdwa v[74:75], v135 src0_sel:WORD_1
	v_cvt_pk_f32_fp8_sdwa v[70:71], v134 src0_sel:WORD_1
	v_cvt_pk_f32_fp8_e32 v[72:73], v135
	v_cvt_pk_f32_fp8_e32 v[76:77], v136
	s_waitcnt vmcnt(23)
	v_cvt_pk_f32_fp8_sdwa v[82:83], v142 src0_sel:WORD_1
	v_cvt_pk_f32_fp8_sdwa v[78:79], v136 src0_sel:WORD_1
	v_cvt_pk_f32_fp8_e32 v[80:81], v142
	v_mov_b32_e32 v134, v62
	v_mov_b32_e32 v135, v74
	v_mov_b32_e32 v74, v63
	v_lshlrev_b32_e32 v85, 16, v31
	v_lshlrev_b32_e32 v84, 16, v30
	v_and_b32_e32 v89, 0xffff0000, v31
	v_and_b32_e32 v88, 0xffff0000, v30
	v_mov_b32_e32 v30, v72
	v_mov_b32_e32 v31, v70
	v_pk_mul_f32 v[134:135], v[134:135], v[50:51] op_sel:[0,1] op_sel_hi:[1,0]
	v_mov_b32_e32 v137, v82
	v_mov_b32_e32 v70, v73
	v_pk_mul_f32 v[62:63], v[74:75], v[50:51] op_sel:[0,1] op_sel_hi:[1,0]
	v_mov_b32_e32 v82, v77
	v_pk_fma_f32 v[30:31], v[30:31], v[50:51], v[134:135]
	v_mov_b32_e32 v135, v78
	v_mov_b32_e32 v136, v76
	v_pk_fma_f32 v[62:63], v[70:71], v[50:51], v[62:63]
	v_mov_b32_e32 v78, v81
	v_pk_mul_f32 v[70:71], v[82:83], v[44:45] op_sel:[0,1] op_sel_hi:[1,0]
	v_mov_b32_e32 v134, v80
	v_pk_mul_f32 v[136:137], v[136:137], v[44:45] op_sel:[0,1] op_sel_hi:[1,0]
	v_pk_fma_f32 v[70:71], v[78:79], v[44:45], v[70:71]
	v_pk_fma_f32 v[134:135], v[134:135], v[44:45], v[136:137]
	v_pk_add_f32 v[62:63], v[62:63], v[70:71]
	v_pk_add_f32 v[30:31], v[30:31], v[134:135]
	v_pk_add_f32 v[62:63], v[62:63], v[88:89]
	v_pk_add_f32 v[30:31], v[30:31], v[84:85]
	v_and_b32_sdwa v71, v63, v129 dst_sel:DWORD dst_unused:UNUSED_PAD src0_sel:WORD_1 src1_sel:DWORD
	v_and_b32_sdwa v72, v62, v129 dst_sel:DWORD dst_unused:UNUSED_PAD src0_sel:WORD_1 src1_sel:DWORD
	v_and_b32_sdwa v19, v31, v129 dst_sel:DWORD dst_unused:UNUSED_PAD src0_sel:WORD_1 src1_sel:DWORD
	v_and_b32_sdwa v70, v30, v129 dst_sel:DWORD dst_unused:UNUSED_PAD src0_sel:WORD_1 src1_sel:DWORD
	v_add3_u32 v71, v63, v71, s4
	v_add3_u32 v72, v62, v72, s4
	v_add3_u32 v70, v30, v70, s4
	v_add3_u32 v19, v31, v19, s4
	v_and_b32_e32 v71, 0xffff0000, v71
	v_and_b32_e32 v72, 0xffff0000, v72
	v_or_b32_sdwa v71, v71, v19 dst_sel:DWORD dst_unused:UNUSED_PAD src0_sel:DWORD src1_sel:WORD_1
	v_or_b32_sdwa v70, v72, v70 dst_sel:DWORD dst_unused:UNUSED_PAD src0_sel:DWORD src1_sel:WORD_1
	global_store_dwordx2 v[20:21], v[70:71], off offset:3072
	v_pk_mul_f32 v[70:71], v[62:63], v[62:63]
	s_nop 0
	v_pk_fma_f32 v[70:71], v[30:31], v[30:31], v[70:71]
	v_cvt_pk_f32_fp8_e32 v[72:73], v86
	v_cvt_pk_f32_fp8_sdwa v[78:79], v87 src0_sel:WORD_1
	v_cvt_pk_f32_fp8_sdwa v[74:75], v86 src0_sel:WORD_1
	v_cvt_pk_f32_fp8_e32 v[76:77], v87
	v_cvt_pk_f32_fp8_e32 v[80:81], v130
	s_waitcnt vmcnt(23)
	v_cvt_pk_f32_fp8_sdwa v[86:87], v132 src0_sel:WORD_1
	v_cvt_pk_f32_fp8_sdwa v[82:83], v130 src0_sel:WORD_1
	v_cvt_pk_f32_fp8_e32 v[84:85], v132
	v_mov_b32_e32 v132, v72
	v_mov_b32_e32 v133, v78
	v_mov_b32_e32 v78, v73
	v_lshlrev_b32_e32 v89, 16, v27
	v_lshlrev_b32_e32 v88, 16, v26
	v_and_b32_e32 v131, 0xffff0000, v27
	v_and_b32_e32 v130, 0xffff0000, v26
	v_mov_b32_e32 v26, v76
	v_mov_b32_e32 v27, v74
	v_pk_mul_f32 v[132:133], v[132:133], v[50:51] op_sel:[0,1] op_sel_hi:[1,0]
	v_mov_b32_e32 v134, v80
	v_mov_b32_e32 v135, v86
	v_mov_b32_e32 v74, v77
	v_pk_mul_f32 v[72:73], v[78:79], v[50:51] op_sel:[0,1] op_sel_hi:[1,0]
	v_mov_b32_e32 v86, v81
	v_pk_fma_f32 v[26:27], v[26:27], v[50:51], v[132:133]
	v_mov_b32_e32 v132, v84
	v_mov_b32_e32 v133, v82
	v_pk_mul_f32 v[134:135], v[134:135], v[44:45] op_sel:[0,1] op_sel_hi:[1,0]
	v_pk_fma_f32 v[50:51], v[74:75], v[50:51], v[72:73]
	v_mov_b32_e32 v82, v85
	v_pk_mul_f32 v[72:73], v[86:87], v[44:45] op_sel:[0,1] op_sel_hi:[1,0]
	v_pk_fma_f32 v[132:133], v[132:133], v[44:45], v[134:135]
	v_pk_fma_f32 v[44:45], v[82:83], v[44:45], v[72:73]
	v_pk_add_f32 v[26:27], v[26:27], v[132:133]
	v_pk_add_f32 v[44:45], v[50:51], v[44:45]
	v_pk_add_f32 v[26:27], v[26:27], v[88:89]
	v_pk_add_f32 v[44:45], v[44:45], v[130:131]
	v_and_b32_sdwa v19, v27, v129 dst_sel:DWORD dst_unused:UNUSED_PAD src0_sel:WORD_1 src1_sel:DWORD
	v_and_b32_sdwa v51, v45, v129 dst_sel:DWORD dst_unused:UNUSED_PAD src0_sel:WORD_1 src1_sel:DWORD
	v_add3_u32 v51, v45, v51, s4
	v_add3_u32 v19, v27, v19, s4
	v_and_b32_e32 v51, 0xffff0000, v51
	v_and_b32_sdwa v72, v44, v129 dst_sel:DWORD dst_unused:UNUSED_PAD src0_sel:WORD_1 src1_sel:DWORD
	v_or_b32_sdwa v51, v51, v19 dst_sel:DWORD dst_unused:UNUSED_PAD src0_sel:DWORD src1_sel:WORD_1
	v_add_f32_e32 v19, v56, v57
	v_add_f32_e32 v48, v48, v49
	v_and_b32_sdwa v50, v26, v129 dst_sel:DWORD dst_unused:UNUSED_PAD src0_sel:WORD_1 src1_sel:DWORD
	v_add3_u32 v72, v44, v72, s4
	v_add_f32_e32 v19, v48, v19
	v_add_f32_e32 v48, v60, v61
	v_add3_u32 v50, v26, v50, s4
	v_and_b32_e32 v72, 0xffff0000, v72
	v_add_f32_e32 v19, v19, v48
	v_add_f32_e32 v48, v64, v65
	v_or_b32_sdwa v50, v72, v50 dst_sel:DWORD dst_unused:UNUSED_PAD src0_sel:DWORD src1_sel:WORD_1
	v_add_f32_e32 v19, v19, v48
	v_add_f32_e32 v48, v66, v67
	global_store_dwordx2 v[20:21], v[50:51], off offset:3584
	v_pk_mul_f32 v[20:21], v[44:45], v[44:45]
	v_add_f32_e32 v19, v19, v48
	v_add_f32_e32 v48, v68, v69
	v_pk_fma_f32 v[20:21], v[26:27], v[26:27], v[20:21]
	v_add_f32_e32 v19, v19, v48
	v_add_f32_e32 v48, v70, v71
	v_add_f32_e32 v19, v19, v48
	v_add_f32_e32 v20, v20, v21
	v_add_f32_e32 v19, v19, v20
	v_mov_b64_e32 v[48:49], v[212:213]
	v_mov_b64_e32 v[50:51], v[214:215]
	ds_bpermute_b32 v20, v1, v19
	s_add_i32 s18, s18, s20
	v_lshl_add_u64 v[14:15], v[14:15], 0, s[22:23]
	v_lshl_add_u64 v[16:17], v[16:17], 0, s[24:25]
	s_cmpk_lt_i32 s18, 0x4000
	s_waitcnt lgkmcnt(0)
	v_add_f32_e32 v19, v19, v20
	ds_bpermute_b32 v20, v90, v19
	v_add_u32_e32 v18, s2, v18
	s_waitcnt lgkmcnt(0)
	v_add_f32_e32 v19, v19, v20
	ds_bpermute_b32 v20, v91, v19
	s_waitcnt lgkmcnt(0)
	v_add_f32_e32 v19, v19, v20
	ds_bpermute_b32 v20, v92, v19
	s_waitcnt lgkmcnt(0)
	v_add_f32_e32 v19, v19, v20
	ds_bpermute_b32 v20, v93, v19
	s_waitcnt lgkmcnt(0)
	v_add_f32_e32 v19, v19, v20
	ds_bpermute_b32 v20, v94, v19
	s_waitcnt lgkmcnt(0)
	v_add_f32_e32 v19, v19, v20
	v_fmamk_f32 v19, v19, 0x3a000000, v127
	v_mul_f32_e32 v20, 0x4f800000, v19
	v_cmp_gt_f32_e32 vcc, s19, v19
	s_nop 1
	v_cndmask_b32_e32 v19, v19, v20, vcc
	v_sqrt_f32_e32 v20, v19
	s_nop 0
	v_add_u32_e32 v21, -1, v20
	v_add_u32_e32 v56, 1, v20
	v_fma_f32 v57, -v21, v20, v19
	v_fma_f32 v60, -v56, v20, v19
	v_cmp_ge_f32_e64 s[8:9], 0, v57
	s_nop 1
	v_cndmask_b32_e64 v20, v20, v21, s[8:9]
	v_cmp_lt_f32_e64 s[8:9], 0, v60
	s_nop 1
	v_cndmask_b32_e64 v20, v20, v56, s[8:9]
	v_mul_f32_e32 v21, 0x37800000, v20
	v_cndmask_b32_e32 v20, v20, v21, vcc
	v_cmp_class_f32_e32 vcc, v19, v128
	v_mov_b32_e32 v56, 0
	s_nop 0
	v_cndmask_b32_e32 v19, v20, v19, vcc
	v_div_scale_f32 v20, s[0:1], v19, v19, 1.0
	v_rcp_f32_e32 v21, v20
	v_div_scale_f32 v57, vcc, 1.0, v19, 1.0
	v_fma_f32 v60, -v20, v21, 1.0
	v_fmac_f32_e32 v21, v60, v21
	v_mul_f32_e32 v60, v57, v21
	v_fma_f32 v61, -v20, v60, v57
	v_fmac_f32_e32 v60, v61, v21
	v_fma_f32 v20, -v20, v60, v57
	v_div_fmas_f32 v20, v20, v21, v60
	v_div_fixup_f32 v19, v20, v19, 1.0
	v_mul_f32_e32 v20, v19, v28
	v_mul_f32_e32 v21, v19, v22

	v_mul_f32_e32 v20, v48, v20
	v_mul_f32_e32 v21, v49, v21
	v_cvt_pk_fp8_f32 v56, v20, v21
	v_mul_f32_e32 v22, v19, v29
	v_mul_f32_e32 v20, v19, v23
	v_mul_f32_e32 v21, v50, v22
	v_mul_f32_e32 v20, v51, v20
	v_cvt_pk_fp8_f32 v56, v21, v20 op_sel:[0,0,1]
	v_mul_f32_e32 v29, v19, v34
	v_mul_f32_e32 v34, v19, v38
	v_mov_b32_e32 v28, 0
	global_store_dword v[24:25], v56, off offset:2048
	v_mov_b64_e32 v[20:21], v[216:217]
	v_mov_b64_e32 v[22:23], v[218:219]
	v_mul_f32_e32 v35, v19, v35
	v_mul_f32_e32 v33, v19, v33
	v_mul_f32_e32 v31, v19, v31
	v_mul_f32_e32 v26, v19, v26
	v_mul_f32_e32 v27, v19, v27

	v_mul_f32_e32 v20, v20, v29
	v_mul_f32_e32 v21, v21, v34
	v_cvt_pk_fp8_f32 v28, v20, v21
	v_mul_f32_e32 v20, v19, v39
	v_mul_f32_e32 v21, v22, v35
	v_mul_f32_e32 v20, v23, v20
	v_cvt_pk_fp8_f32 v28, v21, v20 op_sel:[0,0,1]
	v_mul_f32_e32 v29, v19, v42
	v_mul_f32_e32 v34, v19, v46
	v_mul_f32_e32 v35, v19, v43
	global_store_dword v[24:25], v28, off offset:2304
	v_mov_b64_e32 v[20:21], v[220:221]
	v_mov_b64_e32 v[22:23], v[222:223]
	v_mov_b32_e32 v28, 0

	v_mul_f32_e32 v20, v20, v29
	v_mul_f32_e32 v21, v21, v34
	v_cvt_pk_fp8_f32 v28, v20, v21
	v_mul_f32_e32 v20, v19, v47
	v_mul_f32_e32 v21, v22, v35
	v_mul_f32_e32 v20, v23, v20
	v_cvt_pk_fp8_f32 v28, v21, v20 op_sel:[0,0,1]
	v_mul_f32_e32 v29, v19, v40
	v_mul_f32_e32 v34, v19, v52
	v_mul_f32_e32 v35, v19, v41
	global_store_dword v[24:25], v28, off offset:2560
	v_mov_b64_e32 v[20:21], v[224:225]
	v_mov_b64_e32 v[22:23], v[226:227]
	v_mov_b32_e32 v28, 0

	v_mul_f32_e32 v20, v20, v29
	v_mul_f32_e32 v21, v21, v34
	v_cvt_pk_fp8_f32 v28, v20, v21
	v_mul_f32_e32 v20, v19, v53
	v_mul_f32_e32 v21, v22, v35
	v_mul_f32_e32 v20, v23, v20
	v_cvt_pk_fp8_f32 v28, v21, v20 op_sel:[0,0,1]
	v_mul_f32_e32 v29, v19, v36
	v_mul_f32_e32 v34, v19, v54
	v_mul_f32_e32 v35, v19, v37
	global_store_dword v[24:25], v28, off offset:2816
	v_mov_b64_e32 v[20:21], v[228:229]
	v_mov_b64_e32 v[22:23], v[230:231]
	v_mov_b32_e32 v28, 0

	v_mul_f32_e32 v20, v20, v29
	v_mul_f32_e32 v21, v21, v34
	v_cvt_pk_fp8_f32 v28, v20, v21
	v_mul_f32_e32 v20, v19, v55
	v_mul_f32_e32 v21, v22, v35
	v_mul_f32_e32 v20, v23, v20
	v_cvt_pk_fp8_f32 v28, v21, v20 op_sel:[0,0,1]
	v_mul_f32_e32 v29, v19, v32
	v_mul_f32_e32 v32, v19, v58
	global_store_dword v[24:25], v28, off offset:3072
	v_mov_b64_e32 v[20:21], v[232:233]
	v_mov_b64_e32 v[22:23], v[234:235]
	v_mov_b32_e32 v28, 0

	v_mul_f32_e32 v20, v20, v29
	v_mul_f32_e32 v21, v21, v32
	v_cvt_pk_fp8_f32 v28, v20, v21
	v_mul_f32_e32 v20, v19, v59
	v_mul_f32_e32 v21, v22, v33
	v_mul_f32_e32 v20, v23, v20
	v_cvt_pk_fp8_f32 v28, v21, v20 op_sel:[0,0,1]
	v_mul_f32_e32 v29, v19, v30
	v_mul_f32_e32 v30, v19, v62
	global_store_dword v[24:25], v28, off offset:3328
	v_mov_b64_e32 v[20:21], v[236:237]
	v_mov_b64_e32 v[22:23], v[238:239]
	v_mov_b32_e32 v28, 0

	v_mul_f32_e32 v20, v20, v29
	v_mul_f32_e32 v21, v21, v30
	v_cvt_pk_fp8_f32 v28, v20, v21
	v_mul_f32_e32 v20, v19, v63
	v_mul_f32_e32 v21, v22, v31
	v_mul_f32_e32 v20, v23, v20
	v_cvt_pk_fp8_f32 v28, v21, v20 op_sel:[0,0,1]
	v_mul_f32_e32 v29, v19, v44
	v_mul_f32_e32 v19, v19, v45
	global_store_dword v[24:25], v28, off offset:3584
	v_mov_b64_e32 v[20:21], v[240:241]
	v_mov_b64_e32 v[22:23], v[242:243]
	v_mov_b32_e32 v28, 0

	v_mul_f32_e32 v20, v20, v26
	v_mul_f32_e32 v21, v21, v29
	v_cvt_pk_fp8_f32 v28, v20, v21
	v_mul_f32_e32 v20, v22, v27
	v_mul_f32_e32 v19, v23, v19
	v_cvt_pk_fp8_f32 v28, v20, v19 op_sel:[0,0,1]
	global_store_dword v[24:25], v28, off offset:3840
	s_cbranch_scc0 .LBB0_1431
